# adds: hyconv gate loads hoisted above inverse FFT passes; RG-LRU pass-1 conv loads batched
# speedup vs baseline: 1.0127x; 1.0023x over previous
; #define LAS __attribute__((address_space(3)))
; __device__ __forceinline__ unsigned pk2(float lo, float hi) { const f32x2cv v = {lo, hi}; return __builtin_bit_cast(unsigned, __builtin_convertvector(v, bf16x2cv)); }
; template <int PASS>
; __device__ __forceinline__ void phase_rg(Frame& F0, const Args& A, int l) {
;     ...
;         { const int tok = F.tid >> 3, cg = (F.tid & 7) * 32; const int t = t0 + tok;
; #pragma unroll
;             for (int c8 = 0; c8 < 4; ++c8) { const int ch = cg + c8 * 8; float acc[8];
; #pragma unroll
;                 for (int j = 0; j < 8; ++j) acc[j] = CW[1024 + ch + j];
; #pragma unroll
;                 for (int tap = 0; tap < 4; ++tap) { const int tt = t - 1 + tap;
;                     if (tt >= 0 && tt < L) { const v4u w = *(const v4u*)(P + (size_t)(R0 + tok - 1 + tap) * PROJ + C_RGX + ch); const LAS float* cwp = CW + tap * 256 + ch;
;                         acc[0] += bflo(w.x) * cwp[0]; acc[1] += bfhi(w.x) * cwp[1]; acc[2] += bflo(w.y) * cwp[2]; acc[3] += bfhi(w.y) * cwp[3];
;                         acc[4] += bflo(w.z) * cwp[4]; acc[5] += bfhi(w.z) * cwp[5]; acc[6] += bflo(w.w) * cwp[6]; acc[7] += bfhi(w.w) * cwp[7]; } }
;                 v4u o; o.x = pk2(acc[0], acc[1]); o.y = pk2(acc[2], acc[3]); o.z = pk2(acc[4], acc[5]); o.w = pk2(acc[6], acc[7]);
;                 *(LAS v4u*)(UB + tok * 264 + ch) = o; } }
.LBB0_526:
	s_mul_i32 s0, s5, s70
	v_readlane_b32 s1, v254, 12
	s_add_i32 s8, s0, s1
	s_cmp_lg_u32 s5, 2
	v_readlane_b32 s12, v253, 1
	s_cselect_b64 s[0:1], -1, 0
	v_readlane_b32 s13, v253, 2
	s_or_b64 s[24:25], s[12:13], s[0:1]
	s_and_b64 s[0:1], s[24:25], exec
	v_readlane_b32 s0, v253, 57
	s_cselect_b32 s22, s8, s0
	s_cmpk_gt_i32 s22, 0x21f
	s_cbranch_scc1 .LBB0_525
	s_lshl_b32 s9, s22, 6
	s_waitcnt lgkmcnt(0)
	s_barrier
	s_cmpk_lt_i32 s22, 0x200
	s_movk_i32 s0, 0xfc0
	s_cselect_b32 s0, s0, 0xc0
	s_cselect_b32 s8, s48, 0x100
	s_and_b32 s12, s0, s9
	v_add_u32_e32 v12, s12, v97
	v_add_u32_e32 v8, s9, v97
	v_cmp_gt_u32_e64 s[38:39], s8, v12
	v_add_u32_e32 v10, 1, v12
	v_cmp_gt_u32_e64 s[40:41], s8, v10
	v_add_u32_e32 v10, 2, v12
	v_cmp_gt_u32_e64 s[42:43], s8, v10
	v_add_u32_e32 v10, 3, v12
	v_cmp_gt_u32_e64 s[44:45], s8, v10
	v_ashrrev_i32_e32 v9, 31, v8
	v_lshlrev_b64 v[10:11], 12, v[8:9]
	v_lshl_add_u64 v[10:11], s[46:47], 0, v[10:11]
	v_lshlrev_b32_e32 v180, 1, v92
	v_lshl_add_u64 v[10:11], v[10:11], 0, v[180:181]
	v_add_co_u32_e32 v10, vcc, 0xea00000, v10
	s_nop 1
	v_addc_co_u32_e32 v11, vcc, 0, v11, vcc
	s_mov_b64 s[14:15], 0x1000
	v_lshl_add_u64 v[12:13], v[10:11], 0, s[14:15]
	v_lshl_add_u64 v[14:15], v[12:13], 0, s[14:15]
	v_lshl_add_u64 v[80:81], v[14:15], 0, s[14:15]
	s_mov_b64 s[0:1], exec
	s_and_b64 exec, s[0:1], s[38:39]
	global_load_dwordx4 v[16:19], v[10:11], off offset:3072
	s_and_b64 exec, s[0:1], s[40:41]
	global_load_dwordx4 v[20:23], v[12:13], off offset:3072
	s_and_b64 exec, s[0:1], s[42:43]
	global_load_dwordx4 v[24:27], v[14:15], off offset:3072
	s_and_b64 exec, s[0:1], s[44:45]
	global_load_dwordx4 v[28:31], v[80:81], off offset:3072
	s_and_b64 exec, s[0:1], s[38:39]
	global_load_dwordx4 v[32:35], v[10:11], off offset:3088
	s_and_b64 exec, s[0:1], s[40:41]
	global_load_dwordx4 v[36:39], v[12:13], off offset:3088
	s_and_b64 exec, s[0:1], s[42:43]
	global_load_dwordx4 v[40:43], v[14:15], off offset:3088
	s_and_b64 exec, s[0:1], s[44:45]
	global_load_dwordx4 v[44:47], v[80:81], off offset:3088
	s_and_b64 exec, s[0:1], s[38:39]
	global_load_dwordx4 v[48:51], v[10:11], off offset:3104
	s_and_b64 exec, s[0:1], s[40:41]
	global_load_dwordx4 v[52:55], v[12:13], off offset:3104
	s_and_b64 exec, s[0:1], s[42:43]
	global_load_dwordx4 v[56:59], v[14:15], off offset:3104
	s_and_b64 exec, s[0:1], s[44:45]
	global_load_dwordx4 v[60:63], v[80:81], off offset:3104
	s_and_b64 exec, s[0:1], s[38:39]
	global_load_dwordx4 v[64:67], v[10:11], off offset:3120
	s_and_b64 exec, s[0:1], s[40:41]
	global_load_dwordx4 v[68:71], v[12:13], off offset:3120
	s_and_b64 exec, s[0:1], s[42:43]
	global_load_dwordx4 v[72:75], v[14:15], off offset:3120
	s_and_b64 exec, s[0:1], s[44:45]
	global_load_dwordx4 v[76:79], v[80:81], off offset:3120
	s_mov_b64 exec, s[0:1]
	ds_read_b128 v[4:7], v107 offset:4096
	ds_read_b128 v[0:3], v107 offset:4112
	ds_read_b128 v[116:119], v107
	ds_read_b128 v[120:123], v107 offset:16
	ds_read_b128 v[124:127], v107 offset:1024
	ds_read_b128 v[128:131], v107 offset:1040
	ds_read_b128 v[132:135], v107 offset:2048
	ds_read_b128 v[136:139], v107 offset:2064
	ds_read_b128 v[140:143], v107 offset:3072
	ds_read_b128 v[144:147], v107 offset:3088
	s_waitcnt vmcnt(12)
	s_waitcnt lgkmcnt(0)
	s_and_b64 exec, s[0:1], s[38:39]
	v_lshlrev_b32_e32 v148, 16, v16
	v_and_b32_e32 v149, 0xffff0000, v16
	v_pk_fma_f32 v[4:5], v[116:117], v[148:149], v[4:5]
	v_lshlrev_b32_e32 v148, 16, v17
	v_and_b32_e32 v149, 0xffff0000, v17
	v_pk_fma_f32 v[6:7], v[118:119], v[148:149], v[6:7]
	v_lshlrev_b32_e32 v148, 16, v18
	v_and_b32_e32 v149, 0xffff0000, v18
	v_pk_fma_f32 v[0:1], v[120:121], v[148:149], v[0:1]
	v_lshlrev_b32_e32 v148, 16, v19
	v_and_b32_e32 v149, 0xffff0000, v19
	v_pk_fma_f32 v[2:3], v[122:123], v[148:149], v[2:3]
	s_and_b64 exec, s[0:1], s[40:41]
	v_lshlrev_b32_e32 v148, 16, v20
	v_and_b32_e32 v149, 0xffff0000, v20
	v_pk_fma_f32 v[4:5], v[124:125], v[148:149], v[4:5]
	v_lshlrev_b32_e32 v148, 16, v21
	v_and_b32_e32 v149, 0xffff0000, v21
	v_pk_fma_f32 v[6:7], v[126:127], v[148:149], v[6:7]
	v_lshlrev_b32_e32 v148, 16, v22
	v_and_b32_e32 v149, 0xffff0000, v22
	v_pk_fma_f32 v[0:1], v[128:129], v[148:149], v[0:1]
	v_lshlrev_b32_e32 v148, 16, v23
	v_and_b32_e32 v149, 0xffff0000, v23
	v_pk_fma_f32 v[2:3], v[130:131], v[148:149], v[2:3]
	s_and_b64 exec, s[0:1], s[42:43]
	v_lshlrev_b32_e32 v148, 16, v24
	v_and_b32_e32 v149, 0xffff0000, v24
	v_pk_fma_f32 v[4:5], v[132:133], v[148:149], v[4:5]
	v_lshlrev_b32_e32 v148, 16, v25
	v_and_b32_e32 v149, 0xffff0000, v25
	v_pk_fma_f32 v[6:7], v[134:135], v[148:149], v[6:7]
	v_lshlrev_b32_e32 v148, 16, v26
	v_and_b32_e32 v149, 0xffff0000, v26
	v_pk_fma_f32 v[0:1], v[136:137], v[148:149], v[0:1]
	v_lshlrev_b32_e32 v148, 16, v27
	v_and_b32_e32 v149, 0xffff0000, v27
	v_pk_fma_f32 v[2:3], v[138:139], v[148:149], v[2:3]
	s_and_b64 exec, s[0:1], s[44:45]
	v_lshlrev_b32_e32 v148, 16, v28
	v_and_b32_e32 v149, 0xffff0000, v28
	v_pk_fma_f32 v[4:5], v[140:141], v[148:149], v[4:5]
	v_lshlrev_b32_e32 v148, 16, v29
	v_and_b32_e32 v149, 0xffff0000, v29
	v_pk_fma_f32 v[6:7], v[142:143], v[148:149], v[6:7]
	v_lshlrev_b32_e32 v148, 16, v30
	v_and_b32_e32 v149, 0xffff0000, v30
	v_pk_fma_f32 v[0:1], v[144:145], v[148:149], v[0:1]
	v_lshlrev_b32_e32 v148, 16, v31
	v_and_b32_e32 v149, 0xffff0000, v31
	v_pk_fma_f32 v[2:3], v[146:147], v[148:149], v[2:3]
	s_mov_b64 exec, s[0:1]
	v_cvt_pk_bf16_f32 v4, v4, v5
	v_cvt_pk_bf16_f32 v5, v6, v7
	v_cvt_pk_bf16_f32 v6, v0, v1
	v_cvt_pk_bf16_f32 v7, v2, v3
	ds_write_b128 v108, v[4:7]
	s_mov_b64 exec, s[0:1]
	ds_read_b128 v[4:7], v109 offset:4096
	ds_read_b128 v[0:3], v109 offset:4112
	ds_read_b128 v[116:119], v109
	ds_read_b128 v[120:123], v109 offset:16
	ds_read_b128 v[124:127], v109 offset:1024
	ds_read_b128 v[128:131], v109 offset:1040
	ds_read_b128 v[132:135], v109 offset:2048
	ds_read_b128 v[136:139], v109 offset:2064
	ds_read_b128 v[140:143], v109 offset:3072
	ds_read_b128 v[144:147], v109 offset:3088
	s_waitcnt vmcnt(8)
; #define LAS __attribute__((address_space(3)))
; __device__ __forceinline__ unsigned pk2(float lo, float hi) { const f32x2cv v = {lo, hi}; return __builtin_bit_cast(unsigned, __builtin_convertvector(v, bf16x2cv)); }
; template <int PASS>
; __device__ __forceinline__ void phase_rg(Frame& F0, const Args& A, int l) {
;     ...
;             for (int c8 = 0; c8 < 4; ++c8) { const int ch = cg + c8 * 8; float acc[8];
; #pragma unroll
;                 for (int j = 0; j < 8; ++j) acc[j] = CW[1024 + ch + j];
; #pragma unroll
;                 for (int tap = 0; tap < 4; ++tap) { const int tt = t - 1 + tap;
;                     if (tt >= 0 && tt < L) { const v4u w = *(const v4u*)(P + (size_t)(R0 + tok - 1 + tap) * PROJ + C_RGX + ch); const LAS float* cwp = CW + tap * 256 + ch;
;                         acc[0] += bflo(w.x) * cwp[0]; acc[1] += bfhi(w.x) * cwp[1]; acc[2] += bflo(w.y) * cwp[2]; acc[3] += bfhi(w.y) * cwp[3];
;                         acc[4] += bflo(w.z) * cwp[4]; acc[5] += bfhi(w.z) * cwp[5]; acc[6] += bflo(w.w) * cwp[6]; acc[7] += bfhi(w.w) * cwp[7]; } }
;                 v4u o; o.x = pk2(acc[0], acc[1]); o.y = pk2(acc[2], acc[3]); o.z = pk2(acc[4], acc[5]); o.w = pk2(acc[6], acc[7]);
;                 *(LAS v4u*)(UB + tok * 264 + ch) = o; } }
	s_waitcnt lgkmcnt(0)
	s_and_b64 exec, s[0:1], s[38:39]
	v_lshlrev_b32_e32 v148, 16, v32
	v_and_b32_e32 v149, 0xffff0000, v32
	v_pk_fma_f32 v[4:5], v[116:117], v[148:149], v[4:5]
	v_lshlrev_b32_e32 v148, 16, v33
	v_and_b32_e32 v149, 0xffff0000, v33
	v_pk_fma_f32 v[6:7], v[118:119], v[148:149], v[6:7]
	v_lshlrev_b32_e32 v148, 16, v34
	v_and_b32_e32 v149, 0xffff0000, v34
	v_pk_fma_f32 v[0:1], v[120:121], v[148:149], v[0:1]
	v_lshlrev_b32_e32 v148, 16, v35
	v_and_b32_e32 v149, 0xffff0000, v35
	v_pk_fma_f32 v[2:3], v[122:123], v[148:149], v[2:3]
	s_and_b64 exec, s[0:1], s[40:41]
	v_lshlrev_b32_e32 v148, 16, v36
	v_and_b32_e32 v149, 0xffff0000, v36
	v_pk_fma_f32 v[4:5], v[124:125], v[148:149], v[4:5]
	v_lshlrev_b32_e32 v148, 16, v37
	v_and_b32_e32 v149, 0xffff0000, v37
	v_pk_fma_f32 v[6:7], v[126:127], v[148:149], v[6:7]
	v_lshlrev_b32_e32 v148, 16, v38
	v_and_b32_e32 v149, 0xffff0000, v38
	v_pk_fma_f32 v[0:1], v[128:129], v[148:149], v[0:1]
	v_lshlrev_b32_e32 v148, 16, v39
	v_and_b32_e32 v149, 0xffff0000, v39
	v_pk_fma_f32 v[2:3], v[130:131], v[148:149], v[2:3]
	s_and_b64 exec, s[0:1], s[42:43]
	v_lshlrev_b32_e32 v148, 16, v40
	v_and_b32_e32 v149, 0xffff0000, v40
	v_pk_fma_f32 v[4:5], v[132:133], v[148:149], v[4:5]
	v_lshlrev_b32_e32 v148, 16, v41
	v_and_b32_e32 v149, 0xffff0000, v41
	v_pk_fma_f32 v[6:7], v[134:135], v[148:149], v[6:7]
	v_lshlrev_b32_e32 v148, 16, v42
	v_and_b32_e32 v149, 0xffff0000, v42
	v_pk_fma_f32 v[0:1], v[136:137], v[148:149], v[0:1]
	v_lshlrev_b32_e32 v148, 16, v43
	v_and_b32_e32 v149, 0xffff0000, v43
	v_pk_fma_f32 v[2:3], v[138:139], v[148:149], v[2:3]
	s_and_b64 exec, s[0:1], s[44:45]
	v_lshlrev_b32_e32 v148, 16, v44
	v_and_b32_e32 v149, 0xffff0000, v44
	v_pk_fma_f32 v[4:5], v[140:141], v[148:149], v[4:5]
	v_lshlrev_b32_e32 v148, 16, v45
	v_and_b32_e32 v149, 0xffff0000, v45
	v_pk_fma_f32 v[6:7], v[142:143], v[148:149], v[6:7]
	v_lshlrev_b32_e32 v148, 16, v46
	v_and_b32_e32 v149, 0xffff0000, v46
	v_pk_fma_f32 v[0:1], v[144:145], v[148:149], v[0:1]
	v_lshlrev_b32_e32 v148, 16, v47
	v_and_b32_e32 v149, 0xffff0000, v47
	v_pk_fma_f32 v[2:3], v[146:147], v[148:149], v[2:3]
	s_mov_b64 exec, s[0:1]
	v_cvt_pk_bf16_f32 v4, v4, v5
	v_cvt_pk_bf16_f32 v5, v6, v7
	v_cvt_pk_bf16_f32 v6, v0, v1
	v_cvt_pk_bf16_f32 v7, v2, v3
	ds_write_b128 v108, v[4:7] offset:16
	s_mov_b64 exec, s[0:1]
	ds_read_b128 v[4:7], v110 offset:4096
	ds_read_b128 v[0:3], v110 offset:4112
	ds_read_b128 v[116:119], v110
	ds_read_b128 v[120:123], v110 offset:16
	ds_read_b128 v[124:127], v110 offset:1024
	ds_read_b128 v[128:131], v110 offset:1040
	ds_read_b128 v[132:135], v110 offset:2048
	ds_read_b128 v[136:139], v110 offset:2064
	ds_read_b128 v[140:143], v110 offset:3072
	ds_read_b128 v[144:147], v110 offset:3088
	s_waitcnt vmcnt(4)
	s_waitcnt lgkmcnt(0)
; #define LAS __attribute__((address_space(3)))
; __device__ __forceinline__ unsigned pk2(float lo, float hi) { const f32x2cv v = {lo, hi}; return __builtin_bit_cast(unsigned, __builtin_convertvector(v, bf16x2cv)); }
; template <int PASS>
; __device__ __forceinline__ void phase_rg(Frame& F0, const Args& A, int l) {
;     ...
;             for (int c8 = 0; c8 < 4; ++c8) { const int ch = cg + c8 * 8; float acc[8];
; #pragma unroll
;                 for (int j = 0; j < 8; ++j) acc[j] = CW[1024 + ch + j];
; #pragma unroll
;                 for (int tap = 0; tap < 4; ++tap) { const int tt = t - 1 + tap;
;                     if (tt >= 0 && tt < L) { const v4u w = *(const v4u*)(P + (size_t)(R0 + tok - 1 + tap) * PROJ + C_RGX + ch); const LAS float* cwp = CW + tap * 256 + ch;
;                         acc[0] += bflo(w.x) * cwp[0]; acc[1] += bfhi(w.x) * cwp[1]; acc[2] += bflo(w.y) * cwp[2]; acc[3] += bfhi(w.y) * cwp[3];
;                         acc[4] += bflo(w.z) * cwp[4]; acc[5] += bfhi(w.z) * cwp[5]; acc[6] += bflo(w.w) * cwp[6]; acc[7] += bfhi(w.w) * cwp[7]; } }
;                 v4u o; o.x = pk2(acc[0], acc[1]); o.y = pk2(acc[2], acc[3]); o.z = pk2(acc[4], acc[5]); o.w = pk2(acc[6], acc[7]);
;                 *(LAS v4u*)(UB + tok * 264 + ch) = o; } }
	s_and_b64 exec, s[0:1], s[38:39]
	v_lshlrev_b32_e32 v148, 16, v48
	v_and_b32_e32 v149, 0xffff0000, v48
	v_pk_fma_f32 v[4:5], v[116:117], v[148:149], v[4:5]
	v_lshlrev_b32_e32 v148, 16, v49
	v_and_b32_e32 v149, 0xffff0000, v49
	v_pk_fma_f32 v[6:7], v[118:119], v[148:149], v[6:7]
	v_lshlrev_b32_e32 v148, 16, v50
	v_and_b32_e32 v149, 0xffff0000, v50
	v_pk_fma_f32 v[0:1], v[120:121], v[148:149], v[0:1]
	v_lshlrev_b32_e32 v148, 16, v51
	v_and_b32_e32 v149, 0xffff0000, v51
	v_pk_fma_f32 v[2:3], v[122:123], v[148:149], v[2:3]
	s_and_b64 exec, s[0:1], s[40:41]
	v_lshlrev_b32_e32 v148, 16, v52
	v_and_b32_e32 v149, 0xffff0000, v52
	v_pk_fma_f32 v[4:5], v[124:125], v[148:149], v[4:5]
	v_lshlrev_b32_e32 v148, 16, v53
	v_and_b32_e32 v149, 0xffff0000, v53
	v_pk_fma_f32 v[6:7], v[126:127], v[148:149], v[6:7]
	v_lshlrev_b32_e32 v148, 16, v54
	v_and_b32_e32 v149, 0xffff0000, v54
	v_pk_fma_f32 v[0:1], v[128:129], v[148:149], v[0:1]
	v_lshlrev_b32_e32 v148, 16, v55
	v_and_b32_e32 v149, 0xffff0000, v55
	v_pk_fma_f32 v[2:3], v[130:131], v[148:149], v[2:3]
	s_and_b64 exec, s[0:1], s[42:43]
	v_lshlrev_b32_e32 v148, 16, v56
	v_and_b32_e32 v149, 0xffff0000, v56
	v_pk_fma_f32 v[4:5], v[132:133], v[148:149], v[4:5]
	v_lshlrev_b32_e32 v148, 16, v57
	v_and_b32_e32 v149, 0xffff0000, v57
	v_pk_fma_f32 v[6:7], v[134:135], v[148:149], v[6:7]
	v_lshlrev_b32_e32 v148, 16, v58
	v_and_b32_e32 v149, 0xffff0000, v58
	v_pk_fma_f32 v[0:1], v[136:137], v[148:149], v[0:1]
	v_lshlrev_b32_e32 v148, 16, v59
	v_and_b32_e32 v149, 0xffff0000, v59
	v_pk_fma_f32 v[2:3], v[138:139], v[148:149], v[2:3]
	s_and_b64 exec, s[0:1], s[44:45]
	v_lshlrev_b32_e32 v148, 16, v60
	v_and_b32_e32 v149, 0xffff0000, v60
	v_pk_fma_f32 v[4:5], v[140:141], v[148:149], v[4:5]
	v_lshlrev_b32_e32 v148, 16, v61
	v_and_b32_e32 v149, 0xffff0000, v61
	v_pk_fma_f32 v[6:7], v[142:143], v[148:149], v[6:7]
	v_lshlrev_b32_e32 v148, 16, v62
	v_and_b32_e32 v149, 0xffff0000, v62
	v_pk_fma_f32 v[0:1], v[144:145], v[148:149], v[0:1]
	v_lshlrev_b32_e32 v148, 16, v63
	v_and_b32_e32 v149, 0xffff0000, v63
	v_pk_fma_f32 v[2:3], v[146:147], v[148:149], v[2:3]
	s_mov_b64 exec, s[0:1]
	v_cvt_pk_bf16_f32 v4, v4, v5
	v_cvt_pk_bf16_f32 v5, v6, v7
	v_cvt_pk_bf16_f32 v6, v0, v1
	v_cvt_pk_bf16_f32 v7, v2, v3
	ds_write_b128 v108, v[4:7] offset:32
	s_mov_b64 exec, s[0:1]
	ds_read_b128 v[4:7], v111 offset:4096
	ds_read_b128 v[0:3], v111 offset:4112
	ds_read_b128 v[116:119], v111
	ds_read_b128 v[120:123], v111 offset:16
	ds_read_b128 v[124:127], v111 offset:1024
	ds_read_b128 v[128:131], v111 offset:1040
	ds_read_b128 v[132:135], v111 offset:2048
	ds_read_b128 v[136:139], v111 offset:2064
	ds_read_b128 v[140:143], v111 offset:3072
	ds_read_b128 v[144:147], v111 offset:3088
	s_waitcnt vmcnt(0)
	s_waitcnt lgkmcnt(0)
	s_and_b64 exec, s[0:1], s[38:39]
	v_lshlrev_b32_e32 v148, 16, v64
	v_and_b32_e32 v149, 0xffff0000, v64
	v_pk_fma_f32 v[4:5], v[116:117], v[148:149], v[4:5]
	v_lshlrev_b32_e32 v148, 16, v65
	v_and_b32_e32 v149, 0xffff0000, v65
	v_pk_fma_f32 v[6:7], v[118:119], v[148:149], v[6:7]
	v_lshlrev_b32_e32 v148, 16, v66
	v_and_b32_e32 v149, 0xffff0000, v66
	v_pk_fma_f32 v[0:1], v[120:121], v[148:149], v[0:1]
	v_lshlrev_b32_e32 v148, 16, v67
	v_and_b32_e32 v149, 0xffff0000, v67
	v_pk_fma_f32 v[2:3], v[122:123], v[148:149], v[2:3]
	s_and_b64 exec, s[0:1], s[40:41]
	v_lshlrev_b32_e32 v148, 16, v68
	v_and_b32_e32 v149, 0xffff0000, v68
	v_pk_fma_f32 v[4:5], v[124:125], v[148:149], v[4:5]
	v_lshlrev_b32_e32 v148, 16, v69
	v_and_b32_e32 v149, 0xffff0000, v69
	v_pk_fma_f32 v[6:7], v[126:127], v[148:149], v[6:7]
	v_lshlrev_b32_e32 v148, 16, v70
	v_and_b32_e32 v149, 0xffff0000, v70
	v_pk_fma_f32 v[0:1], v[128:129], v[148:149], v[0:1]
	v_lshlrev_b32_e32 v148, 16, v71
	v_and_b32_e32 v149, 0xffff0000, v71
	v_pk_fma_f32 v[2:3], v[130:131], v[148:149], v[2:3]
	s_and_b64 exec, s[0:1], s[42:43]
	v_lshlrev_b32_e32 v148, 16, v72
	v_and_b32_e32 v149, 0xffff0000, v72
	v_pk_fma_f32 v[4:5], v[132:133], v[148:149], v[4:5]
	v_lshlrev_b32_e32 v148, 16, v73
	v_and_b32_e32 v149, 0xffff0000, v73
	v_pk_fma_f32 v[6:7], v[134:135], v[148:149], v[6:7]
	v_lshlrev_b32_e32 v148, 16, v74
	v_and_b32_e32 v149, 0xffff0000, v74
	v_pk_fma_f32 v[0:1], v[136:137], v[148:149], v[0:1]
	v_lshlrev_b32_e32 v148, 16, v75
	v_and_b32_e32 v149, 0xffff0000, v75
	v_pk_fma_f32 v[2:3], v[138:139], v[148:149], v[2:3]
	s_and_b64 exec, s[0:1], s[44:45]
	v_lshlrev_b32_e32 v148, 16, v76
	v_and_b32_e32 v149, 0xffff0000, v76
	v_pk_fma_f32 v[4:5], v[140:141], v[148:149], v[4:5]
	v_lshlrev_b32_e32 v148, 16, v77
	v_and_b32_e32 v149, 0xffff0000, v77
	v_pk_fma_f32 v[6:7], v[142:143], v[148:149], v[6:7]
	v_lshlrev_b32_e32 v148, 16, v78
	v_and_b32_e32 v149, 0xffff0000, v78
	v_pk_fma_f32 v[0:1], v[144:145], v[148:149], v[0:1]
	v_lshlrev_b32_e32 v148, 16, v79
	v_and_b32_e32 v149, 0xffff0000, v79
	v_pk_fma_f32 v[2:3], v[146:147], v[148:149], v[2:3]

; #define LAS __attribute__((address_space(3)))
; __device__ __forceinline__ float fsigmoid(float x) { return __builtin_amdgcn_rcpf(1.0f + __expf(-x)); }
; template <int PASS, bool REV> ...
;     ...
;         for (int kk = 0; kk < 2; ++kk) { const bf16x8 wa = wcur[0][kk], wx = wcur[1][kk]; bf16x8 uf[4][2];
; #pragma unroll
;             for (int tg = 0; tg < 4; ++tg) uf[tg][kk] = *(const LAS bf16x8*)(UB + (tg * 16 + fr) * 264 + blk * 64 + kk * 32 + fq * 8);
; #pragma unroll
;             for (int tg = 0; tg < 4; ++tg) { aa[tg] = __builtin_amdgcn_mfma_f32_16x16x32_bf16(wa, uf[tg][kk], aa[tg], 0, 0, 0); ax[tg] = __builtin_amdgcn_mfma_f32_16x16x32_bf16(wx, uf[tg][kk], ax[tg], 0, 0, 0); } }
;         { const int ng1 = (ng + 1 < ng_hi) ? ng + 1 : ng_lo;
; #pragma unroll
;             for (int gt = 0; gt < 2; ++gt)
; #pragma unroll
;                 for (int kk = 0; kk < 2; ++kk) wcur[gt][kk] = *(const bf16x8*)(Wg + ((size_t)(gt * 4 + blk) * 64 + ng1 * 16 + fr) * 64 + kk * 32 + fq * 8); }
;         if (PASS == 2 && REV && emit) {
; #pragma unroll
;             for (int tg = 0; tg < 4; ++tg) gwv[tg] = *(const v2u*)(P + (size_t)(R0 + tg * 16 + fr) * PROJ + C_RGG + blk * 64 + ng * 16 + fq * 4); }
;         const int ch = blk * 64 + ng * 16 + fq * 4; const f32x4 sp = *(const LAS f32x4*)(cst + ch), bav = *(const LAS f32x4*)(cst + 256 + ch), bxv = *(const LAS f32x4*)(cst + 512 + ch);
; #pragma unroll
;         for (int tg = 0; tg < 4; ++tg) { const v2u uw = *(const LAS v2u*)(UB + (tg * 16 + fr) * 264 + ch); const float uv[4] = {bflo(uw.x), bfhi(uw.x), bflo(uw.y), bfhi(uw.y)};
; #pragma unroll
;             for (int j = 0; j < 4; ++j) { const float r = fsigmoid(aa[tg][j] + bav[j]), ig = fsigmoid(ax[tg][j] + bxv[j]); const float la = -8.0f * r * sp[j];
;                 float Av = __expf(la); const float om = __builtin_fmaf(-Av, Av, 1.0f);
;                 float Bv = __builtin_amdgcn_sqrtf(om) * (ig * uv[j]);
;                 rg_scan_step<REV, 1>(Av, Bv); rg_scan_step<REV, 2>(Av, Bv); rg_scan_step<REV, 4>(Av, Bv); rg_scan_step<REV, 8>(Av, Bv);
;                 aa[tg][j] = Av; ax[tg][j] = Bv; } }
.LBB0_553:
	s_add_i32 s0, s9, s13
	s_waitcnt vmcnt(0) lgkmcnt(7)
	v_mfma_f32_16x16x32_bf16 v[48:51], v[40:43], v[0:3], 0
	s_add_i32 s0, s0, 1
	s_cmp_lt_u32 s0, s8
	s_cselect_b32 s0, s0, s9
	v_mfma_f32_16x16x32_bf16 v[52:55], v[44:47], v[0:3], 0
	v_lshl_add_u32 v180, s0, 4, v99
	v_add_u32_e32 v118, 0, v116
	s_waitcnt lgkmcnt(5)
	v_mfma_f32_16x16x32_bf16 v[56:59], v[40:43], v[8:11], 0
	s_waitcnt lgkmcnt(3)
	v_mfma_f32_16x16x32_bf16 v[64:67], v[40:43], v[16:19], 0
	s_waitcnt lgkmcnt(1)
	v_mfma_f32_16x16x32_bf16 v[40:43], v[40:43], v[24:27], 0
	v_mfma_f32_16x16x32_bf16 v[60:63], v[44:47], v[8:11], 0
	v_mfma_f32_16x16x32_bf16 v[68:71], v[44:47], v[16:19], 0
	v_mfma_f32_16x16x32_bf16 v[44:47], v[44:47], v[24:27], 0
	v_mfma_f32_16x16x32_bf16 v[88:91], v[32:35], v[4:7], v[48:51]
	v_mfma_f32_16x16x32_bf16 v[84:87], v[36:39], v[4:7], v[52:55]
	v_mfma_f32_16x16x32_bf16 v[80:83], v[32:35], v[12:15], v[56:59]
	v_mfma_f32_16x16x32_bf16 v[72:75], v[32:35], v[20:23], v[64:67]
	s_waitcnt lgkmcnt(0)
	v_mfma_f32_16x16x32_bf16 v[52:55], v[32:35], v[28:31], v[40:43]
	v_lshlrev_b64 v[32:33], 7, v[180:181]
	v_add_u32_e32 v180, 0x100, v180
	v_lshl_add_u64 v[32:33], v[94:95], 0, v[32:33]
	v_mfma_f32_16x16x32_bf16 v[76:79], v[36:39], v[12:15], v[60:63]
	global_load_dwordx4 v[40:43], v[32:33], off
	s_nop 0
	global_load_dwordx4 v[32:35], v[32:33], off offset:64
	v_add_u32_e32 v60, 0, v117
	v_add_u32_e32 v61, 0x12000, v60
	v_mfma_f32_16x16x32_bf16 v[68:71], v[36:39], v[20:23], v[68:71]
	v_add_u32_e32 v56, 0x11c00, v60
	v_add_u32_e32 v60, 0x12400, v60
	v_mfma_f32_16x16x32_bf16 v[48:51], v[36:39], v[28:31], v[44:47]
	v_lshlrev_b64 v[36:37], 7, v[180:181]
	v_lshl_add_u64 v[36:37], v[94:95], 0, v[36:37]
	s_nop 0
	global_load_dwordx4 v[44:47], v[36:37], off
	s_nop 0
	global_load_dwordx4 v[36:39], v[36:37], off offset:64
	ds_read_b128 v[64:67], v61
	ds_read_b64 v[120:121], v118
	ds_read_b128 v[56:59], v56
	ds_read_b128 v[60:63], v60
	s_waitcnt lgkmcnt(3)
	v_add_f32_e32 v88, v88, v64
	v_mul_f32_e32 v88, 0xbfb8aa3b, v88
	v_exp_f32_e32 v88, v88
	s_waitcnt lgkmcnt(0)
	v_add_f32_e32 v84, v84, v60
	v_mul_f32_e32 v84, 0xbfb8aa3b, v84
	v_exp_f32_e32 v84, v84
	v_add_f32_e32 v88, 1.0, v88
	v_rcp_f32_e32 v88, v88
	v_add_f32_e32 v89, v89, v65
	v_mul_f32_e32 v89, 0xbfb8aa3b, v89
	v_exp_f32_e32 v89, v89
	v_mul_f32_e32 v88, 0xc1000000, v88
	v_mul_f32_e32 v88, v56, v88
	v_mul_f32_e32 v88, 0x3fb8aa3b, v88
	v_exp_f32_e32 v88, v88
	v_add_f32_e32 v84, 1.0, v84
	v_rcp_f32_e32 v84, v84
	v_add_f32_e32 v89, 1.0, v89
	v_fma_f32 v123, -v88, v88, 1.0
	v_sqrt_f32_e32 v123, v123
	v_rcp_f32_e32 v89, v89
	v_lshlrev_b32_e32 v119, 16, v120
	v_mul_f32_e32 v84, v84, v119
	v_mul_f32_e32 v84, v84, v123
	v_mov_b32_e32 v119, 1.0
	v_mov_b32_e32 v123, v181
	v_add_f32_e32 v85, v85, v61
	v_mov_b32_dpp v119, v88 row_shl:1 row_mask:0xf bank_mask:0xf
	v_mov_b32_dpp v123, v84 row_shl:1 row_mask:0xf bank_mask:0xf
	v_mul_f32_e32 v89, 0xc1000000, v89
	v_fmac_f32_e32 v84, v88, v123
	v_mul_f32_e32 v88, v88, v119
	v_mov_b32_e32 v119, 1.0
	v_mov_b32_e32 v123, v181
	v_mul_f32_e32 v85, 0xbfb8aa3b, v85
	v_mul_f32_e32 v89, v57, v89
	v_mov_b32_dpp v119, v88 row_shl:2 row_mask:0xf bank_mask:0xf
	v_mov_b32_dpp v123, v84 row_shl:2 row_mask:0xf bank_mask:0xf
	v_exp_f32_e32 v85, v85
	v_mul_f32_e32 v89, 0x3fb8aa3b, v89
	v_add_f32_e32 v90, v90, v66
	v_fmac_f32_e32 v84, v88, v123
	v_mul_f32_e32 v88, v88, v119
	v_mov_b32_e32 v119, 1.0
	v_mov_b32_e32 v123, v181
	v_exp_f32_e32 v89, v89
	v_mul_f32_e32 v90, 0xbfb8aa3b, v90
	v_mov_b32_dpp v119, v88 row_shl:4 row_mask:0xf bank_mask:0xf
	v_mov_b32_dpp v123, v84 row_shl:4 row_mask:0xf bank_mask:0xf
	v_exp_f32_e32 v90, v90
	v_fmac_f32_e32 v84, v88, v123
	v_mul_f32_e32 v88, v88, v119
	v_mov_b32_e32 v119, 1.0
	v_mov_b32_e32 v123, v181
	v_add_f32_e32 v85, 1.0, v85
	v_mov_b32_dpp v119, v88 row_shl:8 row_mask:0xf bank_mask:0xf
	v_mov_b32_dpp v123, v84 row_shl:8 row_mask:0xf bank_mask:0xf
	v_fmac_f32_e32 v84, v88, v123
	v_mul_f32_e32 v88, v88, v119
	v_rcp_f32_e32 v85, v85
	v_fma_f32 v119, -v89, v89, 1.0
	v_sqrt_f32_e32 v119, v119
	v_add_f32_e32 v90, 1.0, v90
	v_rcp_f32_e32 v90, v90
	v_and_b32_e32 v120, 0xffff0000, v120
	v_mul_f32_e32 v85, v85, v120
	v_mul_f32_e32 v85, v85, v119
	v_mov_b32_e32 v119, 1.0
	v_mov_b32_e32 v120, v181
	v_add_f32_e32 v86, v86, v62
	v_mov_b32_dpp v119, v89 row_shl:1 row_mask:0xf bank_mask:0xf
	v_mov_b32_dpp v120, v85 row_shl:1 row_mask:0xf bank_mask:0xf
	v_mul_f32_e32 v90, 0xc1000000, v90
	v_fmac_f32_e32 v85, v89, v120
	v_mul_f32_e32 v89, v89, v119
	v_mov_b32_e32 v119, 1.0
	v_mov_b32_e32 v120, v181
	v_mul_f32_e32 v86, 0xbfb8aa3b, v86
	v_mul_f32_e32 v90, v58, v90
	v_mov_b32_dpp v119, v89 row_shl:2 row_mask:0xf bank_mask:0xf
	v_mov_b32_dpp v120, v85 row_shl:2 row_mask:0xf bank_mask:0xf
	v_exp_f32_e32 v86, v86
	v_mul_f32_e32 v90, 0x3fb8aa3b, v90
	v_add_f32_e32 v91, v91, v67
	v_fmac_f32_e32 v85, v89, v120
	v_mul_f32_e32 v89, v89, v119
	v_mov_b32_e32 v119, 1.0
	v_mov_b32_e32 v120, v181
	v_exp_f32_e32 v90, v90
	v_mul_f32_e32 v91, 0xbfb8aa3b, v91
	v_mov_b32_dpp v119, v89 row_shl:4 row_mask:0xf bank_mask:0xf
	v_mov_b32_dpp v120, v85 row_shl:4 row_mask:0xf bank_mask:0xf
	v_exp_f32_e32 v91, v91
	v_fmac_f32_e32 v85, v89, v120
	v_mul_f32_e32 v89, v89, v119
	v_mov_b32_e32 v119, 1.0
	v_mov_b32_e32 v120, v181
	v_add_f32_e32 v86, 1.0, v86
	v_mov_b32_dpp v119, v89 row_shl:8 row_mask:0xf bank_mask:0xf
	v_mov_b32_dpp v120, v85 row_shl:8 row_mask:0xf bank_mask:0xf
	v_fmac_f32_e32 v85, v89, v120
	v_mul_f32_e32 v89, v89, v119
	v_rcp_f32_e32 v86, v86
	v_fma_f32 v119, -v90, v90, 1.0
	v_sqrt_f32_e32 v119, v119
	v_add_f32_e32 v91, 1.0, v91
	v_rcp_f32_e32 v91, v91
	v_lshlrev_b32_e32 v122, 16, v121
; #define LAS __attribute__((address_space(3)))
; __device__ __forceinline__ float fsigmoid(float x) { return __builtin_amdgcn_rcpf(1.0f + __expf(-x)); }
; template <int PASS, bool REV> ...
;     ...
;         const int ch = blk * 64 + ng * 16 + fq * 4; const f32x4 sp = *(const LAS f32x4*)(cst + ch), bav = *(const LAS f32x4*)(cst + 256 + ch), bxv = *(const LAS f32x4*)(cst + 512 + ch);
; #pragma unroll
;         for (int tg = 0; tg < 4; ++tg) { const v2u uw = *(const LAS v2u*)(UB + (tg * 16 + fr) * 264 + ch); const float uv[4] = {bflo(uw.x), bfhi(uw.x), bflo(uw.y), bfhi(uw.y)};
; #pragma unroll
;             for (int j = 0; j < 4; ++j) { const float r = fsigmoid(aa[tg][j] + bav[j]), ig = fsigmoid(ax[tg][j] + bxv[j]); const float la = -8.0f * r * sp[j];
;                 float Av = __expf(la); const float om = __builtin_fmaf(-Av, Av, 1.0f);
;                 float Bv = __builtin_amdgcn_sqrtf(om) * (ig * uv[j]);
;                 rg_scan_step<REV, 1>(Av, Bv); rg_scan_step<REV, 2>(Av, Bv); rg_scan_step<REV, 4>(Av, Bv); rg_scan_step<REV, 8>(Av, Bv);
;                 aa[tg][j] = Av; ax[tg][j] = Bv; } }
	v_mul_f32_e32 v86, v86, v122
	v_mul_f32_e32 v86, v86, v119
	v_mov_b32_e32 v119, 1.0
	v_mov_b32_e32 v120, v181
	v_add_f32_e32 v87, v87, v63
	v_mov_b32_dpp v119, v90 row_shl:1 row_mask:0xf bank_mask:0xf
	v_mov_b32_dpp v120, v86 row_shl:1 row_mask:0xf bank_mask:0xf
	v_mul_f32_e32 v91, 0xc1000000, v91
	v_fmac_f32_e32 v86, v90, v120
	v_mul_f32_e32 v90, v90, v119
	v_mov_b32_e32 v119, 1.0
	v_mov_b32_e32 v120, v181
	v_mul_f32_e32 v87, 0xbfb8aa3b, v87
	v_mul_f32_e32 v91, v59, v91
	v_mov_b32_dpp v119, v90 row_shl:2 row_mask:0xf bank_mask:0xf
	v_mov_b32_dpp v120, v86 row_shl:2 row_mask:0xf bank_mask:0xf
	v_exp_f32_e32 v87, v87
	v_mul_f32_e32 v91, 0x3fb8aa3b, v91
	v_fmac_f32_e32 v86, v90, v120
	v_mul_f32_e32 v90, v90, v119
	v_mov_b32_e32 v119, 1.0
	v_mov_b32_e32 v120, v181
	v_exp_f32_e32 v91, v91
	v_mov_b32_dpp v119, v90 row_shl:4 row_mask:0xf bank_mask:0xf
	v_mov_b32_dpp v120, v86 row_shl:4 row_mask:0xf bank_mask:0xf
	v_add_f32_e32 v80, v80, v64
	v_fmac_f32_e32 v86, v90, v120
	v_mul_f32_e32 v90, v90, v119
	v_mov_b32_e32 v119, 1.0
	v_mov_b32_e32 v120, v181
	v_mul_f32_e32 v80, 0xbfb8aa3b, v80
	v_mov_b32_dpp v119, v90 row_shl:8 row_mask:0xf bank_mask:0xf
	v_mov_b32_dpp v120, v86 row_shl:8 row_mask:0xf bank_mask:0xf
	v_add_f32_e32 v87, 1.0, v87
	v_exp_f32_e32 v80, v80
	v_fmac_f32_e32 v86, v90, v120
	v_mul_f32_e32 v90, v90, v119
	v_rcp_f32_e32 v87, v87
	v_fma_f32 v119, -v91, v91, 1.0
	v_sqrt_f32_e32 v119, v119
	v_and_b32_e32 v121, 0xffff0000, v121
	v_add_f32_e32 v80, 1.0, v80
	v_mul_f32_e32 v87, v87, v121
	v_rcp_f32_e32 v80, v80
	v_mul_f32_e32 v87, v87, v119
	v_mov_b32_e32 v120, v181
	v_mov_b32_e32 v119, 1.0
	v_add_f32_e32 v76, v76, v60
	v_mov_b32_dpp v120, v87 row_shl:1 row_mask:0xf bank_mask:0xf
	v_mov_b32_dpp v119, v91 row_shl:1 row_mask:0xf bank_mask:0xf
	v_fmac_f32_e32 v87, v91, v120
	v_mov_b32_e32 v120, v181
	v_mul_f32_e32 v91, v91, v119
	v_mov_b32_e32 v119, 1.0
	v_mov_b32_dpp v120, v87 row_shl:2 row_mask:0xf bank_mask:0xf
	v_mul_f32_e32 v80, 0xc1000000, v80
	v_mov_b32_dpp v119, v91 row_shl:2 row_mask:0xf bank_mask:0xf
	v_fmac_f32_e32 v87, v91, v120
	v_mov_b32_e32 v120, v181
	v_mul_f32_e32 v76, 0xbfb8aa3b, v76
	v_mul_f32_e32 v80, v56, v80
	v_mul_f32_e32 v91, v91, v119
	v_mov_b32_e32 v119, 1.0
	v_mov_b32_dpp v120, v87 row_shl:4 row_mask:0xf bank_mask:0xf
	v_exp_f32_e32 v76, v76
	v_mul_f32_e32 v80, 0x3fb8aa3b, v80
	v_add_f32_e32 v81, v81, v65
	v_mov_b32_dpp v119, v91 row_shl:4 row_mask:0xf bank_mask:0xf
	v_fmac_f32_e32 v87, v91, v120
	v_mov_b32_e32 v120, v181
	v_exp_f32_e32 v80, v80
	v_mul_f32_e32 v81, 0xbfb8aa3b, v81
	v_mul_f32_e32 v91, v91, v119
	v_mov_b32_dpp v120, v87 row_shl:8 row_mask:0xf bank_mask:0xf
	v_exp_f32_e32 v81, v81
	v_fmac_f32_e32 v87, v91, v120
	ds_read_b64 v[120:121], v118 offset:8448
	v_add_f32_e32 v76, 1.0, v76
	v_rcp_f32_e32 v76, v76
	v_fma_f32 v123, -v80, v80, 1.0
	v_mov_b32_e32 v119, 1.0
	v_sqrt_f32_e32 v123, v123
	v_add_f32_e32 v81, 1.0, v81
	v_mov_b32_dpp v119, v91 row_shl:8 row_mask:0xf bank_mask:0xf
	v_rcp_f32_e32 v81, v81
	v_mul_f32_e32 v91, v91, v119
	s_waitcnt lgkmcnt(0)
	v_lshlrev_b32_e32 v119, 16, v120
	v_mul_f32_e32 v76, v76, v119
	v_mul_f32_e32 v76, v123, v76
	v_mov_b32_e32 v119, 1.0
	v_mov_b32_e32 v123, v181
	v_add_f32_e32 v77, v77, v61
	v_mov_b32_dpp v119, v80 row_shl:1 row_mask:0xf bank_mask:0xf
	v_mov_b32_dpp v123, v76 row_shl:1 row_mask:0xf bank_mask:0xf
	v_mul_f32_e32 v81, 0xc1000000, v81
	v_fmac_f32_e32 v76, v80, v123
	v_mul_f32_e32 v80, v80, v119
	v_mov_b32_e32 v119, 1.0
	v_mov_b32_e32 v123, v181
	v_mul_f32_e32 v77, 0xbfb8aa3b, v77
	v_mul_f32_e32 v81, v57, v81
	v_mov_b32_dpp v119, v80 row_shl:2 row_mask:0xf bank_mask:0xf
	v_mov_b32_dpp v123, v76 row_shl:2 row_mask:0xf bank_mask:0xf
	v_exp_f32_e32 v77, v77
	v_mul_f32_e32 v81, 0x3fb8aa3b, v81
	v_add_f32_e32 v82, v82, v66
	v_fmac_f32_e32 v76, v80, v123
	v_mul_f32_e32 v80, v80, v119
	v_mov_b32_e32 v119, 1.0
	v_mov_b32_e32 v123, v181
	v_exp_f32_e32 v81, v81
	v_mul_f32_e32 v82, 0xbfb8aa3b, v82
	v_mov_b32_dpp v119, v80 row_shl:4 row_mask:0xf bank_mask:0xf
	v_mov_b32_dpp v123, v76 row_shl:4 row_mask:0xf bank_mask:0xf
	v_exp_f32_e32 v82, v82
	v_fmac_f32_e32 v76, v80, v123
	v_mul_f32_e32 v80, v80, v119
	v_mov_b32_e32 v119, 1.0
	v_mov_b32_e32 v123, v181
	v_add_f32_e32 v77, 1.0, v77
	v_mov_b32_dpp v119, v80 row_shl:8 row_mask:0xf bank_mask:0xf
	v_mov_b32_dpp v123, v76 row_shl:8 row_mask:0xf bank_mask:0xf
	v_fmac_f32_e32 v76, v80, v123
	v_mul_f32_e32 v80, v80, v119
	v_rcp_f32_e32 v77, v77
	v_fma_f32 v119, -v81, v81, 1.0
	v_sqrt_f32_e32 v119, v119
	v_add_f32_e32 v82, 1.0, v82
	v_rcp_f32_e32 v82, v82
	v_and_b32_e32 v120, 0xffff0000, v120
	v_mul_f32_e32 v77, v77, v120
	v_mul_f32_e32 v77, v119, v77
	v_mov_b32_e32 v119, 1.0
	v_mov_b32_e32 v120, v181
	v_add_f32_e32 v78, v78, v62
	v_mov_b32_dpp v119, v81 row_shl:1 row_mask:0xf bank_mask:0xf
	v_mov_b32_dpp v120, v77 row_shl:1 row_mask:0xf bank_mask:0xf
	v_mul_f32_e32 v82, 0xc1000000, v82
	v_fmac_f32_e32 v77, v81, v120
	v_mul_f32_e32 v81, v81, v119
	v_mov_b32_e32 v119, 1.0
	v_mov_b32_e32 v120, v181
	v_mul_f32_e32 v78, 0xbfb8aa3b, v78
	v_mul_f32_e32 v82, v58, v82
	v_mov_b32_dpp v119, v81 row_shl:2 row_mask:0xf bank_mask:0xf
	v_mov_b32_dpp v120, v77 row_shl:2 row_mask:0xf bank_mask:0xf
	v_exp_f32_e32 v78, v78
	v_mul_f32_e32 v82, 0x3fb8aa3b, v82
	v_add_f32_e32 v83, v83, v67
	v_fmac_f32_e32 v77, v81, v120
	v_mul_f32_e32 v81, v81, v119
	v_mov_b32_e32 v119, 1.0
	v_mov_b32_e32 v120, v181
	v_exp_f32_e32 v82, v82
	v_mul_f32_e32 v83, 0xbfb8aa3b, v83
	v_mov_b32_dpp v119, v81 row_shl:4 row_mask:0xf bank_mask:0xf
	v_mov_b32_dpp v120, v77 row_shl:4 row_mask:0xf bank_mask:0xf
	v_exp_f32_e32 v83, v83
	v_fmac_f32_e32 v77, v81, v120
; #define LAS __attribute__((address_space(3)))
; __device__ __forceinline__ float fsigmoid(float x) { return __builtin_amdgcn_rcpf(1.0f + __expf(-x)); }
; template <int PASS, bool REV> ...
;     ...
;         const int ch = blk * 64 + ng * 16 + fq * 4; const f32x4 sp = *(const LAS f32x4*)(cst + ch), bav = *(const LAS f32x4*)(cst + 256 + ch), bxv = *(const LAS f32x4*)(cst + 512 + ch);
; #pragma unroll
;         for (int tg = 0; tg < 4; ++tg) { const v2u uw = *(const LAS v2u*)(UB + (tg * 16 + fr) * 264 + ch); const float uv[4] = {bflo(uw.x), bfhi(uw.x), bflo(uw.y), bfhi(uw.y)};
; #pragma unroll
;             for (int j = 0; j < 4; ++j) { const float r = fsigmoid(aa[tg][j] + bav[j]), ig = fsigmoid(ax[tg][j] + bxv[j]); const float la = -8.0f * r * sp[j];
;                 float Av = __expf(la); const float om = __builtin_fmaf(-Av, Av, 1.0f);
;                 float Bv = __builtin_amdgcn_sqrtf(om) * (ig * uv[j]);
;                 rg_scan_step<REV, 1>(Av, Bv); rg_scan_step<REV, 2>(Av, Bv); rg_scan_step<REV, 4>(Av, Bv); rg_scan_step<REV, 8>(Av, Bv);
;                 aa[tg][j] = Av; ax[tg][j] = Bv; } }
	v_mul_f32_e32 v81, v81, v119
	v_mov_b32_e32 v119, 1.0
	v_mov_b32_e32 v120, v181
	v_add_f32_e32 v78, 1.0, v78
	v_mov_b32_dpp v119, v81 row_shl:8 row_mask:0xf bank_mask:0xf
	v_mov_b32_dpp v120, v77 row_shl:8 row_mask:0xf bank_mask:0xf
	v_fmac_f32_e32 v77, v81, v120
	v_mul_f32_e32 v81, v81, v119
	v_rcp_f32_e32 v78, v78
	v_fma_f32 v119, -v82, v82, 1.0
	v_sqrt_f32_e32 v119, v119
	v_add_f32_e32 v83, 1.0, v83
	v_rcp_f32_e32 v83, v83
	v_lshlrev_b32_e32 v122, 16, v121
	v_mul_f32_e32 v78, v78, v122
	v_mul_f32_e32 v78, v119, v78
	v_mov_b32_e32 v119, 1.0
	v_mov_b32_e32 v120, v181
	v_add_f32_e32 v79, v79, v63
	v_mov_b32_dpp v119, v82 row_shl:1 row_mask:0xf bank_mask:0xf
	v_mov_b32_dpp v120, v78 row_shl:1 row_mask:0xf bank_mask:0xf
	v_mul_f32_e32 v83, 0xc1000000, v83
	v_fmac_f32_e32 v78, v82, v120
	v_mul_f32_e32 v82, v82, v119
	v_mov_b32_e32 v119, 1.0
	v_mov_b32_e32 v120, v181
	v_mul_f32_e32 v79, 0xbfb8aa3b, v79
	v_mul_f32_e32 v83, v59, v83
	v_mov_b32_dpp v119, v82 row_shl:2 row_mask:0xf bank_mask:0xf
	v_mov_b32_dpp v120, v78 row_shl:2 row_mask:0xf bank_mask:0xf
	v_exp_f32_e32 v79, v79
	v_mul_f32_e32 v83, 0x3fb8aa3b, v83
	v_fmac_f32_e32 v78, v82, v120
	v_mul_f32_e32 v82, v82, v119
	v_mov_b32_e32 v119, 1.0
	v_mov_b32_e32 v120, v181
	v_exp_f32_e32 v83, v83
	v_mov_b32_dpp v119, v82 row_shl:4 row_mask:0xf bank_mask:0xf
	v_mov_b32_dpp v120, v78 row_shl:4 row_mask:0xf bank_mask:0xf
	v_add_f32_e32 v72, v72, v64
	v_fmac_f32_e32 v78, v82, v120
	v_mul_f32_e32 v82, v82, v119
	v_mov_b32_e32 v119, 1.0
	v_mov_b32_e32 v120, v181
	v_mul_f32_e32 v72, 0xbfb8aa3b, v72
	v_mov_b32_dpp v119, v82 row_shl:8 row_mask:0xf bank_mask:0xf
	v_mov_b32_dpp v120, v78 row_shl:8 row_mask:0xf bank_mask:0xf
	v_add_f32_e32 v79, 1.0, v79
	v_exp_f32_e32 v72, v72
	v_fmac_f32_e32 v78, v82, v120
	v_mul_f32_e32 v82, v82, v119
	v_rcp_f32_e32 v79, v79
	v_fma_f32 v119, -v83, v83, 1.0
	v_sqrt_f32_e32 v119, v119
	v_and_b32_e32 v121, 0xffff0000, v121
	v_add_f32_e32 v72, 1.0, v72
	v_mul_f32_e32 v79, v79, v121
	v_rcp_f32_e32 v72, v72
	v_mul_f32_e32 v79, v119, v79
	v_mov_b32_e32 v120, v181
	v_mov_b32_e32 v119, 1.0
	v_add_f32_e32 v68, v68, v60
	v_mov_b32_dpp v120, v79 row_shl:1 row_mask:0xf bank_mask:0xf
	v_mov_b32_dpp v119, v83 row_shl:1 row_mask:0xf bank_mask:0xf
	v_fmac_f32_e32 v79, v83, v120
	v_mov_b32_e32 v120, v181
	v_mul_f32_e32 v83, v83, v119
	v_mov_b32_e32 v119, 1.0
	v_mov_b32_dpp v120, v79 row_shl:2 row_mask:0xf bank_mask:0xf
	v_mul_f32_e32 v72, 0xc1000000, v72
	v_mov_b32_dpp v119, v83 row_shl:2 row_mask:0xf bank_mask:0xf
	v_fmac_f32_e32 v79, v83, v120
	v_mov_b32_e32 v120, v181
	v_mul_f32_e32 v68, 0xbfb8aa3b, v68
	v_mul_f32_e32 v72, v56, v72
	v_mul_f32_e32 v83, v83, v119
	v_mov_b32_e32 v119, 1.0
	v_mov_b32_dpp v120, v79 row_shl:4 row_mask:0xf bank_mask:0xf
	v_exp_f32_e32 v68, v68
	v_mul_f32_e32 v72, 0x3fb8aa3b, v72
	v_add_f32_e32 v73, v73, v65
	v_mov_b32_dpp v119, v83 row_shl:4 row_mask:0xf bank_mask:0xf
	v_fmac_f32_e32 v79, v83, v120
	v_mov_b32_e32 v120, v181
	v_exp_f32_e32 v72, v72
	v_mul_f32_e32 v73, 0xbfb8aa3b, v73
	v_mul_f32_e32 v83, v83, v119
	v_mov_b32_dpp v120, v79 row_shl:8 row_mask:0xf bank_mask:0xf
	v_exp_f32_e32 v73, v73
	v_fmac_f32_e32 v79, v83, v120
	ds_read_b64 v[120:121], v118 offset:16896
	v_add_f32_e32 v68, 1.0, v68
	v_rcp_f32_e32 v68, v68
	v_fma_f32 v123, -v72, v72, 1.0
	v_add_f32_e32 v52, v52, v64
	v_mov_b32_e32 v119, 1.0
	v_sqrt_f32_e32 v123, v123
	v_add_f32_e32 v73, 1.0, v73
	v_mul_f32_e32 v52, 0xbfb8aa3b, v52
	v_mov_b32_dpp v119, v83 row_shl:8 row_mask:0xf bank_mask:0xf
	v_rcp_f32_e32 v73, v73
	v_exp_f32_e32 v52, v52
	v_mul_f32_e32 v83, v83, v119
	s_waitcnt lgkmcnt(0)
	v_lshlrev_b32_e32 v119, 16, v120
	v_mul_f32_e32 v68, v68, v119
	v_mul_f32_e32 v68, v123, v68
	v_mov_b32_e32 v119, 1.0
	v_mov_b32_e32 v123, v181
	v_add_f32_e32 v70, v70, v62
	v_mov_b32_dpp v119, v72 row_shl:1 row_mask:0xf bank_mask:0xf
	v_mov_b32_dpp v123, v68 row_shl:1 row_mask:0xf bank_mask:0xf
	v_add_f32_e32 v69, v69, v61
	v_mul_f32_e32 v73, 0xc1000000, v73
	v_mul_f32_e32 v70, 0xbfb8aa3b, v70
	v_add_f32_e32 v52, 1.0, v52
	v_fmac_f32_e32 v68, v72, v123
	v_mul_f32_e32 v72, v72, v119
	v_mov_b32_e32 v119, 1.0
	v_mov_b32_e32 v123, v181
	v_mul_f32_e32 v69, 0xbfb8aa3b, v69
	v_mul_f32_e32 v73, v57, v73
	v_exp_f32_e32 v70, v70
	v_rcp_f32_e32 v52, v52
	v_mov_b32_dpp v119, v72 row_shl:2 row_mask:0xf bank_mask:0xf
	v_mov_b32_dpp v123, v68 row_shl:2 row_mask:0xf bank_mask:0xf
	v_exp_f32_e32 v69, v69
	v_mul_f32_e32 v73, 0x3fb8aa3b, v73
	v_add_f32_e32 v74, v74, v66
	v_fmac_f32_e32 v68, v72, v123
	v_mul_f32_e32 v72, v72, v119
	v_mov_b32_e32 v119, 1.0
	v_mov_b32_e32 v123, v181
	v_exp_f32_e32 v73, v73
	v_mul_f32_e32 v74, 0xbfb8aa3b, v74
	v_mov_b32_dpp v119, v72 row_shl:4 row_mask:0xf bank_mask:0xf
	v_mov_b32_dpp v123, v68 row_shl:4 row_mask:0xf bank_mask:0xf
	v_exp_f32_e32 v74, v74
	v_add_f32_e32 v71, v71, v63
	v_fmac_f32_e32 v68, v72, v123
	v_mul_f32_e32 v72, v72, v119
	v_mov_b32_e32 v119, 1.0
	v_mov_b32_e32 v123, v181
	v_add_f32_e32 v70, 1.0, v70
	v_mul_f32_e32 v71, 0xbfb8aa3b, v71
	v_add_f32_e32 v48, v48, v60
	v_mul_f32_e32 v52, 0xc1000000, v52
	v_mov_b32_dpp v119, v72 row_shl:8 row_mask:0xf bank_mask:0xf
	v_mov_b32_dpp v123, v68 row_shl:8 row_mask:0xf bank_mask:0xf
	v_add_f32_e32 v69, 1.0, v69
	v_rcp_f32_e32 v70, v70
	v_exp_f32_e32 v71, v71
	v_mul_f32_e32 v48, 0xbfb8aa3b, v48
	v_mul_f32_e32 v52, v56, v52
	v_fmac_f32_e32 v68, v72, v123
	v_mul_f32_e32 v72, v72, v119
	v_rcp_f32_e32 v69, v69
	v_fma_f32 v119, -v73, v73, 1.0
	v_exp_f32_e32 v48, v48
	v_mul_f32_e32 v52, 0x3fb8aa3b, v52
	v_sqrt_f32_e32 v119, v119
	v_add_f32_e32 v74, 1.0, v74
	v_exp_f32_e32 v52, v52
	v_lshlrev_b32_e32 v122, 16, v121
	v_rcp_f32_e32 v74, v74
	v_and_b32_e32 v120, 0xffff0000, v120
	v_mul_f32_e32 v70, v70, v122
	v_add_f32_e32 v71, 1.0, v71
	ds_read_b64 v[122:123], v118 offset:25344
	v_mul_f32_e32 v69, v69, v120
	v_rcp_f32_e32 v71, v71
	v_add_f32_e32 v48, 1.0, v48
	v_mul_f32_e32 v69, v119, v69
	v_mov_b32_e32 v119, 1.0
	v_mov_b32_e32 v120, v181
	v_rcp_f32_e32 v48, v48
	v_fma_f32 v56, -v52, v52, 1.0
	v_mov_b32_dpp v119, v73 row_shl:1 row_mask:0xf bank_mask:0xf
	v_mov_b32_dpp v120, v69 row_shl:1 row_mask:0xf bank_mask:0xf
	v_mul_f32_e32 v74, 0xc1000000, v74
	v_sqrt_f32_e32 v56, v56
	v_and_b32_e32 v121, 0xffff0000, v121
	v_fmac_f32_e32 v69, v73, v120
	v_mul_f32_e32 v73, v73, v119
	v_mov_b32_e32 v119, 1.0
	v_mov_b32_e32 v120, v181
	v_mul_f32_e32 v74, v58, v74
	v_mov_b32_dpp v119, v73 row_shl:2 row_mask:0xf bank_mask:0xf
	v_mov_b32_dpp v120, v69 row_shl:2 row_mask:0xf bank_mask:0xf
	v_mul_f32_e32 v74, 0x3fb8aa3b, v74
	v_add_f32_e32 v75, v75, v67
	v_mul_f32_e32 v71, v71, v121
	s_waitcnt lgkmcnt(0)
; #define LAS __attribute__((address_space(3)))
; __device__ __forceinline__ float fsigmoid(float x) { return __builtin_amdgcn_rcpf(1.0f + __expf(-x)); }
; template <int PASS, bool REV> ...
;     ...
;         const int ch = blk * 64 + ng * 16 + fq * 4; const f32x4 sp = *(const LAS f32x4*)(cst + ch), bav = *(const LAS f32x4*)(cst + 256 + ch), bxv = *(const LAS f32x4*)(cst + 512 + ch);
; #pragma unroll
;         for (int tg = 0; tg < 4; ++tg) { const v2u uw = *(const LAS v2u*)(UB + (tg * 16 + fr) * 264 + ch); const float uv[4] = {bflo(uw.x), bfhi(uw.x), bflo(uw.y), bfhi(uw.y)};
; #pragma unroll
;             for (int j = 0; j < 4; ++j) { const float r = fsigmoid(aa[tg][j] + bav[j]), ig = fsigmoid(ax[tg][j] + bxv[j]); const float la = -8.0f * r * sp[j];
;                 float Av = __expf(la); const float om = __builtin_fmaf(-Av, Av, 1.0f);
;                 float Bv = __builtin_amdgcn_sqrtf(om) * (ig * uv[j]);
;                 rg_scan_step<REV, 1>(Av, Bv); rg_scan_step<REV, 2>(Av, Bv); rg_scan_step<REV, 4>(Av, Bv); rg_scan_step<REV, 8>(Av, Bv);
;                 aa[tg][j] = Av; ax[tg][j] = Bv; } }
	v_lshlrev_b32_e32 v121, 16, v122
	v_fmac_f32_e32 v69, v73, v120
	v_mul_f32_e32 v73, v73, v119
	v_mov_b32_e32 v119, 1.0
	v_mov_b32_e32 v120, v181
	v_exp_f32_e32 v74, v74
	v_mul_f32_e32 v75, 0xbfb8aa3b, v75
	v_mul_f32_e32 v48, v48, v121
	v_mov_b32_dpp v119, v73 row_shl:4 row_mask:0xf bank_mask:0xf
	v_mov_b32_dpp v120, v69 row_shl:4 row_mask:0xf bank_mask:0xf
	v_exp_f32_e32 v75, v75
	v_mul_f32_e32 v56, v56, v48
	v_mov_b32_e32 v48, 1.0
	v_mov_b32_e32 v60, v181
	v_fmac_f32_e32 v69, v73, v120
	v_mul_f32_e32 v73, v73, v119
	v_mov_b32_e32 v119, 1.0
	v_mov_b32_e32 v120, v181
	v_mov_b32_dpp v48, v52 row_shl:1 row_mask:0xf bank_mask:0xf
	v_mov_b32_dpp v60, v56 row_shl:1 row_mask:0xf bank_mask:0xf
	v_mov_b32_dpp v119, v73 row_shl:8 row_mask:0xf bank_mask:0xf
	v_mov_b32_dpp v120, v69 row_shl:8 row_mask:0xf bank_mask:0xf
	v_fmac_f32_e32 v56, v52, v60
	v_mul_f32_e32 v48, v52, v48
	v_mov_b32_e32 v52, 1.0
	v_mov_b32_e32 v60, v181
	v_fmac_f32_e32 v69, v73, v120
	v_mul_f32_e32 v73, v73, v119
	v_fma_f32 v119, -v74, v74, 1.0
	v_mov_b32_dpp v52, v48 row_shl:2 row_mask:0xf bank_mask:0xf
	v_mov_b32_dpp v60, v56 row_shl:2 row_mask:0xf bank_mask:0xf
	v_sqrt_f32_e32 v119, v119
	v_add_f32_e32 v75, 1.0, v75
	v_fmac_f32_e32 v56, v48, v60
	v_mul_f32_e32 v48, v48, v52
	v_mov_b32_e32 v52, 1.0
	v_mov_b32_e32 v60, v181
	v_rcp_f32_e32 v75, v75
	v_mov_b32_dpp v52, v48 row_shl:4 row_mask:0xf bank_mask:0xf
	v_mov_b32_dpp v60, v56 row_shl:4 row_mask:0xf bank_mask:0xf
	v_fmac_f32_e32 v56, v48, v60
	v_mul_f32_e32 v48, v48, v52
	v_mov_b32_e32 v52, 1.0
	v_mov_b32_e32 v60, v181
	v_mul_f32_e32 v70, v119, v70
	v_mov_b32_dpp v52, v48 row_shl:8 row_mask:0xf bank_mask:0xf
	v_mov_b32_dpp v60, v56 row_shl:8 row_mask:0xf bank_mask:0xf
	v_mov_b32_e32 v119, 1.0
	v_mov_b32_e32 v120, v181
	v_fmac_f32_e32 v56, v48, v60
	v_mul_f32_e32 v48, v48, v52
	v_add_f32_e32 v52, v53, v65
	v_mov_b32_dpp v119, v74 row_shl:1 row_mask:0xf bank_mask:0xf
	v_mov_b32_dpp v120, v70 row_shl:1 row_mask:0xf bank_mask:0xf
	v_mul_f32_e32 v75, 0xc1000000, v75
	v_mul_f32_e32 v52, 0xbfb8aa3b, v52
	v_fmac_f32_e32 v70, v74, v120
	v_mul_f32_e32 v74, v74, v119
	v_mov_b32_e32 v119, 1.0
	v_mov_b32_e32 v120, v181
	v_mul_f32_e32 v75, v59, v75
	v_exp_f32_e32 v52, v52
	v_mov_b32_dpp v119, v74 row_shl:2 row_mask:0xf bank_mask:0xf
	v_mov_b32_dpp v120, v70 row_shl:2 row_mask:0xf bank_mask:0xf
	v_mul_f32_e32 v75, 0x3fb8aa3b, v75
	v_fmac_f32_e32 v70, v74, v120
	v_mul_f32_e32 v74, v74, v119
	v_mov_b32_e32 v119, 1.0
	v_mov_b32_e32 v120, v181
	v_exp_f32_e32 v75, v75
	v_mov_b32_dpp v119, v74 row_shl:4 row_mask:0xf bank_mask:0xf
	v_mov_b32_dpp v120, v70 row_shl:4 row_mask:0xf bank_mask:0xf
	v_fmac_f32_e32 v70, v74, v120
	v_mul_f32_e32 v74, v74, v119
	v_mov_b32_e32 v119, 1.0
	v_mov_b32_e32 v120, v181
	v_add_f32_e32 v52, 1.0, v52
	v_mov_b32_dpp v119, v74 row_shl:8 row_mask:0xf bank_mask:0xf
	v_mov_b32_dpp v120, v70 row_shl:8 row_mask:0xf bank_mask:0xf
	v_rcp_f32_e32 v52, v52
	v_fmac_f32_e32 v70, v74, v120
	v_mul_f32_e32 v74, v74, v119
	v_fma_f32 v119, -v75, v75, 1.0
	v_sqrt_f32_e32 v119, v119
	v_add_f32_e32 v49, v49, v61
	v_mul_f32_e32 v52, 0xc1000000, v52
	v_mul_f32_e32 v49, 0xbfb8aa3b, v49
	v_mul_f32_e32 v52, v57, v52
	v_mul_f32_e32 v71, v119, v71
	v_mov_b32_e32 v120, v181
	v_exp_f32_e32 v49, v49
	v_mul_f32_e32 v52, 0x3fb8aa3b, v52
	v_mov_b32_e32 v119, 1.0
	v_mov_b32_dpp v120, v71 row_shl:1 row_mask:0xf bank_mask:0xf
	v_exp_f32_e32 v52, v52
	v_mov_b32_dpp v119, v75 row_shl:1 row_mask:0xf bank_mask:0xf
	v_fmac_f32_e32 v71, v75, v120
	v_mov_b32_e32 v120, v181
	v_mul_f32_e32 v75, v75, v119
	v_mov_b32_e32 v119, 1.0
	v_mov_b32_dpp v120, v71 row_shl:2 row_mask:0xf bank_mask:0xf
	v_fmac_f32_e32 v71, v75, v120
	v_mov_b32_dpp v119, v75 row_shl:2 row_mask:0xf bank_mask:0xf
	v_mov_b32_e32 v120, v181
	v_add_f32_e32 v49, 1.0, v49
	v_mul_f32_e32 v75, v75, v119
	v_mov_b32_e32 v119, 1.0
	v_mov_b32_dpp v120, v71 row_shl:4 row_mask:0xf bank_mask:0xf
	v_rcp_f32_e32 v49, v49
	v_fma_f32 v53, -v52, v52, 1.0
	v_mov_b32_dpp v119, v75 row_shl:4 row_mask:0xf bank_mask:0xf
	v_fmac_f32_e32 v71, v75, v120
	v_mov_b32_e32 v120, v181
	v_sqrt_f32_e32 v53, v53
	v_mul_f32_e32 v75, v75, v119
	v_mov_b32_dpp v120, v71 row_shl:8 row_mask:0xf bank_mask:0xf
	v_fmac_f32_e32 v71, v75, v120
	v_and_b32_e32 v120, 0xffff0000, v122
	v_mul_f32_e32 v49, v49, v120
	v_mul_f32_e32 v53, v53, v49
	v_mov_b32_e32 v49, 1.0
	v_mov_b32_e32 v57, v181
	v_add_f32_e32 v50, v50, v62
	v_mov_b32_dpp v49, v52 row_shl:1 row_mask:0xf bank_mask:0xf
	v_mov_b32_dpp v57, v53 row_shl:1 row_mask:0xf bank_mask:0xf
	v_fmac_f32_e32 v53, v52, v57
	v_mul_f32_e32 v49, v52, v49
	v_mov_b32_e32 v52, 1.0
	v_mov_b32_e32 v57, v181
	v_mul_f32_e32 v50, 0xbfb8aa3b, v50
	v_mov_b32_dpp v52, v49 row_shl:2 row_mask:0xf bank_mask:0xf
	v_mov_b32_dpp v57, v53 row_shl:2 row_mask:0xf bank_mask:0xf
	v_fmac_f32_e32 v53, v49, v57
	v_mul_f32_e32 v49, v49, v52
	v_mov_b32_e32 v52, 1.0
	v_mov_b32_e32 v57, v181
	v_exp_f32_e32 v50, v50
	v_mov_b32_dpp v52, v49 row_shl:4 row_mask:0xf bank_mask:0xf
	v_mov_b32_dpp v57, v53 row_shl:4 row_mask:0xf bank_mask:0xf
	v_fmac_f32_e32 v53, v49, v57
	v_mul_f32_e32 v49, v49, v52
	v_mov_b32_e32 v52, 1.0
	v_mov_b32_e32 v57, v181
	v_add_f32_e32 v50, 1.0, v50
	v_mov_b32_dpp v52, v49 row_shl:8 row_mask:0xf bank_mask:0xf
; #define LAS __attribute__((address_space(3)))
; __device__ __forceinline__ float fsigmoid(float x) { return __builtin_amdgcn_rcpf(1.0f + __expf(-x)); }
; __device__ __forceinline__ float bperm_f(int idx4, float x) { return __builtin_bit_cast(float, __builtin_amdgcn_ds_bpermute(idx4, __builtin_bit_cast(int, x))); }
; template <int PASS, bool REV> ...
;     ...
;         for (int tg = 0; tg < 4; ++tg) { const v2u uw = *(const LAS v2u*)(UB + (tg * 16 + fr) * 264 + ch); const float uv[4] = {bflo(uw.x), bfhi(uw.x), bflo(uw.y), bfhi(uw.y)};
; #pragma unroll
;             for (int j = 0; j < 4; ++j) { const float r = fsigmoid(aa[tg][j] + bav[j]), ig = fsigmoid(ax[tg][j] + bxv[j]); const float la = -8.0f * r * sp[j];
;                 float Av = __expf(la); const float om = __builtin_fmaf(-Av, Av, 1.0f);
;                 float Bv = __builtin_amdgcn_sqrtf(om) * (ig * uv[j]);
;                 rg_scan_step<REV, 1>(Av, Bv); rg_scan_step<REV, 2>(Av, Bv); rg_scan_step<REV, 4>(Av, Bv); rg_scan_step<REV, 8>(Av, Bv);
;                 aa[tg][j] = Av; ax[tg][j] = Bv; } }
;         const int lastl4 = ((lane & 48) | (REV ? 0 : 15)) << 2;
;         if (PASS == 1) {
;             f32x4 At = (f32x4){1.f, 1.f, 1.f, 1.f}, Bt = (f32x4){0.f, 0.f, 0.f, 0.f};
; #pragma unroll
;             for (int t4 = 0; t4 < 4; ++t4) { const int tg = REV ? 3 - t4 : t4;
; #pragma unroll
;                 for (int j = 0; j < 4; ++j) { const float ta = bperm_f(lastl4, aa[tg][j]), tb = bperm_f(lastl4, ax[tg][j]); Bt[j] = ta * Bt[j] + tb; At[j] = At[j] * ta; } }
;             if (fr == 0) { f32x4* cp = (f32x4*)(CAR + ((size_t)u * 2 + d) * 256 + ch); cp[0] = (f32x4){At[0], Bt[0], At[1], Bt[1]}; cp[1] = (f32x4){At[2], Bt[2], At[3], Bt[3]}; }
	v_mov_b32_dpp v57, v53 row_shl:8 row_mask:0xf bank_mask:0xf
	v_fmac_f32_e32 v53, v49, v57
	v_mul_f32_e32 v49, v49, v52
	v_add_f32_e32 v52, v54, v66
	v_mul_f32_e32 v52, 0xbfb8aa3b, v52
	v_exp_f32_e32 v52, v52
	v_rcp_f32_e32 v50, v50
	v_mov_b32_e32 v119, 1.0
	v_mov_b32_e32 v57, v181
	v_add_f32_e32 v52, 1.0, v52
	v_rcp_f32_e32 v52, v52
	v_mov_b32_dpp v119, v75 row_shl:8 row_mask:0xf bank_mask:0xf
	v_mul_f32_e32 v75, v75, v119
	v_lshlrev_b32_e32 v119, 16, v123
	v_mul_f32_e32 v52, 0xc1000000, v52
	v_mul_f32_e32 v52, v58, v52
	v_mul_f32_e32 v52, 0x3fb8aa3b, v52
	v_exp_f32_e32 v52, v52
	v_mul_f32_e32 v50, v50, v119
	v_add_f32_e32 v51, v51, v63
	v_mul_f32_e32 v51, 0xbfb8aa3b, v51
	v_fma_f32 v54, -v52, v52, 1.0
	v_sqrt_f32_e32 v54, v54
	v_exp_f32_e32 v51, v51
	v_and_b32_e32 v118, 0xffff0000, v123
	ds_bpermute_b32 v48, v101, v48
	v_mul_f32_e32 v54, v54, v50
	v_mov_b32_e32 v50, 1.0
	v_add_f32_e32 v51, 1.0, v51
	v_mov_b32_dpp v57, v54 row_shl:1 row_mask:0xf bank_mask:0xf
	v_mov_b32_dpp v50, v52 row_shl:1 row_mask:0xf bank_mask:0xf
	v_fmac_f32_e32 v54, v52, v57
	v_mul_f32_e32 v50, v52, v50
	v_mov_b32_e32 v52, 1.0
	v_mov_b32_e32 v57, v181
	v_rcp_f32_e32 v51, v51
	v_mov_b32_dpp v52, v50 row_shl:2 row_mask:0xf bank_mask:0xf
	v_mov_b32_dpp v57, v54 row_shl:2 row_mask:0xf bank_mask:0xf
	v_fmac_f32_e32 v54, v50, v57
	v_mul_f32_e32 v50, v50, v52
	v_mov_b32_e32 v52, 1.0
	v_mov_b32_e32 v57, v181
	v_mul_f32_e32 v51, v51, v118
	v_mov_b32_dpp v52, v50 row_shl:4 row_mask:0xf bank_mask:0xf
	v_mov_b32_dpp v57, v54 row_shl:4 row_mask:0xf bank_mask:0xf
	v_fmac_f32_e32 v54, v50, v57
	v_mul_f32_e32 v50, v50, v52
	v_mov_b32_e32 v52, 1.0
	v_mov_b32_e32 v57, v181
	ds_bpermute_b32 v49, v101, v49
	v_mov_b32_dpp v52, v50 row_shl:8 row_mask:0xf bank_mask:0xf
	v_mov_b32_dpp v57, v54 row_shl:8 row_mask:0xf bank_mask:0xf
	v_fmac_f32_e32 v54, v50, v57
	v_mul_f32_e32 v50, v50, v52
	v_add_f32_e32 v52, v55, v67
	v_mul_f32_e32 v52, 0xbfb8aa3b, v52
	v_exp_f32_e32 v52, v52
	v_mov_b32_e32 v57, v181
	ds_bpermute_b32 v53, v101, v53
	ds_bpermute_b32 v50, v101, v50
	v_add_f32_e32 v52, 1.0, v52
	v_rcp_f32_e32 v52, v52
	ds_bpermute_b32 v54, v101, v54
	ds_bpermute_b32 v60, v101, v68
	ds_bpermute_b32 v61, v101, v69
	v_mul_f32_e32 v52, 0xc1000000, v52
	v_mul_f32_e32 v52, v59, v52
	v_mul_f32_e32 v52, 0x3fb8aa3b, v52
	v_exp_f32_e32 v52, v52
	ds_bpermute_b32 v58, v101, v74
	ds_bpermute_b32 v62, v101, v70
	ds_bpermute_b32 v59, v101, v75
	v_fma_f32 v55, -v52, v52, 1.0
	v_sqrt_f32_e32 v55, v55
	ds_bpermute_b32 v63, v101, v71
	ds_bpermute_b32 v64, v101, v80
	ds_bpermute_b32 v68, v101, v76
	v_mul_f32_e32 v55, v55, v51
	v_mov_b32_e32 v51, 1.0
	ds_bpermute_b32 v65, v101, v81
	v_mov_b32_dpp v57, v55 row_shl:1 row_mask:0xf bank_mask:0xf
	v_mov_b32_dpp v51, v52 row_shl:1 row_mask:0xf bank_mask:0xf
	v_fmac_f32_e32 v55, v52, v57
	v_mul_f32_e32 v51, v52, v51
	v_mov_b32_e32 v52, 1.0
	v_mov_b32_e32 v57, v181
	ds_bpermute_b32 v69, v101, v77
	v_mov_b32_dpp v52, v51 row_shl:2 row_mask:0xf bank_mask:0xf
	v_mov_b32_dpp v57, v55 row_shl:2 row_mask:0xf bank_mask:0xf
	v_fmac_f32_e32 v55, v51, v57
	v_mul_f32_e32 v51, v51, v52
	v_mov_b32_e32 v52, 1.0
	v_mov_b32_e32 v57, v181
	ds_bpermute_b32 v66, v101, v82
	v_mov_b32_dpp v52, v51 row_shl:4 row_mask:0xf bank_mask:0xf
	v_mov_b32_dpp v57, v55 row_shl:4 row_mask:0xf bank_mask:0xf
	v_fmac_f32_e32 v55, v51, v57
	v_mul_f32_e32 v51, v51, v52
	v_mov_b32_e32 v52, 1.0
	v_mov_b32_e32 v57, v181
	ds_bpermute_b32 v70, v101, v78
	v_mov_b32_dpp v52, v51 row_shl:8 row_mask:0xf bank_mask:0xf
	v_mov_b32_dpp v57, v55 row_shl:8 row_mask:0xf bank_mask:0xf
	v_fmac_f32_e32 v55, v51, v57
	v_mul_f32_e32 v51, v51, v52
	ds_bpermute_b32 v52, v101, v56
	ds_bpermute_b32 v51, v101, v51
	ds_bpermute_b32 v55, v101, v55
	ds_bpermute_b32 v56, v101, v72
	ds_bpermute_b32 v57, v101, v73
	ds_bpermute_b32 v67, v101, v83
	ds_bpermute_b32 v71, v101, v79
	ds_bpermute_b32 v72, v101, v88
	ds_bpermute_b32 v76, v101, v84
	ds_bpermute_b32 v73, v101, v89
	ds_bpermute_b32 v77, v101, v85
	ds_bpermute_b32 v74, v101, v90
	ds_bpermute_b32 v78, v101, v86
	ds_bpermute_b32 v75, v101, v91
	ds_bpermute_b32 v79, v101, v87
	s_and_saveexec_b64 s[0:1], s[36:37]
	s_cbranch_execz .LBB0_552
	s_waitcnt lgkmcnt(10)
	v_pk_mul_f32 v[80:81], v[48:49], v[56:57]
	v_pk_fma_f32 v[48:49], v[48:49], 0, v[52:53] op_sel_hi:[1,0,1]
	v_pk_mul_f32 v[80:81], v[80:81], v[64:65]
	v_pk_fma_f32 v[48:49], v[48:49], v[56:57], v[60:61]
	v_pk_mul_f32 v[82:83], v[50:51], v[58:59]
	v_pk_fma_f32 v[48:49], v[48:49], v[64:65], v[68:69]
	s_waitcnt lgkmcnt(5)
	v_pk_mul_f32 v[80:81], v[80:81], v[72:73]
	s_waitcnt lgkmcnt(4)
	v_pk_fma_f32 v[52:53], v[48:49], v[72:73], v[76:77]
	v_pk_fma_f32 v[48:49], v[50:51], 0, v[54:55] op_sel_hi:[1,0,1]
	v_pk_mul_f32 v[82:83], v[82:83], v[66:67]
	v_pk_fma_f32 v[48:49], v[48:49], v[58:59], v[62:63]
	s_waitcnt lgkmcnt(1)
	v_pk_mul_f32 v[82:83], v[82:83], v[74:75]
	v_pk_fma_f32 v[48:49], v[48:49], v[66:67], v[70:71]
	v_mov_b32_e32 v50, v80
	s_waitcnt lgkmcnt(0)
	v_pk_fma_f32 v[54:55], v[48:49], v[74:75], v[78:79]
	v_mov_b32_e32 v51, v52
	v_mov_b32_e32 v52, v81
	global_store_dwordx4 v[102:103], v[50:53], off offset:-16
	s_nop 1
	v_mov_b32_e32 v52, v82
	v_mov_b32_e32 v53, v54
	v_mov_b32_e32 v54, v83
	global_store_dwordx4 v[102:103], v[52:55], off
	s_branch .LBB0_552
.LBB0_564:
	s_mov_b64 s[0:1], 0

; template <int R, class XT, class TWT>
; __device__ __forceinline__ void dif_task(XT X, TWT tw, int s, int task) {
;     const int lgM = 13 - s, lgq = lgM - R, q = 1 << lgq;
;     const int j0 = task & (q - 1), blk = task >> lgq, base = (blk << lgM) + j0;
;     const int pb = PADI(base), qp = (q >= 32) ? q + (q >> 4) : q;
;     f32x2v v[1 << R];
; #pragma unroll
;     for (int k = 0; k < (1 << R); ++k) v[k] = X[pb + k * qp];
; #pragma unroll
;     for (int r = 0; r < R; ++r) {
;         const int pb = R - 1 - r;
; #pragma unroll
;         for (int k = 0; k < (1 << R); ++k) if (!((k >> pb) & 1)) {
;             const int klo = k & ((1 << pb) - 1);
;             const f32x2v w = tw[(j0 + (klo << lgq)) << (s + r)];
;             const f32x2v a = v[k], b = v[k + (1 << pb)], d = a - b;
;             v[k] = a + b; v[k + (1 << pb)] = (f32x2v){d.x * w.x - d.y * w.y, d.x * w.y + d.y * w.x};
;         }
;     }
; #pragma unroll
;     for (int k = 0; k < (1 << R); ++k) X[pb + k * qp] = v[k];
; }
; template <bool LAT>
; __device__ __forceinline__ void hyconv_unit(const Frame& F, LAS f32x2v* X, const TwHalf tw, LAS bf16* OUT, const float* skip, bf16* MIX, int u) {
;     ...
;             const f32x2v* SP = SPb + (size_t)ord * 256 * N;
;             f32x4 kq[8];
; #pragma unroll
;             for (int r = 0; r < 8; ++r) kq[r] = *(const f32x4*)(SP + 2 * (F.tid + 512 * r));
;             fft_fwd_upper(X, tw, 13 - lgN, F.tid);
.LBB0_780:
	s_lshl_b32 s90, s0, 21
	s_xor_b64 s[20:21], s[22:23], -1
	s_lshl_b64 s[2:3], s[90:91], 3
	s_add_u32 s2, s29, s2
	s_addc_u32 s3, s52, s3
	v_lshl_add_u64 v[0:1], v[34:35], 3, s[2:3]
	v_lshl_add_u64 v[2:3], v[36:37], 3, s[2:3]
	global_load_dwordx4 v[28:31], v[0:1], off
	global_load_dwordx4 v[24:27], v[2:3], off
	v_lshl_add_u64 v[0:1], v[38:39], 3, s[2:3]
	v_lshl_add_u64 v[2:3], v[40:41], 3, s[2:3]
	global_load_dwordx4 v[20:23], v[0:1], off
	global_load_dwordx4 v[16:19], v[2:3], off
	v_lshl_add_u64 v[0:1], v[42:43], 3, s[2:3]
	v_lshl_add_u64 v[2:3], v[44:45], 3, s[2:3]
	global_load_dwordx4 v[12:15], v[0:1], off
	global_load_dwordx4 v[8:11], v[2:3], off
	v_lshl_add_u64 v[0:1], v[46:47], 3, s[2:3]
	v_lshl_add_u64 v[2:3], v[48:49], 3, s[2:3]
	global_load_dwordx4 v[4:7], v[0:1], off
	s_nop 0
	global_load_dwordx4 v[0:3], v[2:3], off
	ds_read_b64 v[110:111], v75
	ds_read_b64 v[120:121], v75 offset:4352
	ds_read_b64 v[122:123], v75 offset:8704
	ds_read_b64 v[124:125], v75 offset:13056
	ds_read_b64 v[126:127], v75 offset:17408
	ds_read_b64 v[128:129], v75 offset:21760
	ds_read_b64 v[130:131], v75 offset:26112
	ds_read_b64 v[132:133], v75 offset:30464
	ds_read_b64 v[136:137], v75 offset:34816
	ds_read_b64 v[138:139], v75 offset:39168
	ds_read_b64 v[140:141], v75 offset:43520
	ds_read_b64 v[142:143], v75 offset:47872
	ds_read_b64 v[144:145], v75 offset:52224
	ds_read_b64 v[146:147], v75 offset:56576
	ds_read_b64 v[148:149], v75 offset:60928
	ds_read_b64 v[150:151], v75 offset:65280
	ds_read2st64_b64 v[116:119], v76 offset1:16
	ds_read_b64 v[152:153], v91
	ds_read_b64 v[154:155], v92
	ds_read_b64 v[156:157], v93
	ds_read_b64 v[158:159], v77
	ds_read_b64 v[160:161], v78
	ds_read_b64 v[162:163], v79
	ds_read_b64 v[164:165], v80
	s_waitcnt lgkmcnt(14)
	v_pk_add_f32 v[166:167], v[110:111], v[136:137] neg_lo:[0,1] neg_hi:[0,1]
	v_pk_add_f32 v[110:111], v[110:111], v[136:137]
	s_waitcnt lgkmcnt(7)
	v_pk_mul_f32 v[168:169], v[166:167], v[116:117] op_sel:[1,1] op_sel_hi:[1,0]
	s_lshl_b32 s0, s0, 8
	v_pk_fma_f32 v[170:171], v[166:167], v[116:117], v[168:169] neg_lo:[0,0,1] neg_hi:[0,0,1]
	v_pk_fma_f32 v[166:167], v[166:167], v[116:117], v[168:169] op_sel_hi:[0,1,1]
	v_mov_b32_e32 v171, v167
	v_pk_add_f32 v[166:167], v[126:127], v[144:145] neg_lo:[0,1] neg_hi:[0,1]
	v_pk_add_f32 v[126:127], v[126:127], v[144:145]
	v_pk_mul_f32 v[168:169], v[166:167], v[116:117] op_sel:[1,0] op_sel_hi:[0,0]
	v_pk_fma_f32 v[172:173], v[166:167], v[116:117], v[168:169] op_sel:[0,1,0]
	v_pk_fma_f32 v[116:117], v[166:167], v[116:117], v[168:169] op_sel:[0,1,0] neg_lo:[0,0,1] neg_hi:[0,0,1]
	v_pk_add_f32 v[136:137], v[110:111], v[126:127]
	v_mov_b32_e32 v173, v117
	v_pk_add_f32 v[116:117], v[170:171], v[172:173] neg_lo:[0,1] neg_hi:[0,1]
	v_pk_add_f32 v[110:111], v[110:111], v[126:127] neg_lo:[0,1] neg_hi:[0,1]
	s_waitcnt lgkmcnt(6)
	v_pk_mul_f32 v[166:167], v[152:153], v[116:117] op_sel:[1,1] op_sel_hi:[0,1]
	v_pk_fma_f32 v[168:169], v[152:153], v[116:117], v[166:167] neg_lo:[0,0,1] neg_hi:[0,0,1]
	v_pk_fma_f32 v[116:117], v[152:153], v[116:117], v[166:167] op_sel_hi:[1,0,1]
	v_pk_mul_f32 v[126:127], v[110:111], v[152:153] op_sel:[1,1] op_sel_hi:[1,0]
	v_mov_b32_e32 v169, v117
	v_pk_add_f32 v[116:117], v[122:123], v[140:141] neg_lo:[0,1] neg_hi:[0,1]
	v_pk_add_f32 v[122:123], v[122:123], v[140:141]
	v_pk_mul_f32 v[166:167], v[116:117], v[118:119] op_sel:[1,1] op_sel_hi:[1,0]
	s_add_i32 s90, s0, s28
	v_pk_fma_f32 v[174:175], v[116:117], v[118:119], v[166:167] neg_lo:[0,0,1] neg_hi:[0,0,1]
	v_pk_fma_f32 v[116:117], v[116:117], v[118:119], v[166:167] op_sel_hi:[0,1,1]
	v_mov_b32_e32 v175, v117
	v_pk_add_f32 v[116:117], v[130:131], v[148:149] neg_lo:[0,1] neg_hi:[0,1]
	v_pk_add_f32 v[130:131], v[130:131], v[148:149]
	v_pk_mul_f32 v[166:167], v[116:117], v[118:119] op_sel:[1,0] op_sel_hi:[0,0]
	v_pk_fma_f32 v[176:177], v[116:117], v[118:119], v[166:167] op_sel:[0,1,0]
	v_pk_fma_f32 v[116:117], v[116:117], v[118:119], v[166:167] op_sel:[0,1,0] neg_lo:[0,0,1] neg_hi:[0,0,1]
	v_pk_add_f32 v[140:141], v[122:123], v[130:131]
	v_mov_b32_e32 v177, v117
	v_pk_add_f32 v[116:117], v[174:175], v[176:177] neg_lo:[0,1] neg_hi:[0,1]
	v_pk_add_f32 v[144:145], v[136:137], v[140:141]
	v_pk_mul_f32 v[118:119], v[152:153], v[116:117] op_sel_hi:[0,1]
	v_pk_fma_f32 v[166:167], v[152:153], v[116:117], v[118:119] op_sel:[1,0,1] op_sel_hi:[1,1,0]
	v_pk_fma_f32 v[116:117], v[152:153], v[116:117], v[118:119] op_sel:[1,0,1] op_sel_hi:[1,1,0] neg_lo:[0,0,1] neg_hi:[0,0,1]
	v_pk_add_f32 v[136:137], v[136:137], v[140:141] neg_lo:[0,1] neg_hi:[0,1]
	v_mov_b32_e32 v167, v117
	v_pk_add_f32 v[116:117], v[168:169], v[166:167] neg_lo:[0,1] neg_hi:[0,1]
	s_waitcnt lgkmcnt(4)
	v_pk_mul_f32 v[140:141], v[136:137], v[156:157] op_sel:[1,1] op_sel_hi:[1,0]
	v_pk_mul_f32 v[118:119], v[156:157], v[116:117] op_sel:[1,1] op_sel_hi:[0,1]
	v_pk_fma_f32 v[178:179], v[156:157], v[116:117], v[118:119] neg_lo:[0,0,1] neg_hi:[0,0,1]
	v_pk_fma_f32 v[116:117], v[156:157], v[116:117], v[118:119] op_sel_hi:[1,0,1]
	s_lshl_b64 s[0:1], s[90:91], 2
	v_mov_b32_e32 v179, v117
	v_pk_add_f32 v[116:117], v[120:121], v[138:139] neg_lo:[0,1] neg_hi:[0,1]
	v_pk_add_f32 v[120:121], v[120:121], v[138:139]
	s_waitcnt lgkmcnt(3)
; template <int R, class XT, class TWT>
; __device__ __forceinline__ void dif_task(XT X, TWT tw, int s, int task) {
;     const int lgM = 13 - s, lgq = lgM - R, q = 1 << lgq;
;     const int j0 = task & (q - 1), blk = task >> lgq, base = (blk << lgM) + j0;
;     const int pb = PADI(base), qp = (q >= 32) ? q + (q >> 4) : q;
;     f32x2v v[1 << R];
; #pragma unroll
;     for (int k = 0; k < (1 << R); ++k) v[k] = X[pb + k * qp];
; #pragma unroll
;     for (int r = 0; r < R; ++r) {
;         const int pb = R - 1 - r;
; #pragma unroll
;         for (int k = 0; k < (1 << R); ++k) if (!((k >> pb) & 1)) {
;             const int klo = k & ((1 << pb) - 1);
;             const f32x2v w = tw[(j0 + (klo << lgq)) << (s + r)];
;             const f32x2v a = v[k], b = v[k + (1 << pb)], d = a - b;
;             v[k] = a + b; v[k + (1 << pb)] = (f32x2v){d.x * w.x - d.y * w.y, d.x * w.y + d.y * w.x};
;         }
;     }
; #pragma unroll
;     for (int k = 0; k < (1 << R); ++k) X[pb + k * qp] = v[k];
; }
	v_pk_mul_f32 v[118:119], v[116:117], v[158:159] op_sel:[1,1] op_sel_hi:[1,0]
	s_add_u32 s0, s6, s0
	v_pk_fma_f32 v[182:183], v[116:117], v[158:159], v[118:119] neg_lo:[0,0,1] neg_hi:[0,0,1]
	v_pk_fma_f32 v[116:117], v[116:117], v[158:159], v[118:119] op_sel_hi:[0,1,1]
	v_mov_b32_e32 v183, v117
	v_pk_add_f32 v[116:117], v[128:129], v[146:147] neg_lo:[0,1] neg_hi:[0,1]
	v_pk_add_f32 v[128:129], v[128:129], v[146:147]
	v_pk_mul_f32 v[118:119], v[116:117], v[158:159] op_sel:[1,0] op_sel_hi:[0,0]
	v_pk_fma_f32 v[184:185], v[116:117], v[158:159], v[118:119] op_sel:[0,1,0]
	v_pk_fma_f32 v[116:117], v[116:117], v[158:159], v[118:119] op_sel:[0,1,0] neg_lo:[0,0,1] neg_hi:[0,0,1]
	v_pk_add_f32 v[138:139], v[120:121], v[128:129]
	v_mov_b32_e32 v185, v117
	v_pk_add_f32 v[116:117], v[182:183], v[184:185] neg_lo:[0,1] neg_hi:[0,1]
	v_pk_add_f32 v[120:121], v[120:121], v[128:129] neg_lo:[0,1] neg_hi:[0,1]
	v_pk_mul_f32 v[118:119], v[154:155], v[116:117] op_sel:[1,1] op_sel_hi:[0,1]
	v_pk_fma_f32 v[158:159], v[154:155], v[116:117], v[118:119] neg_lo:[0,0,1] neg_hi:[0,0,1]
	v_pk_fma_f32 v[116:117], v[154:155], v[116:117], v[118:119] op_sel_hi:[1,0,1]
	s_addc_u32 s1, s7, s1
	v_mov_b32_e32 v159, v117
	v_pk_add_f32 v[116:117], v[124:125], v[142:143] neg_lo:[0,1] neg_hi:[0,1]
	v_pk_add_f32 v[124:125], v[124:125], v[142:143]
	s_waitcnt lgkmcnt(2)
	v_pk_mul_f32 v[118:119], v[116:117], v[160:161] op_sel:[1,1] op_sel_hi:[1,0]
	s_lshl_b64 s[2:3], s[90:91], 13
	v_pk_fma_f32 v[186:187], v[116:117], v[160:161], v[118:119] neg_lo:[0,0,1] neg_hi:[0,0,1]
	v_pk_fma_f32 v[116:117], v[116:117], v[160:161], v[118:119] op_sel_hi:[0,1,1]
	v_mov_b32_e32 v187, v117
	v_pk_add_f32 v[116:117], v[132:133], v[150:151] neg_lo:[0,1] neg_hi:[0,1]
	v_pk_add_f32 v[132:133], v[132:133], v[150:151]
	v_pk_mul_f32 v[118:119], v[116:117], v[160:161] op_sel:[1,0] op_sel_hi:[0,0]
	v_pk_fma_f32 v[188:189], v[116:117], v[160:161], v[118:119] op_sel:[0,1,0]
	v_pk_fma_f32 v[116:117], v[116:117], v[160:161], v[118:119] op_sel:[0,1,0] neg_lo:[0,0,1] neg_hi:[0,0,1]
	v_pk_add_f32 v[142:143], v[124:125], v[132:133]
	v_mov_b32_e32 v189, v117
	v_pk_add_f32 v[116:117], v[186:187], v[188:189] neg_lo:[0,1] neg_hi:[0,1]
	v_pk_add_f32 v[146:147], v[138:139], v[142:143]
	s_waitcnt lgkmcnt(1)
	v_pk_mul_f32 v[118:119], v[162:163], v[116:117] op_sel_hi:[0,1]
	v_pk_fma_f32 v[160:161], v[162:163], v[116:117], v[118:119] op_sel:[1,0,1] op_sel_hi:[1,1,0]
	v_pk_fma_f32 v[116:117], v[162:163], v[116:117], v[118:119] op_sel:[1,0,1] op_sel_hi:[1,1,0] neg_lo:[0,0,1] neg_hi:[0,0,1]
	v_pk_add_f32 v[148:149], v[144:145], v[146:147]
	v_mov_b32_e32 v161, v117
	v_pk_add_f32 v[116:117], v[158:159], v[160:161] neg_lo:[0,1] neg_hi:[0,1]
	v_pk_add_f32 v[144:145], v[144:145], v[146:147] neg_lo:[0,1] neg_hi:[0,1]
	v_pk_mul_f32 v[118:119], v[156:157], v[116:117] op_sel_hi:[0,1]
	v_pk_fma_f32 v[190:191], v[156:157], v[116:117], v[118:119] op_sel:[1,0,1] op_sel_hi:[1,1,0]
	v_pk_fma_f32 v[116:117], v[156:157], v[116:117], v[118:119] op_sel:[1,0,1] op_sel_hi:[1,1,0] neg_lo:[0,0,1] neg_hi:[0,0,1]
	s_waitcnt lgkmcnt(0)
	v_xor_b32_e32 v118, 0x80000000, v164
	v_cndmask_b32_e64 v119, v118, v165, s[38:39]
	v_cndmask_b32_e64 v118, v165, v164, s[38:39]
	v_pk_mul_f32 v[146:147], v[144:145], v[118:119] op_sel:[1,1] op_sel_hi:[1,0]
	v_mov_b32_e32 v191, v117
	v_pk_fma_f32 v[150:151], v[144:145], v[118:119], v[146:147] neg_lo:[0,0,1] neg_hi:[0,0,1]
	v_pk_fma_f32 v[144:145], v[144:145], v[118:119], v[146:147] op_sel_hi:[0,1,1]
	v_mov_b32_e32 v151, v145
	v_pk_fma_f32 v[144:145], v[136:137], v[156:157], v[140:141] neg_lo:[0,0,1] neg_hi:[0,0,1]
	v_pk_fma_f32 v[136:137], v[136:137], v[156:157], v[140:141] op_sel_hi:[0,1,1]
	v_mov_b32_e32 v145, v137
	v_pk_add_f32 v[136:137], v[138:139], v[142:143] neg_lo:[0,1] neg_hi:[0,1]
	v_pk_add_f32 v[116:117], v[178:179], v[190:191] neg_lo:[0,1] neg_hi:[0,1]
	v_pk_mul_f32 v[138:139], v[136:137], v[156:157] op_sel_hi:[1,0]
	s_nop 0
	v_pk_fma_f32 v[140:141], v[136:137], v[156:157], v[138:139] op_sel:[0,1,1] op_sel_hi:[1,1,0]
	v_pk_fma_f32 v[136:137], v[136:137], v[156:157], v[138:139] op_sel:[0,1,1] op_sel_hi:[1,1,0] neg_lo:[0,0,1] neg_hi:[0,0,1]
	s_nop 0
	v_mov_b32_e32 v141, v137
	v_pk_add_f32 v[138:139], v[144:145], v[140:141] neg_lo:[0,1] neg_hi:[0,1]
	v_pk_add_f32 v[136:137], v[144:145], v[140:141]
	v_pk_mul_f32 v[140:141], v[118:119], v[138:139] op_sel:[1,1] op_sel_hi:[0,1]
	v_pk_fma_f32 v[142:143], v[118:119], v[138:139], v[140:141] neg_lo:[0,0,1] neg_hi:[0,0,1]
	v_pk_fma_f32 v[138:139], v[118:119], v[138:139], v[140:141] op_sel_hi:[1,0,1]
	s_nop 0
	v_mov_b32_e32 v143, v139
	v_pk_fma_f32 v[138:139], v[110:111], v[152:153], v[126:127] neg_lo:[0,0,1] neg_hi:[0,0,1]
	v_pk_fma_f32 v[110:111], v[110:111], v[152:153], v[126:127] op_sel_hi:[0,1,1]
	v_mov_b32_e32 v139, v111
	v_pk_add_f32 v[110:111], v[122:123], v[130:131] neg_lo:[0,1] neg_hi:[0,1]
	s_nop 0
	v_pk_mul_f32 v[122:123], v[110:111], v[152:153] op_sel_hi:[1,0]
	s_nop 0
	v_pk_fma_f32 v[126:127], v[110:111], v[152:153], v[122:123] op_sel:[0,1,1] op_sel_hi:[1,1,0]
	v_pk_fma_f32 v[110:111], v[110:111], v[152:153], v[122:123] op_sel:[0,1,1] op_sel_hi:[1,1,0] neg_lo:[0,0,1] neg_hi:[0,0,1]
	v_pk_mul_f32 v[122:123], v[120:121], v[154:155] op_sel:[1,1] op_sel_hi:[1,0]
	v_mov_b32_e32 v127, v111
	v_pk_fma_f32 v[128:129], v[120:121], v[154:155], v[122:123] neg_lo:[0,0,1] neg_hi:[0,0,1]
	v_pk_fma_f32 v[120:121], v[120:121], v[154:155], v[122:123] op_sel_hi:[0,1,1]
	v_mov_b32_e32 v129, v121
	v_pk_add_f32 v[120:121], v[124:125], v[132:133] neg_lo:[0,1] neg_hi:[0,1]
	v_pk_add_f32 v[110:111], v[138:139], v[126:127]
	v_pk_mul_f32 v[122:123], v[120:121], v[162:163] op_sel_hi:[1,0]
; template <int R, class XT, class TWT>
; __device__ __forceinline__ void dif_task(XT X, TWT tw, int s, int task) {
;     const int lgM = 13 - s, lgq = lgM - R, q = 1 << lgq;
;     const int j0 = task & (q - 1), blk = task >> lgq, base = (blk << lgM) + j0;
;     const int pb = PADI(base), qp = (q >= 32) ? q + (q >> 4) : q;
;     f32x2v v[1 << R];
; #pragma unroll
;     for (int k = 0; k < (1 << R); ++k) v[k] = X[pb + k * qp];
; #pragma unroll
;     for (int r = 0; r < R; ++r) {
;         const int pb = R - 1 - r;
; #pragma unroll
;         for (int k = 0; k < (1 << R); ++k) if (!((k >> pb) & 1)) {
;             const int klo = k & ((1 << pb) - 1);
;             const f32x2v w = tw[(j0 + (klo << lgq)) << (s + r)];
;             const f32x2v a = v[k], b = v[k + (1 << pb)], d = a - b;
;             v[k] = a + b; v[k + (1 << pb)] = (f32x2v){d.x * w.x - d.y * w.y, d.x * w.y + d.y * w.x};
;         }
;     }
; #pragma unroll
;     for (int k = 0; k < (1 << R); ++k) X[pb + k * qp] = v[k];
; }
	v_pk_add_f32 v[132:133], v[182:183], v[184:185]
	v_pk_fma_f32 v[124:125], v[120:121], v[162:163], v[122:123] op_sel:[0,1,1] op_sel_hi:[1,1,0]
	v_pk_fma_f32 v[120:121], v[120:121], v[162:163], v[122:123] op_sel:[0,1,1] op_sel_hi:[1,1,0] neg_lo:[0,0,1] neg_hi:[0,0,1]
	s_nop 0
	v_mov_b32_e32 v125, v121
	v_pk_add_f32 v[120:121], v[128:129], v[124:125]
	s_nop 0
	v_pk_add_f32 v[122:123], v[110:111], v[120:121]
	v_pk_add_f32 v[110:111], v[110:111], v[120:121] neg_lo:[0,1] neg_hi:[0,1]
	s_nop 0
	v_pk_mul_f32 v[120:121], v[118:119], v[110:111] op_sel:[1,1] op_sel_hi:[0,1]
	v_pk_fma_f32 v[130:131], v[118:119], v[110:111], v[120:121] neg_lo:[0,0,1] neg_hi:[0,0,1]
	v_pk_fma_f32 v[110:111], v[118:119], v[110:111], v[120:121] op_sel_hi:[1,0,1]
	s_nop 0
	v_mov_b32_e32 v131, v111
	v_pk_add_f32 v[110:111], v[138:139], v[126:127] neg_lo:[0,1] neg_hi:[0,1]
	v_pk_add_f32 v[138:139], v[186:187], v[188:189]
	v_pk_mul_f32 v[120:121], v[156:157], v[110:111] op_sel:[1,1] op_sel_hi:[0,1]
	v_pk_fma_f32 v[126:127], v[156:157], v[110:111], v[120:121] neg_lo:[0,0,1] neg_hi:[0,0,1]
	v_pk_fma_f32 v[110:111], v[156:157], v[110:111], v[120:121] op_sel_hi:[1,0,1]
	v_pk_add_f32 v[140:141], v[132:133], v[138:139]
	v_mov_b32_e32 v127, v111
	v_pk_add_f32 v[110:111], v[128:129], v[124:125] neg_lo:[0,1] neg_hi:[0,1]
	s_nop 0
	v_pk_mul_f32 v[120:121], v[156:157], v[110:111] op_sel_hi:[0,1]
	v_pk_fma_f32 v[124:125], v[156:157], v[110:111], v[120:121] op_sel:[1,0,1] op_sel_hi:[1,1,0]
	v_pk_fma_f32 v[110:111], v[156:157], v[110:111], v[120:121] op_sel:[1,0,1] op_sel_hi:[1,1,0] neg_lo:[0,0,1] neg_hi:[0,0,1]
	s_nop 0
	v_mov_b32_e32 v125, v111
	v_pk_add_f32 v[120:121], v[126:127], v[124:125] neg_lo:[0,1] neg_hi:[0,1]
	v_pk_add_f32 v[110:111], v[126:127], v[124:125]
	v_pk_mul_f32 v[124:125], v[118:119], v[120:121] op_sel:[1,1] op_sel_hi:[0,1]
	v_pk_fma_f32 v[126:127], v[118:119], v[120:121], v[124:125] neg_lo:[0,0,1] neg_hi:[0,0,1]
	v_pk_fma_f32 v[120:121], v[118:119], v[120:121], v[124:125] op_sel_hi:[1,0,1]
	v_pk_add_f32 v[124:125], v[174:175], v[176:177]
	v_mov_b32_e32 v127, v121
	v_pk_add_f32 v[120:121], v[170:171], v[172:173]
	s_nop 0
	v_pk_add_f32 v[128:129], v[120:121], v[124:125]
	v_pk_add_f32 v[120:121], v[120:121], v[124:125] neg_lo:[0,1] neg_hi:[0,1]
	v_pk_add_f32 v[144:145], v[128:129], v[140:141]
	v_pk_add_f32 v[128:129], v[128:129], v[140:141] neg_lo:[0,1] neg_hi:[0,1]
	v_pk_mul_f32 v[124:125], v[156:157], v[120:121] op_sel:[1,1] op_sel_hi:[0,1]
	v_pk_mul_f32 v[140:141], v[128:129], v[118:119] op_sel:[1,1] op_sel_hi:[1,0]
	s_nop 0
	v_pk_fma_f32 v[146:147], v[128:129], v[118:119], v[140:141] neg_lo:[0,0,1] neg_hi:[0,0,1]
	v_pk_fma_f32 v[128:129], v[128:129], v[118:119], v[140:141] op_sel_hi:[0,1,1]
	v_mov_b32_e32 v147, v129
	v_pk_fma_f32 v[128:129], v[156:157], v[120:121], v[124:125] neg_lo:[0,0,1] neg_hi:[0,0,1]
	v_pk_fma_f32 v[120:121], v[156:157], v[120:121], v[124:125] op_sel_hi:[1,0,1]
	s_nop 0
	v_mov_b32_e32 v129, v121
	v_pk_add_f32 v[120:121], v[132:133], v[138:139] neg_lo:[0,1] neg_hi:[0,1]
	s_nop 0
	v_pk_mul_f32 v[124:125], v[156:157], v[120:121] op_sel_hi:[0,1]
	v_pk_fma_f32 v[132:133], v[156:157], v[120:121], v[124:125] op_sel:[1,0,1] op_sel_hi:[1,1,0]
	v_pk_fma_f32 v[120:121], v[156:157], v[120:121], v[124:125] op_sel:[1,0,1] op_sel_hi:[1,1,0] neg_lo:[0,0,1] neg_hi:[0,0,1]
	s_nop 0
	v_mov_b32_e32 v133, v121
	v_pk_add_f32 v[124:125], v[128:129], v[132:133] neg_lo:[0,1] neg_hi:[0,1]
	v_pk_add_f32 v[120:121], v[128:129], v[132:133]
	v_pk_mul_f32 v[128:129], v[118:119], v[124:125] op_sel:[1,1] op_sel_hi:[0,1]
	v_pk_fma_f32 v[132:133], v[118:119], v[124:125], v[128:129] neg_lo:[0,0,1] neg_hi:[0,0,1]
	v_pk_fma_f32 v[124:125], v[118:119], v[124:125], v[128:129] op_sel_hi:[1,0,1]
	v_pk_add_f32 v[128:129], v[158:159], v[160:161]
	v_mov_b32_e32 v133, v125
	v_pk_add_f32 v[124:125], v[168:169], v[166:167]
	s_nop 0
	v_pk_add_f32 v[138:139], v[124:125], v[128:129]
	v_pk_add_f32 v[124:125], v[124:125], v[128:129] neg_lo:[0,1] neg_hi:[0,1]
	s_nop 0
	v_pk_mul_f32 v[128:129], v[118:119], v[124:125] op_sel:[1,1] op_sel_hi:[0,1]
	v_pk_fma_f32 v[140:141], v[118:119], v[124:125], v[128:129] neg_lo:[0,0,1] neg_hi:[0,0,1]
	v_pk_fma_f32 v[124:125], v[118:119], v[124:125], v[128:129] op_sel_hi:[1,0,1]
	v_pk_mul_f32 v[128:129], v[118:119], v[116:117] op_sel:[1,1] op_sel_hi:[0,1]
	v_pk_fma_f32 v[152:153], v[118:119], v[116:117], v[128:129] neg_lo:[0,0,1] neg_hi:[0,0,1]
	v_pk_fma_f32 v[116:117], v[118:119], v[116:117], v[128:129] op_sel_hi:[1,0,1]
	v_mov_b32_e32 v141, v125
	v_pk_add_f32 v[124:125], v[178:179], v[190:191]
	v_mov_b32_e32 v153, v117
	ds_write_b64 v75, v[148:149]
	ds_write_b64 v75, v[150:151] offset:4352
	ds_write_b64 v75, v[136:137] offset:8704
	ds_write_b64 v75, v[142:143] offset:13056
	ds_write_b64 v75, v[122:123] offset:17408
	ds_write_b64 v75, v[130:131] offset:21760
	ds_write_b64 v75, v[110:111] offset:26112
	ds_write_b64 v75, v[126:127] offset:30464
	ds_write_b64 v75, v[144:145] offset:34816
	ds_write_b64 v75, v[146:147] offset:39168
	ds_write_b64 v75, v[120:121] offset:43520
	ds_write_b64 v75, v[132:133] offset:47872
	ds_write_b64 v75, v[138:139] offset:52224
	ds_write_b64 v75, v[140:141] offset:56576
	ds_write_b64 v75, v[124:125] offset:60928
	ds_write_b64 v75, v[152:153] offset:65280
	s_waitcnt lgkmcnt(0)
	s_barrier
; #define LAS __attribute__((address_space(3)))
; __device__ __forceinline__ void lds_barrier() { asm volatile("s_waitcnt lgkmcnt(0)" ::: "memory"); __builtin_amdgcn_s_barrier(); asm volatile("" ::: "memory"); }
; template <int R, class XT, class TWT>
; __device__ __forceinline__ void dif_task(XT X, TWT tw, int s, int task) {
;     const int lgM = 13 - s, lgq = lgM - R, q = 1 << lgq;
;     const int j0 = task & (q - 1), blk = task >> lgq, base = (blk << lgM) + j0;
;     const int pb = PADI(base), qp = (q >= 32) ? q + (q >> 4) : q;
;     f32x2v v[1 << R];
; #pragma unroll
;     for (int k = 0; k < (1 << R); ++k) v[k] = X[pb + k * qp];
; #pragma unroll
;     for (int r = 0; r < R; ++r) {
;         const int pb = R - 1 - r;
; #pragma unroll
;         for (int k = 0; k < (1 << R); ++k) if (!((k >> pb) & 1)) {
;             const int klo = k & ((1 << pb) - 1);
;             const f32x2v w = tw[(j0 + (klo << lgq)) << (s + r)];
;             const f32x2v a = v[k], b = v[k + (1 << pb)], d = a - b;
;             v[k] = a + b; v[k + (1 << pb)] = (f32x2v){d.x * w.x - d.y * w.y, d.x * w.y + d.y * w.x};
;         }
;     }
; #pragma unroll
;     for (int k = 0; k < (1 << R); ++k) X[pb + k * qp] = v[k];
; }
; __device__ __forceinline__ void fft_fwd_upper(LAS f32x2v* X, TwHalf tw, int s0, int tid) {
;     if (s0 == 0) { dif_task<4>(X, tw, 0, tid); lds_barrier(); }
;     dif_task<4>(X, tw, 4, tid); lds_barrier();
;     dif_task<4>(X, tw, 8, tid); lds_barrier();
; }
	ds_read2_b64 v[116:119], v81 offset1:34
	ds_read2_b64 v[120:123], v81 offset0:68 offset1:102
	ds_read2_b64 v[124:127], v81 offset0:136 offset1:170
	ds_read2_b64 v[128:131], v81 offset0:204 offset1:238
	v_add_u32_e32 v110, 0x800, v81
	ds_read2_b64 v[136:139], v110 offset0:16 offset1:50
	ds_read2_b64 v[140:143], v110 offset0:84 offset1:118
	ds_read2_b64 v[144:147], v110 offset0:152 offset1:186
	ds_read2_b64 v[148:151], v110 offset0:220 offset1:254
	ds_read2st64_b64 v[152:155], v94 offset1:16
	ds_read_b64 v[132:133], v97
	ds_read_b64 v[156:157], v98
	ds_read_b64 v[158:159], v99
	ds_read_b64 v[160:161], v95
	ds_read_b64 v[162:163], v96
	ds_read_b64 v[164:165], v82
	ds_read_b64 v[166:167], v83
	s_waitcnt lgkmcnt(11)
	v_pk_add_f32 v[168:169], v[116:117], v[136:137] neg_lo:[0,1] neg_hi:[0,1]
	v_pk_add_f32 v[116:117], v[116:117], v[136:137]
	s_waitcnt lgkmcnt(7)
	v_pk_mul_f32 v[170:171], v[168:169], v[152:153] op_sel:[1,1] op_sel_hi:[1,0]
	s_waitcnt lgkmcnt(0)
	v_xor_b32_e32 v111, 0x80000000, v166
	v_pk_fma_f32 v[172:173], v[168:169], v[152:153], v[170:171] neg_lo:[0,0,1] neg_hi:[0,0,1]
	v_pk_fma_f32 v[168:169], v[168:169], v[152:153], v[170:171] op_sel_hi:[0,1,1]
	v_mov_b32_e32 v173, v169
	v_pk_add_f32 v[168:169], v[124:125], v[144:145] neg_lo:[0,1] neg_hi:[0,1]
	v_pk_add_f32 v[124:125], v[124:125], v[144:145]
	v_pk_mul_f32 v[170:171], v[168:169], v[152:153] op_sel:[1,0] op_sel_hi:[0,0]
	v_pk_fma_f32 v[174:175], v[168:169], v[152:153], v[170:171] op_sel:[0,1,0]
	v_pk_fma_f32 v[152:153], v[168:169], v[152:153], v[170:171] op_sel:[0,1,0] neg_lo:[0,0,1] neg_hi:[0,0,1]
	v_pk_add_f32 v[136:137], v[116:117], v[124:125]
	v_mov_b32_e32 v175, v153
	v_pk_add_f32 v[152:153], v[172:173], v[174:175] neg_lo:[0,1] neg_hi:[0,1]
	v_pk_add_f32 v[116:117], v[116:117], v[124:125] neg_lo:[0,1] neg_hi:[0,1]
	v_pk_mul_f32 v[168:169], v[132:133], v[152:153] op_sel:[1,1] op_sel_hi:[0,1]
	v_pk_fma_f32 v[170:171], v[132:133], v[152:153], v[168:169] neg_lo:[0,0,1] neg_hi:[0,0,1]
	v_pk_fma_f32 v[152:153], v[132:133], v[152:153], v[168:169] op_sel_hi:[1,0,1]
	v_pk_mul_f32 v[124:125], v[116:117], v[132:133] op_sel:[1,1] op_sel_hi:[1,0]
	v_mov_b32_e32 v171, v153
	v_pk_add_f32 v[152:153], v[120:121], v[140:141] neg_lo:[0,1] neg_hi:[0,1]
	v_pk_add_f32 v[120:121], v[120:121], v[140:141]
	v_pk_mul_f32 v[168:169], v[152:153], v[154:155] op_sel:[1,1] op_sel_hi:[1,0]
	s_nop 0
	v_pk_fma_f32 v[176:177], v[152:153], v[154:155], v[168:169] neg_lo:[0,0,1] neg_hi:[0,0,1]
	v_pk_fma_f32 v[152:153], v[152:153], v[154:155], v[168:169] op_sel_hi:[0,1,1]
	v_mov_b32_e32 v177, v153
	v_pk_add_f32 v[152:153], v[128:129], v[148:149] neg_lo:[0,1] neg_hi:[0,1]
	v_pk_add_f32 v[128:129], v[128:129], v[148:149]
	v_pk_mul_f32 v[168:169], v[152:153], v[154:155] op_sel:[1,0] op_sel_hi:[0,0]
	v_pk_fma_f32 v[178:179], v[152:153], v[154:155], v[168:169] op_sel:[0,1,0]
	v_pk_fma_f32 v[152:153], v[152:153], v[154:155], v[168:169] op_sel:[0,1,0] neg_lo:[0,0,1] neg_hi:[0,0,1]
	v_pk_add_f32 v[140:141], v[120:121], v[128:129]
	v_mov_b32_e32 v179, v153
	v_pk_add_f32 v[152:153], v[176:177], v[178:179] neg_lo:[0,1] neg_hi:[0,1]
	v_pk_add_f32 v[144:145], v[136:137], v[140:141]
	v_pk_mul_f32 v[154:155], v[132:133], v[152:153] op_sel_hi:[0,1]
	v_pk_fma_f32 v[168:169], v[132:133], v[152:153], v[154:155] op_sel:[1,0,1] op_sel_hi:[1,1,0]
	v_pk_fma_f32 v[152:153], v[132:133], v[152:153], v[154:155] op_sel:[1,0,1] op_sel_hi:[1,1,0] neg_lo:[0,0,1] neg_hi:[0,0,1]
	v_pk_add_f32 v[136:137], v[136:137], v[140:141] neg_lo:[0,1] neg_hi:[0,1]
	v_mov_b32_e32 v169, v153
	v_pk_add_f32 v[152:153], v[170:171], v[168:169] neg_lo:[0,1] neg_hi:[0,1]
	v_pk_mul_f32 v[140:141], v[136:137], v[158:159] op_sel:[1,1] op_sel_hi:[1,0]
	v_pk_mul_f32 v[154:155], v[158:159], v[152:153] op_sel:[1,1] op_sel_hi:[0,1]
	v_pk_fma_f32 v[182:183], v[158:159], v[152:153], v[154:155] neg_lo:[0,0,1] neg_hi:[0,0,1]
	v_pk_fma_f32 v[152:153], v[158:159], v[152:153], v[154:155] op_sel_hi:[1,0,1]
	s_nop 0
	v_mov_b32_e32 v183, v153
	v_pk_add_f32 v[152:153], v[118:119], v[138:139] neg_lo:[0,1] neg_hi:[0,1]
	v_pk_add_f32 v[118:119], v[118:119], v[138:139]
	v_pk_mul_f32 v[154:155], v[152:153], v[160:161] op_sel:[1,1] op_sel_hi:[1,0]
	s_nop 0
	v_pk_fma_f32 v[184:185], v[152:153], v[160:161], v[154:155] neg_lo:[0,0,1] neg_hi:[0,0,1]
	v_pk_fma_f32 v[152:153], v[152:153], v[160:161], v[154:155] op_sel_hi:[0,1,1]
	v_mov_b32_e32 v185, v153
	v_pk_add_f32 v[152:153], v[126:127], v[146:147] neg_lo:[0,1] neg_hi:[0,1]
	v_pk_add_f32 v[126:127], v[126:127], v[146:147]
	v_pk_mul_f32 v[154:155], v[152:153], v[160:161] op_sel:[1,0] op_sel_hi:[0,0]
	v_pk_fma_f32 v[186:187], v[152:153], v[160:161], v[154:155] op_sel:[0,1,0]
	v_pk_fma_f32 v[152:153], v[152:153], v[160:161], v[154:155] op_sel:[0,1,0] neg_lo:[0,0,1] neg_hi:[0,0,1]
	v_pk_add_f32 v[138:139], v[118:119], v[126:127]
	v_mov_b32_e32 v187, v153
	v_pk_add_f32 v[152:153], v[184:185], v[186:187] neg_lo:[0,1] neg_hi:[0,1]
	v_pk_add_f32 v[118:119], v[118:119], v[126:127] neg_lo:[0,1] neg_hi:[0,1]
	v_pk_mul_f32 v[154:155], v[156:157], v[152:153] op_sel:[1,1] op_sel_hi:[0,1]
	v_pk_fma_f32 v[160:161], v[156:157], v[152:153], v[154:155] neg_lo:[0,0,1] neg_hi:[0,0,1]
	v_pk_fma_f32 v[152:153], v[156:157], v[152:153], v[154:155] op_sel_hi:[1,0,1]
	s_nop 0
	v_mov_b32_e32 v161, v153
	v_pk_add_f32 v[152:153], v[122:123], v[142:143] neg_lo:[0,1] neg_hi:[0,1]
	v_pk_add_f32 v[122:123], v[122:123], v[142:143]
	v_pk_mul_f32 v[154:155], v[152:153], v[162:163] op_sel:[1,1] op_sel_hi:[1,0]
	s_nop 0
	v_pk_fma_f32 v[188:189], v[152:153], v[162:163], v[154:155] neg_lo:[0,0,1] neg_hi:[0,0,1]
	v_pk_fma_f32 v[152:153], v[152:153], v[162:163], v[154:155] op_sel_hi:[0,1,1]
; template <int R, class XT, class TWT>
; __device__ __forceinline__ void dif_task(XT X, TWT tw, int s, int task) {
;     const int lgM = 13 - s, lgq = lgM - R, q = 1 << lgq;
;     const int j0 = task & (q - 1), blk = task >> lgq, base = (blk << lgM) + j0;
;     const int pb = PADI(base), qp = (q >= 32) ? q + (q >> 4) : q;
;     f32x2v v[1 << R];
; #pragma unroll
;     for (int k = 0; k < (1 << R); ++k) v[k] = X[pb + k * qp];
; #pragma unroll
;     for (int r = 0; r < R; ++r) {
;         const int pb = R - 1 - r;
; #pragma unroll
;         for (int k = 0; k < (1 << R); ++k) if (!((k >> pb) & 1)) {
;             const int klo = k & ((1 << pb) - 1);
;             const f32x2v w = tw[(j0 + (klo << lgq)) << (s + r)];
;             const f32x2v a = v[k], b = v[k + (1 << pb)], d = a - b;
;             v[k] = a + b; v[k + (1 << pb)] = (f32x2v){d.x * w.x - d.y * w.y, d.x * w.y + d.y * w.x};
;         }
;     }
; #pragma unroll
;     for (int k = 0; k < (1 << R); ++k) X[pb + k * qp] = v[k];
; }
	v_mov_b32_e32 v189, v153
	v_pk_add_f32 v[152:153], v[130:131], v[150:151] neg_lo:[0,1] neg_hi:[0,1]
	v_pk_add_f32 v[130:131], v[130:131], v[150:151]
	v_pk_mul_f32 v[154:155], v[152:153], v[162:163] op_sel:[1,0] op_sel_hi:[0,0]
	v_pk_fma_f32 v[190:191], v[152:153], v[162:163], v[154:155] op_sel:[0,1,0]
	v_pk_fma_f32 v[152:153], v[152:153], v[162:163], v[154:155] op_sel:[0,1,0] neg_lo:[0,0,1] neg_hi:[0,0,1]
	v_pk_add_f32 v[142:143], v[122:123], v[130:131]
	v_mov_b32_e32 v191, v153
	v_pk_add_f32 v[152:153], v[188:189], v[190:191] neg_lo:[0,1] neg_hi:[0,1]
	v_pk_add_f32 v[146:147], v[138:139], v[142:143]
	v_pk_mul_f32 v[154:155], v[164:165], v[152:153] op_sel_hi:[0,1]
	v_pk_fma_f32 v[162:163], v[164:165], v[152:153], v[154:155] op_sel:[1,0,1] op_sel_hi:[1,1,0]
	v_pk_fma_f32 v[152:153], v[164:165], v[152:153], v[154:155] op_sel:[1,0,1] op_sel_hi:[1,1,0] neg_lo:[0,0,1] neg_hi:[0,0,1]
	v_pk_add_f32 v[148:149], v[144:145], v[146:147]
	v_mov_b32_e32 v163, v153
	v_pk_add_f32 v[152:153], v[160:161], v[162:163] neg_lo:[0,1] neg_hi:[0,1]
	v_pk_add_f32 v[144:145], v[144:145], v[146:147] neg_lo:[0,1] neg_hi:[0,1]
	v_pk_mul_f32 v[154:155], v[158:159], v[152:153] op_sel_hi:[0,1]
	v_pk_fma_f32 v[192:193], v[158:159], v[152:153], v[154:155] op_sel:[1,0,1] op_sel_hi:[1,1,0]
	v_pk_fma_f32 v[152:153], v[158:159], v[152:153], v[154:155] op_sel:[1,0,1] op_sel_hi:[1,1,0] neg_lo:[0,0,1] neg_hi:[0,0,1]
	v_cndmask_b32_e64 v155, v111, v167, s[40:41]
	v_cndmask_b32_e64 v154, v167, v166, s[40:41]
	v_pk_mul_f32 v[146:147], v[144:145], v[154:155] op_sel:[1,1] op_sel_hi:[1,0]
	v_mov_b32_e32 v193, v153
	v_pk_fma_f32 v[150:151], v[144:145], v[154:155], v[146:147] neg_lo:[0,0,1] neg_hi:[0,0,1]
	v_pk_fma_f32 v[144:145], v[144:145], v[154:155], v[146:147] op_sel_hi:[0,1,1]
	v_mov_b32_e32 v151, v145
	v_pk_fma_f32 v[144:145], v[136:137], v[158:159], v[140:141] neg_lo:[0,0,1] neg_hi:[0,0,1]
	v_pk_fma_f32 v[136:137], v[136:137], v[158:159], v[140:141] op_sel_hi:[0,1,1]
	v_mov_b32_e32 v145, v137
	v_pk_add_f32 v[136:137], v[138:139], v[142:143] neg_lo:[0,1] neg_hi:[0,1]
	v_pk_add_f32 v[152:153], v[182:183], v[192:193] neg_lo:[0,1] neg_hi:[0,1]
	v_pk_mul_f32 v[138:139], v[136:137], v[158:159] op_sel_hi:[1,0]
	v_mov_b32_e32 v111, s16
	v_pk_fma_f32 v[140:141], v[136:137], v[158:159], v[138:139] op_sel:[0,1,1] op_sel_hi:[1,1,0]
	v_pk_fma_f32 v[136:137], v[136:137], v[158:159], v[138:139] op_sel:[0,1,1] op_sel_hi:[1,1,0] neg_lo:[0,0,1] neg_hi:[0,0,1]
	s_nop 0
	v_mov_b32_e32 v141, v137
	v_pk_add_f32 v[138:139], v[144:145], v[140:141] neg_lo:[0,1] neg_hi:[0,1]
	v_pk_add_f32 v[136:137], v[144:145], v[140:141]
	v_pk_mul_f32 v[140:141], v[154:155], v[138:139] op_sel:[1,1] op_sel_hi:[0,1]
	v_pk_fma_f32 v[142:143], v[154:155], v[138:139], v[140:141] neg_lo:[0,0,1] neg_hi:[0,0,1]
	v_pk_fma_f32 v[138:139], v[154:155], v[138:139], v[140:141] op_sel_hi:[1,0,1]
	s_nop 0
	v_mov_b32_e32 v143, v139
	v_pk_fma_f32 v[138:139], v[116:117], v[132:133], v[124:125] neg_lo:[0,0,1] neg_hi:[0,0,1]
	v_pk_fma_f32 v[116:117], v[116:117], v[132:133], v[124:125] op_sel_hi:[0,1,1]
	v_mov_b32_e32 v139, v117
	v_pk_add_f32 v[116:117], v[120:121], v[128:129] neg_lo:[0,1] neg_hi:[0,1]
	s_nop 0
	v_pk_mul_f32 v[120:121], v[116:117], v[132:133] op_sel_hi:[1,0]
	s_nop 0
	v_pk_fma_f32 v[124:125], v[116:117], v[132:133], v[120:121] op_sel:[0,1,1] op_sel_hi:[1,1,0]
	v_pk_fma_f32 v[116:117], v[116:117], v[132:133], v[120:121] op_sel:[0,1,1] op_sel_hi:[1,1,0] neg_lo:[0,0,1] neg_hi:[0,0,1]
	v_pk_mul_f32 v[120:121], v[118:119], v[156:157] op_sel:[1,1] op_sel_hi:[1,0]
	v_mov_b32_e32 v125, v117
	v_pk_fma_f32 v[126:127], v[118:119], v[156:157], v[120:121] neg_lo:[0,0,1] neg_hi:[0,0,1]
	v_pk_fma_f32 v[118:119], v[118:119], v[156:157], v[120:121] op_sel_hi:[0,1,1]
	v_mov_b32_e32 v127, v119
	v_pk_add_f32 v[118:119], v[122:123], v[130:131] neg_lo:[0,1] neg_hi:[0,1]
	v_pk_add_f32 v[116:117], v[138:139], v[124:125]
	v_pk_mul_f32 v[120:121], v[118:119], v[164:165] op_sel_hi:[1,0]
	v_pk_add_f32 v[130:131], v[184:185], v[186:187]
	v_pk_fma_f32 v[122:123], v[118:119], v[164:165], v[120:121] op_sel:[0,1,1] op_sel_hi:[1,1,0]
	v_pk_fma_f32 v[118:119], v[118:119], v[164:165], v[120:121] op_sel:[0,1,1] op_sel_hi:[1,1,0] neg_lo:[0,0,1] neg_hi:[0,0,1]
	v_pk_add_f32 v[132:133], v[188:189], v[190:191]
	v_mov_b32_e32 v123, v119
	v_pk_add_f32 v[118:119], v[126:127], v[122:123]
	s_nop 0
	v_pk_add_f32 v[120:121], v[116:117], v[118:119]
	v_pk_add_f32 v[116:117], v[116:117], v[118:119] neg_lo:[0,1] neg_hi:[0,1]
	s_nop 0
	v_pk_mul_f32 v[118:119], v[154:155], v[116:117] op_sel:[1,1] op_sel_hi:[0,1]
	v_pk_fma_f32 v[128:129], v[154:155], v[116:117], v[118:119] neg_lo:[0,0,1] neg_hi:[0,0,1]
	v_pk_fma_f32 v[116:117], v[154:155], v[116:117], v[118:119] op_sel_hi:[1,0,1]
	s_nop 0
	v_mov_b32_e32 v129, v117
	v_pk_add_f32 v[116:117], v[138:139], v[124:125] neg_lo:[0,1] neg_hi:[0,1]
	v_pk_add_f32 v[138:139], v[130:131], v[132:133]
	v_pk_mul_f32 v[118:119], v[158:159], v[116:117] op_sel:[1,1] op_sel_hi:[0,1]
	v_pk_fma_f32 v[124:125], v[158:159], v[116:117], v[118:119] neg_lo:[0,0,1] neg_hi:[0,0,1]
	v_pk_fma_f32 v[116:117], v[158:159], v[116:117], v[118:119] op_sel_hi:[1,0,1]
	s_nop 0
	v_mov_b32_e32 v125, v117
	v_pk_add_f32 v[116:117], v[126:127], v[122:123] neg_lo:[0,1] neg_hi:[0,1]
	s_nop 0
	v_pk_mul_f32 v[118:119], v[158:159], v[116:117] op_sel_hi:[0,1]
	v_pk_fma_f32 v[122:123], v[158:159], v[116:117], v[118:119] op_sel:[1,0,1] op_sel_hi:[1,1,0]
	v_pk_fma_f32 v[116:117], v[158:159], v[116:117], v[118:119] op_sel:[1,0,1] op_sel_hi:[1,1,0] neg_lo:[0,0,1] neg_hi:[0,0,1]
	s_nop 0
	v_mov_b32_e32 v123, v117
	v_pk_add_f32 v[118:119], v[124:125], v[122:123] neg_lo:[0,1] neg_hi:[0,1]
; #define LAS __attribute__((address_space(3)))
; __device__ __forceinline__ void lds_barrier() { asm volatile("s_waitcnt lgkmcnt(0)" ::: "memory"); __builtin_amdgcn_s_barrier(); asm volatile("" ::: "memory"); }
; template <int R, class XT, class TWT>
; __device__ __forceinline__ void dif_task(XT X, TWT tw, int s, int task) {
;     const int lgM = 13 - s, lgq = lgM - R, q = 1 << lgq;
;     const int j0 = task & (q - 1), blk = task >> lgq, base = (blk << lgM) + j0;
;     const int pb = PADI(base), qp = (q >= 32) ? q + (q >> 4) : q;
;     f32x2v v[1 << R];
; #pragma unroll
;     for (int k = 0; k < (1 << R); ++k) v[k] = X[pb + k * qp];
; #pragma unroll
;     for (int r = 0; r < R; ++r) {
;         const int pb = R - 1 - r;
; #pragma unroll
;         for (int k = 0; k < (1 << R); ++k) if (!((k >> pb) & 1)) {
;             const int klo = k & ((1 << pb) - 1);
;             const f32x2v w = tw[(j0 + (klo << lgq)) << (s + r)];
;             const f32x2v a = v[k], b = v[k + (1 << pb)], d = a - b;
;             v[k] = a + b; v[k + (1 << pb)] = (f32x2v){d.x * w.x - d.y * w.y, d.x * w.y + d.y * w.x};
;         }
;     }
; #pragma unroll
;     for (int k = 0; k < (1 << R); ++k) X[pb + k * qp] = v[k];
; }
; __device__ __forceinline__ void fft_fwd_upper(LAS f32x2v* X, TwHalf tw, int s0, int tid) {
;     if (s0 == 0) { dif_task<4>(X, tw, 0, tid); lds_barrier(); }
;     dif_task<4>(X, tw, 4, tid); lds_barrier();
;     dif_task<4>(X, tw, 8, tid); lds_barrier();
; }
	v_pk_add_f32 v[116:117], v[124:125], v[122:123]
	v_pk_mul_f32 v[122:123], v[154:155], v[118:119] op_sel:[1,1] op_sel_hi:[0,1]
	v_pk_fma_f32 v[124:125], v[154:155], v[118:119], v[122:123] neg_lo:[0,0,1] neg_hi:[0,0,1]
	v_pk_fma_f32 v[118:119], v[154:155], v[118:119], v[122:123] op_sel_hi:[1,0,1]
	v_pk_add_f32 v[122:123], v[176:177], v[178:179]
	v_mov_b32_e32 v125, v119
	v_pk_add_f32 v[118:119], v[172:173], v[174:175]
	s_nop 0
	v_pk_add_f32 v[126:127], v[118:119], v[122:123]
	v_pk_add_f32 v[118:119], v[118:119], v[122:123] neg_lo:[0,1] neg_hi:[0,1]
	v_pk_add_f32 v[140:141], v[126:127], v[138:139]
	v_pk_add_f32 v[126:127], v[126:127], v[138:139] neg_lo:[0,1] neg_hi:[0,1]
	v_pk_mul_f32 v[122:123], v[158:159], v[118:119] op_sel:[1,1] op_sel_hi:[0,1]
	v_pk_mul_f32 v[138:139], v[126:127], v[154:155] op_sel:[1,1] op_sel_hi:[1,0]
	s_nop 0
	v_pk_fma_f32 v[144:145], v[126:127], v[154:155], v[138:139] neg_lo:[0,0,1] neg_hi:[0,0,1]
	v_pk_fma_f32 v[126:127], v[126:127], v[154:155], v[138:139] op_sel_hi:[0,1,1]
	v_mov_b32_e32 v145, v127
	v_pk_fma_f32 v[126:127], v[158:159], v[118:119], v[122:123] neg_lo:[0,0,1] neg_hi:[0,0,1]
	v_pk_fma_f32 v[118:119], v[158:159], v[118:119], v[122:123] op_sel_hi:[1,0,1]
	s_nop 0
	v_mov_b32_e32 v127, v119
	v_pk_add_f32 v[118:119], v[130:131], v[132:133] neg_lo:[0,1] neg_hi:[0,1]
	s_nop 0
	v_pk_mul_f32 v[122:123], v[158:159], v[118:119] op_sel_hi:[0,1]
	v_pk_fma_f32 v[130:131], v[158:159], v[118:119], v[122:123] op_sel:[1,0,1] op_sel_hi:[1,1,0]
	v_pk_fma_f32 v[118:119], v[158:159], v[118:119], v[122:123] op_sel:[1,0,1] op_sel_hi:[1,1,0] neg_lo:[0,0,1] neg_hi:[0,0,1]
	s_nop 0
	v_mov_b32_e32 v131, v119
	v_pk_add_f32 v[122:123], v[126:127], v[130:131] neg_lo:[0,1] neg_hi:[0,1]
	v_pk_add_f32 v[118:119], v[126:127], v[130:131]
	v_pk_mul_f32 v[126:127], v[154:155], v[122:123] op_sel:[1,1] op_sel_hi:[0,1]
	v_pk_fma_f32 v[130:131], v[154:155], v[122:123], v[126:127] neg_lo:[0,0,1] neg_hi:[0,0,1]
	v_pk_fma_f32 v[122:123], v[154:155], v[122:123], v[126:127] op_sel_hi:[1,0,1]
	v_pk_add_f32 v[126:127], v[160:161], v[162:163]
	v_mov_b32_e32 v131, v123
	v_pk_add_f32 v[122:123], v[170:171], v[168:169]
	s_nop 0
	v_pk_add_f32 v[132:133], v[122:123], v[126:127]
	v_pk_add_f32 v[122:123], v[122:123], v[126:127] neg_lo:[0,1] neg_hi:[0,1]
	s_nop 0
	v_pk_mul_f32 v[126:127], v[154:155], v[122:123] op_sel:[1,1] op_sel_hi:[0,1]
	v_pk_fma_f32 v[138:139], v[154:155], v[122:123], v[126:127] neg_lo:[0,0,1] neg_hi:[0,0,1]
	v_pk_fma_f32 v[122:123], v[154:155], v[122:123], v[126:127] op_sel_hi:[1,0,1]
	v_pk_mul_f32 v[126:127], v[154:155], v[152:153] op_sel:[1,1] op_sel_hi:[0,1]
	v_pk_fma_f32 v[146:147], v[154:155], v[152:153], v[126:127] neg_lo:[0,0,1] neg_hi:[0,0,1]
	v_pk_fma_f32 v[126:127], v[154:155], v[152:153], v[126:127] op_sel_hi:[1,0,1]
	v_mov_b32_e32 v139, v123
	v_pk_add_f32 v[122:123], v[182:183], v[192:193]
	v_mov_b32_e32 v147, v127
	ds_write2_b64 v81, v[148:149], v[150:151] offset1:34
	ds_write2_b64 v81, v[136:137], v[142:143] offset0:68 offset1:102
	ds_write2_b64 v81, v[120:121], v[128:129] offset0:136 offset1:170
	ds_write2_b64 v81, v[116:117], v[124:125] offset0:204 offset1:238
	ds_write2_b64 v110, v[140:141], v[144:145] offset0:16 offset1:50
	ds_write2_b64 v110, v[118:119], v[130:131] offset0:84 offset1:118
	ds_write2_b64 v110, v[132:133], v[138:139] offset0:152 offset1:186
	ds_write2_b64 v110, v[122:123], v[146:147] offset0:220 offset1:254
	s_waitcnt lgkmcnt(0)
	s_barrier
	ds_read2_b64 v[116:119], v84 offset1:2
	ds_read2_b64 v[120:123], v84 offset0:4 offset1:6
	ds_read2_b64 v[124:127], v84 offset0:8 offset1:10
	ds_read2_b64 v[128:131], v84 offset0:12 offset1:14
	ds_read2_b64 v[136:139], v84 offset0:16 offset1:18
	ds_read2_b64 v[140:143], v84 offset0:20 offset1:22
	ds_read2_b64 v[144:147], v84 offset0:24 offset1:26
	ds_read2_b64 v[148:151], v84 offset0:28 offset1:30
	ds_read2st64_b64 v[152:155], v100 offset1:16
	ds_read_b64 v[132:133], v101
	ds_read_b64 v[156:157], v102
	ds_read_b64 v[158:159], v103
	ds_read_b64 v[160:161], v85
	s_waitcnt lgkmcnt(8)
	v_pk_add_f32 v[168:169], v[116:117], v[136:137] neg_lo:[0,1] neg_hi:[0,1]
	ds_read_b64 v[162:163], v104
	ds_read_b64 v[164:165], v105
	ds_read_b64 v[166:167], v111
	s_waitcnt lgkmcnt(7)
	v_pk_mul_f32 v[170:171], v[168:169], v[152:153] op_sel:[1,1] op_sel_hi:[1,0]
	v_pk_add_f32 v[116:117], v[116:117], v[136:137]
	v_pk_fma_f32 v[172:173], v[168:169], v[152:153], v[170:171] neg_lo:[0,0,1] neg_hi:[0,0,1]
	v_pk_fma_f32 v[168:169], v[168:169], v[152:153], v[170:171] op_sel_hi:[0,1,1]
	v_mov_b32_e32 v173, v169
	v_pk_add_f32 v[168:169], v[124:125], v[144:145] neg_lo:[0,1] neg_hi:[0,1]
	v_pk_add_f32 v[124:125], v[124:125], v[144:145]
	v_pk_mul_f32 v[170:171], v[168:169], v[152:153] op_sel:[1,0] op_sel_hi:[0,0]
	v_pk_fma_f32 v[174:175], v[168:169], v[152:153], v[170:171] op_sel:[0,1,0]
	v_pk_fma_f32 v[152:153], v[168:169], v[152:153], v[170:171] op_sel:[0,1,0] neg_lo:[0,0,1] neg_hi:[0,0,1]
	v_pk_add_f32 v[136:137], v[116:117], v[124:125]
	v_mov_b32_e32 v175, v153
	v_pk_add_f32 v[152:153], v[172:173], v[174:175] neg_lo:[0,1] neg_hi:[0,1]
	s_waitcnt lgkmcnt(0)
; template <int R, class XT, class TWT>
; __device__ __forceinline__ void dif_task(XT X, TWT tw, int s, int task) {
;     const int lgM = 13 - s, lgq = lgM - R, q = 1 << lgq;
;     const int j0 = task & (q - 1), blk = task >> lgq, base = (blk << lgM) + j0;
;     const int pb = PADI(base), qp = (q >= 32) ? q + (q >> 4) : q;
;     f32x2v v[1 << R];
; #pragma unroll
;     for (int k = 0; k < (1 << R); ++k) v[k] = X[pb + k * qp];
; #pragma unroll
;     for (int r = 0; r < R; ++r) {
;         const int pb = R - 1 - r;
; #pragma unroll
;         for (int k = 0; k < (1 << R); ++k) if (!((k >> pb) & 1)) {
;             const int klo = k & ((1 << pb) - 1);
;             const f32x2v w = tw[(j0 + (klo << lgq)) << (s + r)];
;             const f32x2v a = v[k], b = v[k + (1 << pb)], d = a - b;
;             v[k] = a + b; v[k + (1 << pb)] = (f32x2v){d.x * w.x - d.y * w.y, d.x * w.y + d.y * w.x};
;         }
;     }
; #pragma unroll
;     for (int k = 0; k < (1 << R); ++k) X[pb + k * qp] = v[k];
; }
	v_xor_b32_e32 v135, 0x80000000, v166
	v_pk_mul_f32 v[168:169], v[158:159], v[152:153] op_sel:[1,1] op_sel_hi:[0,1]
	v_pk_fma_f32 v[170:171], v[158:159], v[152:153], v[168:169] neg_lo:[0,0,1] neg_hi:[0,0,1]
	v_pk_fma_f32 v[152:153], v[158:159], v[152:153], v[168:169] op_sel_hi:[1,0,1]
	v_pk_add_f32 v[116:117], v[116:117], v[124:125] neg_lo:[0,1] neg_hi:[0,1]
	v_mov_b32_e32 v171, v153
	v_pk_add_f32 v[152:153], v[120:121], v[140:141] neg_lo:[0,1] neg_hi:[0,1]
	v_pk_add_f32 v[120:121], v[120:121], v[140:141]
	v_pk_mul_f32 v[168:169], v[152:153], v[154:155] op_sel:[1,1] op_sel_hi:[1,0]
	v_pk_mul_f32 v[124:125], v[116:117], v[158:159] op_sel:[1,1] op_sel_hi:[1,0]
	v_pk_fma_f32 v[176:177], v[152:153], v[154:155], v[168:169] neg_lo:[0,0,1] neg_hi:[0,0,1]
	v_pk_fma_f32 v[152:153], v[152:153], v[154:155], v[168:169] op_sel_hi:[0,1,1]
	v_mov_b32_e32 v177, v153
	v_pk_add_f32 v[152:153], v[128:129], v[148:149] neg_lo:[0,1] neg_hi:[0,1]
	v_pk_add_f32 v[128:129], v[128:129], v[148:149]
	v_pk_mul_f32 v[168:169], v[152:153], v[154:155] op_sel:[1,0] op_sel_hi:[0,0]
	v_pk_fma_f32 v[178:179], v[152:153], v[154:155], v[168:169] op_sel:[0,1,0]
	v_pk_fma_f32 v[152:153], v[152:153], v[154:155], v[168:169] op_sel:[0,1,0] neg_lo:[0,0,1] neg_hi:[0,0,1]
	v_pk_add_f32 v[140:141], v[120:121], v[128:129]
	v_mov_b32_e32 v179, v153
	v_pk_add_f32 v[152:153], v[176:177], v[178:179] neg_lo:[0,1] neg_hi:[0,1]
	v_pk_add_f32 v[144:145], v[136:137], v[140:141]
	v_pk_mul_f32 v[154:155], v[158:159], v[152:153] op_sel_hi:[0,1]
	v_pk_fma_f32 v[168:169], v[158:159], v[152:153], v[154:155] op_sel:[1,0,1] op_sel_hi:[1,1,0]
	v_pk_fma_f32 v[152:153], v[158:159], v[152:153], v[154:155] op_sel:[1,0,1] op_sel_hi:[1,1,0] neg_lo:[0,0,1] neg_hi:[0,0,1]
	v_pk_add_f32 v[136:137], v[136:137], v[140:141] neg_lo:[0,1] neg_hi:[0,1]
	v_mov_b32_e32 v169, v153
	v_pk_add_f32 v[152:153], v[170:171], v[168:169] neg_lo:[0,1] neg_hi:[0,1]
	v_pk_mul_f32 v[140:141], v[136:137], v[164:165] op_sel:[1,1] op_sel_hi:[1,0]
	v_pk_mul_f32 v[154:155], v[164:165], v[152:153] op_sel:[1,1] op_sel_hi:[0,1]
	v_pk_fma_f32 v[182:183], v[164:165], v[152:153], v[154:155] neg_lo:[0,0,1] neg_hi:[0,0,1]
	v_pk_fma_f32 v[152:153], v[164:165], v[152:153], v[154:155] op_sel_hi:[1,0,1]
	s_nop 0
	v_mov_b32_e32 v183, v153
	v_pk_add_f32 v[152:153], v[118:119], v[138:139] neg_lo:[0,1] neg_hi:[0,1]
	v_pk_add_f32 v[118:119], v[118:119], v[138:139]
	v_pk_mul_f32 v[154:155], v[152:153], v[132:133] op_sel:[1,1] op_sel_hi:[1,0]
	s_nop 0
	v_pk_fma_f32 v[184:185], v[152:153], v[132:133], v[154:155] neg_lo:[0,0,1] neg_hi:[0,0,1]
	v_pk_fma_f32 v[152:153], v[152:153], v[132:133], v[154:155] op_sel_hi:[0,1,1]
	v_mov_b32_e32 v185, v153
	v_pk_add_f32 v[152:153], v[126:127], v[146:147] neg_lo:[0,1] neg_hi:[0,1]
	v_pk_add_f32 v[126:127], v[126:127], v[146:147]
	v_pk_mul_f32 v[154:155], v[152:153], v[132:133] op_sel:[1,0] op_sel_hi:[0,0]
	v_pk_fma_f32 v[186:187], v[152:153], v[132:133], v[154:155] op_sel:[0,1,0]
	v_pk_fma_f32 v[132:133], v[152:153], v[132:133], v[154:155] op_sel:[0,1,0] neg_lo:[0,0,1] neg_hi:[0,0,1]
	v_pk_add_f32 v[138:139], v[118:119], v[126:127]
	v_mov_b32_e32 v187, v133
	v_pk_add_f32 v[132:133], v[184:185], v[186:187] neg_lo:[0,1] neg_hi:[0,1]
	v_pk_add_f32 v[118:119], v[118:119], v[126:127] neg_lo:[0,1] neg_hi:[0,1]
	v_pk_mul_f32 v[152:153], v[162:163], v[132:133] op_sel:[1,1] op_sel_hi:[0,1]
	v_pk_fma_f32 v[154:155], v[162:163], v[132:133], v[152:153] neg_lo:[0,0,1] neg_hi:[0,0,1]
	v_pk_fma_f32 v[132:133], v[162:163], v[132:133], v[152:153] op_sel_hi:[1,0,1]
	s_nop 0
	v_mov_b32_e32 v155, v133
	v_pk_add_f32 v[132:133], v[122:123], v[142:143] neg_lo:[0,1] neg_hi:[0,1]
	v_pk_add_f32 v[122:123], v[122:123], v[142:143]
	v_pk_mul_f32 v[152:153], v[132:133], v[156:157] op_sel:[1,1] op_sel_hi:[1,0]
	s_nop 0
	v_pk_fma_f32 v[188:189], v[132:133], v[156:157], v[152:153] neg_lo:[0,0,1] neg_hi:[0,0,1]
	v_pk_fma_f32 v[132:133], v[132:133], v[156:157], v[152:153] op_sel_hi:[0,1,1]
	v_mov_b32_e32 v189, v133
	v_pk_add_f32 v[132:133], v[130:131], v[150:151] neg_lo:[0,1] neg_hi:[0,1]
	v_pk_add_f32 v[130:131], v[130:131], v[150:151]
	v_pk_mul_f32 v[152:153], v[132:133], v[156:157] op_sel:[1,0] op_sel_hi:[0,0]
	v_pk_fma_f32 v[190:191], v[132:133], v[156:157], v[152:153] op_sel:[0,1,0]
	v_pk_fma_f32 v[132:133], v[132:133], v[156:157], v[152:153] op_sel:[0,1,0] neg_lo:[0,0,1] neg_hi:[0,0,1]
	v_pk_add_f32 v[142:143], v[122:123], v[130:131]
	v_mov_b32_e32 v191, v133
	v_pk_add_f32 v[132:133], v[188:189], v[190:191] neg_lo:[0,1] neg_hi:[0,1]
	v_pk_add_f32 v[146:147], v[138:139], v[142:143]
	v_pk_mul_f32 v[152:153], v[160:161], v[132:133] op_sel_hi:[0,1]
	v_pk_fma_f32 v[156:157], v[160:161], v[132:133], v[152:153] op_sel:[1,0,1] op_sel_hi:[1,1,0]
	v_pk_fma_f32 v[132:133], v[160:161], v[132:133], v[152:153] op_sel:[1,0,1] op_sel_hi:[1,1,0] neg_lo:[0,0,1] neg_hi:[0,0,1]
	v_pk_add_f32 v[148:149], v[144:145], v[146:147]
	v_mov_b32_e32 v157, v133
	v_pk_add_f32 v[132:133], v[154:155], v[156:157] neg_lo:[0,1] neg_hi:[0,1]
	v_pk_add_f32 v[144:145], v[144:145], v[146:147] neg_lo:[0,1] neg_hi:[0,1]
	v_pk_mul_f32 v[152:153], v[164:165], v[132:133] op_sel_hi:[0,1]
	v_pk_fma_f32 v[192:193], v[164:165], v[132:133], v[152:153] op_sel:[1,0,1] op_sel_hi:[1,1,0]
	v_pk_fma_f32 v[132:133], v[164:165], v[132:133], v[152:153] op_sel:[1,0,1] op_sel_hi:[1,1,0] neg_lo:[0,0,1] neg_hi:[0,0,1]
	v_cndmask_b32_e64 v153, v135, v167, s[42:43]
	v_cndmask_b32_e64 v152, v167, v166, s[42:43]
	v_pk_mul_f32 v[146:147], v[144:145], v[152:153] op_sel:[1,1] op_sel_hi:[1,0]
	v_mov_b32_e32 v193, v133
	v_pk_fma_f32 v[150:151], v[144:145], v[152:153], v[146:147] neg_lo:[0,0,1] neg_hi:[0,0,1]
; template <int R, class XT, class TWT>
; __device__ __forceinline__ void dif_task(XT X, TWT tw, int s, int task) {
;     const int lgM = 13 - s, lgq = lgM - R, q = 1 << lgq;
;     const int j0 = task & (q - 1), blk = task >> lgq, base = (blk << lgM) + j0;
;     const int pb = PADI(base), qp = (q >= 32) ? q + (q >> 4) : q;
;     f32x2v v[1 << R];
; #pragma unroll
;     for (int k = 0; k < (1 << R); ++k) v[k] = X[pb + k * qp];
; #pragma unroll
;     for (int r = 0; r < R; ++r) {
;         const int pb = R - 1 - r;
; #pragma unroll
;         for (int k = 0; k < (1 << R); ++k) if (!((k >> pb) & 1)) {
;             const int klo = k & ((1 << pb) - 1);
;             const f32x2v w = tw[(j0 + (klo << lgq)) << (s + r)];
;             const f32x2v a = v[k], b = v[k + (1 << pb)], d = a - b;
;             v[k] = a + b; v[k + (1 << pb)] = (f32x2v){d.x * w.x - d.y * w.y, d.x * w.y + d.y * w.x};
;         }
;     }
; #pragma unroll
;     for (int k = 0; k < (1 << R); ++k) X[pb + k * qp] = v[k];
; }
	v_pk_fma_f32 v[144:145], v[144:145], v[152:153], v[146:147] op_sel_hi:[0,1,1]
	v_mov_b32_e32 v151, v145
	v_pk_fma_f32 v[144:145], v[136:137], v[164:165], v[140:141] neg_lo:[0,0,1] neg_hi:[0,0,1]
	v_pk_fma_f32 v[136:137], v[136:137], v[164:165], v[140:141] op_sel_hi:[0,1,1]
	v_mov_b32_e32 v145, v137
	v_pk_add_f32 v[136:137], v[138:139], v[142:143] neg_lo:[0,1] neg_hi:[0,1]
	v_pk_add_f32 v[132:133], v[182:183], v[192:193] neg_lo:[0,1] neg_hi:[0,1]
	v_pk_mul_f32 v[138:139], v[136:137], v[164:165] op_sel_hi:[1,0]
	s_nop 0
	v_pk_fma_f32 v[140:141], v[136:137], v[164:165], v[138:139] op_sel:[0,1,1] op_sel_hi:[1,1,0]
	v_pk_fma_f32 v[136:137], v[136:137], v[164:165], v[138:139] op_sel:[0,1,1] op_sel_hi:[1,1,0] neg_lo:[0,0,1] neg_hi:[0,0,1]
	s_nop 0
	v_mov_b32_e32 v141, v137
	v_pk_add_f32 v[138:139], v[144:145], v[140:141] neg_lo:[0,1] neg_hi:[0,1]
	v_pk_add_f32 v[136:137], v[144:145], v[140:141]
	v_pk_mul_f32 v[140:141], v[152:153], v[138:139] op_sel:[1,1] op_sel_hi:[0,1]
	v_pk_fma_f32 v[142:143], v[152:153], v[138:139], v[140:141] neg_lo:[0,0,1] neg_hi:[0,0,1]
	v_pk_fma_f32 v[138:139], v[152:153], v[138:139], v[140:141] op_sel_hi:[1,0,1]
	s_nop 0
	v_mov_b32_e32 v143, v139
	v_pk_fma_f32 v[138:139], v[116:117], v[158:159], v[124:125] neg_lo:[0,0,1] neg_hi:[0,0,1]
	v_pk_fma_f32 v[116:117], v[116:117], v[158:159], v[124:125] op_sel_hi:[0,1,1]
	v_mov_b32_e32 v139, v117
	v_pk_add_f32 v[116:117], v[120:121], v[128:129] neg_lo:[0,1] neg_hi:[0,1]
	s_nop 0
	v_pk_mul_f32 v[120:121], v[116:117], v[158:159] op_sel_hi:[1,0]
	s_nop 0
	v_pk_fma_f32 v[124:125], v[116:117], v[158:159], v[120:121] op_sel:[0,1,1] op_sel_hi:[1,1,0]
	v_pk_fma_f32 v[116:117], v[116:117], v[158:159], v[120:121] op_sel:[0,1,1] op_sel_hi:[1,1,0] neg_lo:[0,0,1] neg_hi:[0,0,1]
	v_pk_mul_f32 v[120:121], v[118:119], v[162:163] op_sel:[1,1] op_sel_hi:[1,0]
	v_mov_b32_e32 v125, v117
	v_pk_fma_f32 v[126:127], v[118:119], v[162:163], v[120:121] neg_lo:[0,0,1] neg_hi:[0,0,1]
	v_pk_fma_f32 v[118:119], v[118:119], v[162:163], v[120:121] op_sel_hi:[0,1,1]
	v_mov_b32_e32 v127, v119
	v_pk_add_f32 v[118:119], v[122:123], v[130:131] neg_lo:[0,1] neg_hi:[0,1]
	v_pk_add_f32 v[116:117], v[138:139], v[124:125]
	v_pk_mul_f32 v[120:121], v[118:119], v[160:161] op_sel_hi:[1,0]
	v_pk_add_f32 v[130:131], v[184:185], v[186:187]
	v_pk_fma_f32 v[122:123], v[118:119], v[160:161], v[120:121] op_sel:[0,1,1] op_sel_hi:[1,1,0]
	v_pk_fma_f32 v[118:119], v[118:119], v[160:161], v[120:121] op_sel:[0,1,1] op_sel_hi:[1,1,0] neg_lo:[0,0,1] neg_hi:[0,0,1]
	s_nop 0
	v_mov_b32_e32 v123, v119
	v_pk_add_f32 v[118:119], v[126:127], v[122:123]
	s_nop 0
	v_pk_add_f32 v[120:121], v[116:117], v[118:119]
	v_pk_add_f32 v[116:117], v[116:117], v[118:119] neg_lo:[0,1] neg_hi:[0,1]
	s_nop 0
	v_pk_mul_f32 v[118:119], v[152:153], v[116:117] op_sel:[1,1] op_sel_hi:[0,1]
	v_pk_fma_f32 v[128:129], v[152:153], v[116:117], v[118:119] neg_lo:[0,0,1] neg_hi:[0,0,1]
	v_pk_fma_f32 v[116:117], v[152:153], v[116:117], v[118:119] op_sel_hi:[1,0,1]
	s_nop 0
	v_mov_b32_e32 v129, v117
	v_pk_add_f32 v[116:117], v[138:139], v[124:125] neg_lo:[0,1] neg_hi:[0,1]
	v_pk_add_f32 v[138:139], v[188:189], v[190:191]
	v_pk_mul_f32 v[118:119], v[164:165], v[116:117] op_sel:[1,1] op_sel_hi:[0,1]
	v_pk_fma_f32 v[124:125], v[164:165], v[116:117], v[118:119] neg_lo:[0,0,1] neg_hi:[0,0,1]
	v_pk_fma_f32 v[116:117], v[164:165], v[116:117], v[118:119] op_sel_hi:[1,0,1]
	v_pk_add_f32 v[140:141], v[130:131], v[138:139]
	v_mov_b32_e32 v125, v117
	v_pk_add_f32 v[116:117], v[126:127], v[122:123] neg_lo:[0,1] neg_hi:[0,1]
	s_nop 0
	v_pk_mul_f32 v[118:119], v[164:165], v[116:117] op_sel_hi:[0,1]
	v_pk_fma_f32 v[122:123], v[164:165], v[116:117], v[118:119] op_sel:[1,0,1] op_sel_hi:[1,1,0]
	v_pk_fma_f32 v[116:117], v[164:165], v[116:117], v[118:119] op_sel:[1,0,1] op_sel_hi:[1,1,0] neg_lo:[0,0,1] neg_hi:[0,0,1]
	s_nop 0
	v_mov_b32_e32 v123, v117
	v_pk_add_f32 v[118:119], v[124:125], v[122:123] neg_lo:[0,1] neg_hi:[0,1]
	v_pk_add_f32 v[116:117], v[124:125], v[122:123]
	v_pk_mul_f32 v[122:123], v[152:153], v[118:119] op_sel:[1,1] op_sel_hi:[0,1]
	v_pk_fma_f32 v[124:125], v[152:153], v[118:119], v[122:123] neg_lo:[0,0,1] neg_hi:[0,0,1]
	v_pk_fma_f32 v[118:119], v[152:153], v[118:119], v[122:123] op_sel_hi:[1,0,1]
	v_pk_add_f32 v[122:123], v[176:177], v[178:179]
	v_mov_b32_e32 v125, v119
	v_pk_add_f32 v[118:119], v[172:173], v[174:175]
	s_nop 0
	v_pk_add_f32 v[126:127], v[118:119], v[122:123]
	v_pk_add_f32 v[118:119], v[118:119], v[122:123] neg_lo:[0,1] neg_hi:[0,1]
	v_pk_add_f32 v[144:145], v[126:127], v[140:141]
	v_pk_add_f32 v[126:127], v[126:127], v[140:141] neg_lo:[0,1] neg_hi:[0,1]
	v_pk_mul_f32 v[122:123], v[164:165], v[118:119] op_sel:[1,1] op_sel_hi:[0,1]
	v_pk_mul_f32 v[140:141], v[126:127], v[152:153] op_sel:[1,1] op_sel_hi:[1,0]
	s_nop 0
	v_pk_fma_f32 v[146:147], v[126:127], v[152:153], v[140:141] neg_lo:[0,0,1] neg_hi:[0,0,1]
	v_pk_fma_f32 v[126:127], v[126:127], v[152:153], v[140:141] op_sel_hi:[0,1,1]
	v_mov_b32_e32 v147, v127
	v_pk_fma_f32 v[126:127], v[164:165], v[118:119], v[122:123] neg_lo:[0,0,1] neg_hi:[0,0,1]
	v_pk_fma_f32 v[118:119], v[164:165], v[118:119], v[122:123] op_sel_hi:[1,0,1]
	s_nop 0
	v_mov_b32_e32 v127, v119
	v_pk_add_f32 v[118:119], v[130:131], v[138:139] neg_lo:[0,1] neg_hi:[0,1]
	s_nop 0
	v_pk_mul_f32 v[122:123], v[164:165], v[118:119] op_sel_hi:[0,1]
	v_pk_fma_f32 v[130:131], v[164:165], v[118:119], v[122:123] op_sel:[1,0,1] op_sel_hi:[1,1,0]
	v_pk_fma_f32 v[118:119], v[164:165], v[118:119], v[122:123] op_sel:[1,0,1] op_sel_hi:[1,1,0] neg_lo:[0,0,1] neg_hi:[0,0,1]
	s_nop 0
	v_mov_b32_e32 v131, v119
	v_pk_add_f32 v[122:123], v[126:127], v[130:131] neg_lo:[0,1] neg_hi:[0,1]
; __device__ __forceinline__ void lds_barrier() { asm volatile("s_waitcnt lgkmcnt(0)" ::: "memory"); __builtin_amdgcn_s_barrier(); asm volatile("" ::: "memory"); }
; template <int R, class XT, class TWT>
; __device__ __forceinline__ void dif_task(XT X, TWT tw, int s, int task) {
;     ...
;     for (int k = 0; k < (1 << R); ++k) X[pb + k * qp] = v[k];
; template <bool LAT>
; __device__ __forceinline__ void hyconv_unit(const Frame& F, LAS f32x2v* X, const TwHalf tw, LAS bf16* OUT, const float* skip, bf16* MIX, int u) {
;     ...
; #pragma unroll
;             for (int r = 0; r < 8; ++r) { const int e = 2 * (F.tid + 512 * r);
;                 const f32x2v a = X[PADI(e)], b = X[PADI(e + 1)]; const f32x4 k = kq[r];
;                 const f32x2v p = a + b, q = a - b; const f32x2v pk = (f32x2v){p.x * k.x - p.y * k.y, p.x * k.y + p.y * k.x}, qk = (f32x2v){q.x * k.z - q.y * k.w, q.x * k.w + q.y * k.z};
;                 X[PADI(e)] = pk + qk; X[PADI(e + 1)] = pk - qk; }
;             lds_barrier();
	v_pk_add_f32 v[118:119], v[126:127], v[130:131]
	v_pk_mul_f32 v[126:127], v[152:153], v[122:123] op_sel:[1,1] op_sel_hi:[0,1]
	v_pk_fma_f32 v[130:131], v[152:153], v[122:123], v[126:127] neg_lo:[0,0,1] neg_hi:[0,0,1]
	v_pk_fma_f32 v[122:123], v[152:153], v[122:123], v[126:127] op_sel_hi:[1,0,1]
	v_pk_add_f32 v[126:127], v[154:155], v[156:157]
	v_mov_b32_e32 v131, v123
	v_pk_add_f32 v[122:123], v[170:171], v[168:169]
	s_nop 0
	v_pk_add_f32 v[138:139], v[122:123], v[126:127]
	v_pk_add_f32 v[122:123], v[122:123], v[126:127] neg_lo:[0,1] neg_hi:[0,1]
	s_nop 0
	v_pk_mul_f32 v[126:127], v[152:153], v[122:123] op_sel:[1,1] op_sel_hi:[0,1]
	v_pk_fma_f32 v[140:141], v[152:153], v[122:123], v[126:127] neg_lo:[0,0,1] neg_hi:[0,0,1]
	v_pk_fma_f32 v[122:123], v[152:153], v[122:123], v[126:127] op_sel_hi:[1,0,1]
	v_pk_mul_f32 v[126:127], v[152:153], v[132:133] op_sel:[1,1] op_sel_hi:[0,1]
	v_pk_fma_f32 v[154:155], v[152:153], v[132:133], v[126:127] neg_lo:[0,0,1] neg_hi:[0,0,1]
	v_pk_fma_f32 v[126:127], v[152:153], v[132:133], v[126:127] op_sel_hi:[1,0,1]
	v_mov_b32_e32 v141, v123
	v_pk_add_f32 v[122:123], v[182:183], v[192:193]
	v_mov_b32_e32 v155, v127
	ds_write2_b64 v84, v[148:149], v[150:151] offset1:2
	ds_write2_b64 v84, v[136:137], v[142:143] offset0:4 offset1:6
	ds_write2_b64 v84, v[120:121], v[128:129] offset0:8 offset1:10
	ds_write2_b64 v84, v[116:117], v[124:125] offset0:12 offset1:14
	ds_write2_b64 v84, v[144:145], v[146:147] offset0:16 offset1:18
	ds_write2_b64 v84, v[118:119], v[130:131] offset0:20 offset1:22
	ds_write2_b64 v84, v[138:139], v[140:141] offset0:24 offset1:26
	ds_write2_b64 v84, v[122:123], v[154:155] offset0:28 offset1:30
	s_waitcnt lgkmcnt(0)
	s_barrier
	ds_read_b128 v[116:119], v33
	s_waitcnt lgkmcnt(0)
	v_pk_add_f32 v[120:121], v[116:117], v[118:119]
	v_pk_add_f32 v[116:117], v[116:117], v[118:119] neg_lo:[0,1] neg_hi:[0,1]
	s_waitcnt vmcnt(7)
	v_pk_mul_f32 v[118:119], v[28:29], v[120:121] op_sel:[1,1] op_sel_hi:[0,1]
	v_pk_fma_f32 v[122:123], v[28:29], v[120:121], v[118:119] neg_lo:[0,0,1] neg_hi:[0,0,1]
	v_pk_fma_f32 v[28:29], v[28:29], v[120:121], v[118:119] op_sel_hi:[1,0,1]
	s_nop 0
	v_mov_b32_e32 v123, v29
	v_pk_mul_f32 v[28:29], v[30:31], v[116:117] op_sel:[1,1] op_sel_hi:[0,1]
	v_pk_fma_f32 v[118:119], v[30:31], v[116:117], v[28:29] neg_lo:[0,0,1] neg_hi:[0,0,1]
	v_pk_fma_f32 v[28:29], v[30:31], v[116:117], v[28:29] op_sel_hi:[1,0,1]
	s_nop 0
	v_mov_b32_e32 v119, v29
	v_pk_add_f32 v[28:29], v[122:123], v[118:119]
	v_pk_add_f32 v[30:31], v[122:123], v[118:119] neg_lo:[0,1] neg_hi:[0,1]
	ds_write_b128 v33, v[28:31]
	ds_read_b128 v[28:31], v68 offset:8192
	s_waitcnt lgkmcnt(0)
	v_pk_add_f32 v[116:117], v[28:29], v[30:31]
	v_pk_add_f32 v[28:29], v[28:29], v[30:31] neg_lo:[0,1] neg_hi:[0,1]
	s_waitcnt vmcnt(6)
	v_pk_mul_f32 v[30:31], v[24:25], v[116:117] op_sel:[1,1] op_sel_hi:[0,1]
	v_pk_fma_f32 v[118:119], v[24:25], v[116:117], v[30:31] neg_lo:[0,0,1] neg_hi:[0,0,1]
	v_pk_fma_f32 v[24:25], v[24:25], v[116:117], v[30:31] op_sel_hi:[1,0,1]
	s_nop 0
	v_mov_b32_e32 v119, v25
	v_pk_mul_f32 v[24:25], v[26:27], v[28:29] op_sel:[1,1] op_sel_hi:[0,1]
	v_pk_fma_f32 v[30:31], v[26:27], v[28:29], v[24:25] neg_lo:[0,0,1] neg_hi:[0,0,1]
	v_pk_fma_f32 v[24:25], v[26:27], v[28:29], v[24:25] op_sel_hi:[1,0,1]
	s_nop 0
	v_mov_b32_e32 v31, v25
	v_pk_add_f32 v[24:25], v[118:119], v[30:31]
	v_pk_add_f32 v[26:27], v[118:119], v[30:31] neg_lo:[0,1] neg_hi:[0,1]
	ds_write_b128 v68, v[24:27] offset:8192
	ds_read_b128 v[24:27], v69 offset:16384
	s_waitcnt lgkmcnt(0)
	v_pk_add_f32 v[28:29], v[24:25], v[26:27]
	v_pk_add_f32 v[24:25], v[24:25], v[26:27] neg_lo:[0,1] neg_hi:[0,1]
	s_waitcnt vmcnt(5)
	v_pk_mul_f32 v[26:27], v[20:21], v[28:29] op_sel:[1,1] op_sel_hi:[0,1]
	v_pk_fma_f32 v[30:31], v[20:21], v[28:29], v[26:27] neg_lo:[0,0,1] neg_hi:[0,0,1]
	v_pk_fma_f32 v[20:21], v[20:21], v[28:29], v[26:27] op_sel_hi:[1,0,1]
	s_nop 0
	v_mov_b32_e32 v31, v21
	v_pk_mul_f32 v[20:21], v[22:23], v[24:25] op_sel:[1,1] op_sel_hi:[0,1]
	v_pk_fma_f32 v[26:27], v[22:23], v[24:25], v[20:21] neg_lo:[0,0,1] neg_hi:[0,0,1]
	v_pk_fma_f32 v[20:21], v[22:23], v[24:25], v[20:21] op_sel_hi:[1,0,1]
	s_nop 0
	v_mov_b32_e32 v27, v21
	v_pk_add_f32 v[20:21], v[30:31], v[26:27]
	v_pk_add_f32 v[22:23], v[30:31], v[26:27] neg_lo:[0,1] neg_hi:[0,1]
	ds_write_b128 v69, v[20:23] offset:16384
	ds_read_b128 v[20:23], v70 offset:24576
	s_waitcnt lgkmcnt(0)
	v_pk_add_f32 v[24:25], v[20:21], v[22:23]
	v_pk_add_f32 v[20:21], v[20:21], v[22:23] neg_lo:[0,1] neg_hi:[0,1]
	s_waitcnt vmcnt(4)
	v_pk_mul_f32 v[22:23], v[16:17], v[24:25] op_sel:[1,1] op_sel_hi:[0,1]
	v_pk_fma_f32 v[26:27], v[16:17], v[24:25], v[22:23] neg_lo:[0,0,1] neg_hi:[0,0,1]
	v_pk_fma_f32 v[16:17], v[16:17], v[24:25], v[22:23] op_sel_hi:[1,0,1]
	s_nop 0
	v_mov_b32_e32 v27, v17
	v_pk_mul_f32 v[16:17], v[18:19], v[20:21] op_sel:[1,1] op_sel_hi:[0,1]
	v_pk_fma_f32 v[22:23], v[18:19], v[20:21], v[16:17] neg_lo:[0,0,1] neg_hi:[0,0,1]
	v_pk_fma_f32 v[16:17], v[18:19], v[20:21], v[16:17] op_sel_hi:[1,0,1]
	s_nop 0
	v_mov_b32_e32 v23, v17
	v_pk_add_f32 v[16:17], v[26:27], v[22:23]
	v_pk_add_f32 v[18:19], v[26:27], v[22:23] neg_lo:[0,1] neg_hi:[0,1]
	ds_write_b128 v70, v[16:19] offset:24576
	ds_read_b128 v[16:19], v71 offset:32768
	s_waitcnt lgkmcnt(0)
	v_pk_add_f32 v[20:21], v[16:17], v[18:19]
	v_pk_add_f32 v[16:17], v[16:17], v[18:19] neg_lo:[0,1] neg_hi:[0,1]
	s_waitcnt vmcnt(3)
; __device__ __forceinline__ void lds_barrier() { asm volatile("s_waitcnt lgkmcnt(0)" ::: "memory"); __builtin_amdgcn_s_barrier(); asm volatile("" ::: "memory"); }
; template <int R, class XT, class TWT>
; __device__ __forceinline__ void dit_task(XT X, TWT tw, int s, int task) {
;     const int lgM = 13 - s, lgq = lgM - R, q = 1 << lgq;
;     const int j0 = task & (q - 1), blk = task >> lgq, base = (blk << lgM) + j0;
;     const int pb = PADI(base), qp = (q >= 32) ? q + (q >> 4) : q;
;     f32x2v v[1 << R];
; #pragma unroll
;     for (int k = 0; k < (1 << R); ++k) v[k] = X[pb + k * qp];
; #pragma unroll
;     for (int r = R - 1; r >= 0; --r) {
;         const int pb = R - 1 - r;
; #pragma unroll
;         for (int k = 0; k < (1 << R); ++k) if (!((k >> pb) & 1)) {
;             const int klo = k & ((1 << pb) - 1);
;             const f32x2v w = tw[(j0 + (klo << lgq)) << (s + r)];
;             const f32x2v a = v[k], qv = v[k + (1 << pb)]; const f32x2v b = (f32x2v){qv.x * w.x + qv.y * w.y, qv.y * w.x - qv.x * w.y};
;             v[k] = a + b; v[k + (1 << pb)] = a - b;
;         }
;     }
; #pragma unroll
;     for (int k = 0; k < (1 << R); ++k) X[pb + k * qp] = v[k];
; }
; template <bool LAT>
; __device__ __forceinline__ void hyconv_unit(const Frame& F, LAS f32x2v* X, const TwHalf tw, LAS bf16* OUT, const float* skip, bf16* MIX, int u) {
;     ...
;             for (int r = 0; r < 8; ++r) { const int e = 2 * (F.tid + 512 * r);
;                 const f32x2v a = X[PADI(e)], b = X[PADI(e + 1)]; const f32x4 k = kq[r];
;                 const f32x2v p = a + b, q = a - b; const f32x2v pk = (f32x2v){p.x * k.x - p.y * k.y, p.x * k.y + p.y * k.x}, qk = (f32x2v){q.x * k.z - q.y * k.w, q.x * k.w + q.y * k.z};
;                 X[PADI(e)] = pk + qk; X[PADI(e + 1)] = pk - qk; }
;             lds_barrier();
;             if constexpr (LAT) {
;                 const float sk = skip[ord * 256 + c0];
	v_pk_mul_f32 v[18:19], v[12:13], v[20:21] op_sel:[1,1] op_sel_hi:[0,1]
	v_pk_fma_f32 v[22:23], v[12:13], v[20:21], v[18:19] neg_lo:[0,0,1] neg_hi:[0,0,1]
	v_pk_fma_f32 v[12:13], v[12:13], v[20:21], v[18:19] op_sel_hi:[1,0,1]
	s_nop 0
	v_mov_b32_e32 v23, v13
	v_pk_mul_f32 v[12:13], v[14:15], v[16:17] op_sel:[1,1] op_sel_hi:[0,1]
	v_pk_fma_f32 v[18:19], v[14:15], v[16:17], v[12:13] neg_lo:[0,0,1] neg_hi:[0,0,1]
	v_pk_fma_f32 v[12:13], v[14:15], v[16:17], v[12:13] op_sel_hi:[1,0,1]
	s_nop 0
	v_mov_b32_e32 v19, v13
	v_pk_add_f32 v[12:13], v[22:23], v[18:19]
	v_pk_add_f32 v[14:15], v[22:23], v[18:19] neg_lo:[0,1] neg_hi:[0,1]
	ds_write_b128 v71, v[12:15] offset:32768
	ds_read_b128 v[12:15], v72 offset:40960
	s_waitcnt lgkmcnt(0)
	v_pk_add_f32 v[16:17], v[12:13], v[14:15]
	v_pk_add_f32 v[12:13], v[12:13], v[14:15] neg_lo:[0,1] neg_hi:[0,1]
	s_waitcnt vmcnt(2)
	v_pk_mul_f32 v[14:15], v[8:9], v[16:17] op_sel:[1,1] op_sel_hi:[0,1]
	v_pk_fma_f32 v[18:19], v[8:9], v[16:17], v[14:15] neg_lo:[0,0,1] neg_hi:[0,0,1]
	v_pk_fma_f32 v[8:9], v[8:9], v[16:17], v[14:15] op_sel_hi:[1,0,1]
	s_nop 0
	v_mov_b32_e32 v19, v9
	v_pk_mul_f32 v[8:9], v[10:11], v[12:13] op_sel:[1,1] op_sel_hi:[0,1]
	v_pk_fma_f32 v[14:15], v[10:11], v[12:13], v[8:9] neg_lo:[0,0,1] neg_hi:[0,0,1]
	v_pk_fma_f32 v[8:9], v[10:11], v[12:13], v[8:9] op_sel_hi:[1,0,1]
	s_nop 0
	v_mov_b32_e32 v15, v9
	v_pk_add_f32 v[8:9], v[18:19], v[14:15]
	v_pk_add_f32 v[10:11], v[18:19], v[14:15] neg_lo:[0,1] neg_hi:[0,1]
	ds_write_b128 v72, v[8:11] offset:40960
	ds_read_b128 v[8:11], v73 offset:49152
	s_waitcnt lgkmcnt(0)
	v_pk_add_f32 v[12:13], v[8:9], v[10:11]
	v_pk_add_f32 v[8:9], v[8:9], v[10:11] neg_lo:[0,1] neg_hi:[0,1]
	s_waitcnt vmcnt(1)
	v_pk_mul_f32 v[10:11], v[4:5], v[12:13] op_sel:[1,1] op_sel_hi:[0,1]
	v_pk_fma_f32 v[14:15], v[4:5], v[12:13], v[10:11] neg_lo:[0,0,1] neg_hi:[0,0,1]
	v_pk_fma_f32 v[4:5], v[4:5], v[12:13], v[10:11] op_sel_hi:[1,0,1]
	s_nop 0
	v_mov_b32_e32 v15, v5
	v_pk_mul_f32 v[4:5], v[6:7], v[8:9] op_sel:[1,1] op_sel_hi:[0,1]
	v_pk_fma_f32 v[10:11], v[6:7], v[8:9], v[4:5] neg_lo:[0,0,1] neg_hi:[0,0,1]
	v_pk_fma_f32 v[4:5], v[6:7], v[8:9], v[4:5] op_sel_hi:[1,0,1]
	s_nop 0
	v_mov_b32_e32 v11, v5
	v_pk_add_f32 v[4:5], v[14:15], v[10:11]
	v_pk_add_f32 v[6:7], v[14:15], v[10:11] neg_lo:[0,1] neg_hi:[0,1]
	ds_write_b128 v73, v[4:7] offset:49152
	ds_read_b128 v[4:7], v74 offset:57344
	s_waitcnt lgkmcnt(0)
	v_pk_add_f32 v[8:9], v[4:5], v[6:7]
	v_pk_add_f32 v[4:5], v[4:5], v[6:7] neg_lo:[0,1] neg_hi:[0,1]
	s_waitcnt vmcnt(0)
	v_pk_mul_f32 v[6:7], v[0:1], v[8:9] op_sel:[1,1] op_sel_hi:[0,1]
	v_pk_fma_f32 v[10:11], v[0:1], v[8:9], v[6:7] neg_lo:[0,0,1] neg_hi:[0,0,1]
	v_pk_fma_f32 v[0:1], v[0:1], v[8:9], v[6:7] op_sel_hi:[1,0,1]
	s_nop 0
	v_mov_b32_e32 v11, v1
	v_pk_mul_f32 v[0:1], v[2:3], v[4:5] op_sel:[1,1] op_sel_hi:[0,1]
	v_pk_fma_f32 v[6:7], v[2:3], v[4:5], v[0:1] neg_lo:[0,0,1] neg_hi:[0,0,1]
	v_pk_fma_f32 v[0:1], v[2:3], v[4:5], v[0:1] op_sel_hi:[1,0,1]
	s_nop 0
	v_mov_b32_e32 v7, v1
	v_pk_add_f32 v[0:1], v[10:11], v[6:7]
	v_pk_add_f32 v[2:3], v[10:11], v[6:7] neg_lo:[0,1] neg_hi:[0,1]
	ds_write_b128 v74, v[0:3] offset:57344
	s_waitcnt lgkmcnt(0)
	s_barrier
	global_load_dword v4, v181, s[0:1]
	ds_read2_b64 v[0:3], v84 offset1:2
	ds_read2_b64 v[6:9], v84 offset0:4 offset1:6
	ds_read2_b64 v[10:13], v84 offset0:8 offset1:10
	ds_read2_b64 v[14:17], v84 offset0:12 offset1:14
	ds_read2_b64 v[18:21], v84 offset0:16 offset1:18
	ds_read2_b64 v[22:25], v84 offset0:20 offset1:22
	ds_read2_b64 v[26:29], v84 offset0:24 offset1:26
	ds_read2_b64 v[116:119], v84 offset0:28 offset1:30
	ds_read_b64 v[30:31], v111
	ds_read_b64 v[124:125], v105
	ds_read_b64 v[126:127], v104
	ds_read2st64_b64 v[120:123], v100 offset1:16
	ds_read_b64 v[128:129], v103
	ds_read_b64 v[130:131], v85
	ds_read_b64 v[132:133], v101
	ds_read_b64 v[136:137], v102
	s_waitcnt lgkmcnt(7)
	v_xor_b32_e32 v5, 0x80000000, v30
	v_cndmask_b32_e64 v139, v5, v31, s[42:43]
	v_cndmask_b32_e64 v138, v31, v30, s[42:43]
	v_mov_b32_e32 v30, v139
	v_pk_mul_f32 v[140:141], v[2:3], v[30:31] op_sel_hi:[1,0]
	s_add_u32 s0, s24, s2
	v_pk_fma_f32 v[142:143], v[2:3], v[138:139], v[140:141] op_sel:[0,0,1] op_sel_hi:[1,1,0]
	v_pk_fma_f32 v[2:3], v[2:3], v[138:139], v[140:141] op_sel:[0,0,1] op_sel_hi:[1,0,0] neg_lo:[0,0,1] neg_hi:[0,0,1]
	v_pk_mul_f32 v[140:141], v[8:9], v[30:31] op_sel_hi:[1,0]
	v_mov_b32_e32 v143, v3
	v_pk_fma_f32 v[144:145], v[8:9], v[138:139], v[140:141] op_sel:[0,0,1] op_sel_hi:[1,1,0]
	v_pk_fma_f32 v[8:9], v[8:9], v[138:139], v[140:141] op_sel:[0,0,1] op_sel_hi:[1,0,0] neg_lo:[0,0,1] neg_hi:[0,0,1]
	v_pk_add_f32 v[2:3], v[0:1], v[142:143]
	v_mov_b32_e32 v145, v9
	v_pk_add_f32 v[8:9], v[6:7], v[144:145]
	v_pk_add_f32 v[6:7], v[6:7], v[144:145] neg_lo:[0,1] neg_hi:[0,1]
	s_waitcnt lgkmcnt(6)
	v_pk_mul_f32 v[140:141], v[124:125], v[8:9] op_sel:[1,0]
	v_pk_add_f32 v[0:1], v[0:1], v[142:143] neg_lo:[0,1] neg_hi:[0,1]
	v_pk_fma_f32 v[146:147], v[124:125], v[8:9], v[140:141] op_sel:[0,0,1] op_sel_hi:[1,1,0]
	v_pk_fma_f32 v[8:9], v[124:125], v[8:9], v[140:141] op_sel:[0,0,1] op_sel_hi:[0,1,0] neg_lo:[0,0,1] neg_hi:[0,0,1]
	v_pk_mul_f32 v[140:141], v[12:13], v[30:31] op_sel_hi:[1,0]
	v_mov_b32_e32 v147, v9
	v_pk_fma_f32 v[148:149], v[12:13], v[138:139], v[140:141] op_sel:[0,0,1] op_sel_hi:[1,1,0]
	v_pk_fma_f32 v[12:13], v[12:13], v[138:139], v[140:141] op_sel:[0,0,1] op_sel_hi:[1,0,0] neg_lo:[0,0,1] neg_hi:[0,0,1]
	v_pk_mul_f32 v[140:141], v[16:17], v[30:31] op_sel_hi:[1,0]
	v_mov_b32_e32 v149, v13
	v_pk_fma_f32 v[150:151], v[16:17], v[138:139], v[140:141] op_sel:[0,0,1] op_sel_hi:[1,1,0]
	v_pk_fma_f32 v[16:17], v[16:17], v[138:139], v[140:141] op_sel:[0,0,1] op_sel_hi:[1,0,0] neg_lo:[0,0,1] neg_hi:[0,0,1]
	v_pk_add_f32 v[12:13], v[10:11], v[148:149]
	v_mov_b32_e32 v151, v17
	v_pk_add_f32 v[16:17], v[14:15], v[150:151]
	v_pk_add_f32 v[14:15], v[14:15], v[150:151] neg_lo:[0,1] neg_hi:[0,1]
	v_pk_mul_f32 v[140:141], v[124:125], v[16:17] op_sel:[1,0]
	v_pk_add_f32 v[10:11], v[10:11], v[148:149] neg_lo:[0,1] neg_hi:[0,1]
	v_pk_fma_f32 v[152:153], v[124:125], v[16:17], v[140:141] op_sel:[0,0,1] op_sel_hi:[1,1,0]
	v_pk_fma_f32 v[16:17], v[124:125], v[16:17], v[140:141] op_sel:[0,0,1] op_sel_hi:[0,1,0] neg_lo:[0,0,1] neg_hi:[0,0,1]
	v_mov_b32_e32 v153, v17
	v_pk_add_f32 v[16:17], v[12:13], v[152:153]
	v_pk_add_f32 v[12:13], v[12:13], v[152:153] neg_lo:[0,1] neg_hi:[0,1]
	s_waitcnt lgkmcnt(3)
; template <int R, class XT, class TWT>
; __device__ __forceinline__ void dit_task(XT X, TWT tw, int s, int task) {
;     const int lgM = 13 - s, lgq = lgM - R, q = 1 << lgq;
;     const int j0 = task & (q - 1), blk = task >> lgq, base = (blk << lgM) + j0;
;     const int pb = PADI(base), qp = (q >= 32) ? q + (q >> 4) : q;
;     f32x2v v[1 << R];
; #pragma unroll
;     for (int k = 0; k < (1 << R); ++k) v[k] = X[pb + k * qp];
; #pragma unroll
;     for (int r = R - 1; r >= 0; --r) {
;         const int pb = R - 1 - r;
; #pragma unroll
;         for (int k = 0; k < (1 << R); ++k) if (!((k >> pb) & 1)) {
;             const int klo = k & ((1 << pb) - 1);
;             const f32x2v w = tw[(j0 + (klo << lgq)) << (s + r)];
;             const f32x2v a = v[k], qv = v[k + (1 << pb)]; const f32x2v b = (f32x2v){qv.x * w.x + qv.y * w.y, qv.y * w.x - qv.x * w.y};
;             v[k] = a + b; v[k + (1 << pb)] = a - b;
;         }
;     }
; #pragma unroll
;     for (int k = 0; k < (1 << R); ++k) X[pb + k * qp] = v[k];
; }
	v_pk_mul_f32 v[140:141], v[128:129], v[16:17] op_sel:[1,0]
	v_pk_add_f32 v[8:9], v[2:3], v[146:147]
	v_pk_fma_f32 v[154:155], v[128:129], v[16:17], v[140:141] op_sel:[0,0,1] op_sel_hi:[1,1,0]
	v_pk_fma_f32 v[16:17], v[128:129], v[16:17], v[140:141] op_sel:[0,0,1] op_sel_hi:[0,1,0] neg_lo:[0,0,1] neg_hi:[0,0,1]
	v_pk_mul_f32 v[140:141], v[20:21], v[30:31] op_sel_hi:[1,0]
	v_pk_add_f32 v[2:3], v[2:3], v[146:147] neg_lo:[0,1] neg_hi:[0,1]
	v_pk_fma_f32 v[156:157], v[20:21], v[138:139], v[140:141] op_sel:[0,0,1] op_sel_hi:[1,1,0]
	v_pk_fma_f32 v[20:21], v[20:21], v[138:139], v[140:141] op_sel:[0,0,1] op_sel_hi:[1,0,0] neg_lo:[0,0,1] neg_hi:[0,0,1]
	v_pk_mul_f32 v[140:141], v[24:25], v[30:31] op_sel_hi:[1,0]
	v_mov_b32_e32 v157, v21
	v_pk_fma_f32 v[158:159], v[24:25], v[138:139], v[140:141] op_sel:[0,0,1] op_sel_hi:[1,1,0]
	v_pk_fma_f32 v[24:25], v[24:25], v[138:139], v[140:141] op_sel:[0,0,1] op_sel_hi:[1,0,0] neg_lo:[0,0,1] neg_hi:[0,0,1]
	v_pk_add_f32 v[20:21], v[18:19], v[156:157]
	v_mov_b32_e32 v159, v25
	v_pk_add_f32 v[24:25], v[22:23], v[158:159]
	v_pk_add_f32 v[22:23], v[22:23], v[158:159] neg_lo:[0,1] neg_hi:[0,1]
	v_pk_mul_f32 v[140:141], v[124:125], v[24:25] op_sel:[1,0]
	v_pk_add_f32 v[18:19], v[18:19], v[156:157] neg_lo:[0,1] neg_hi:[0,1]
	v_pk_fma_f32 v[160:161], v[124:125], v[24:25], v[140:141] op_sel:[0,0,1] op_sel_hi:[1,1,0]
	v_pk_fma_f32 v[24:25], v[124:125], v[24:25], v[140:141] op_sel:[0,0,1] op_sel_hi:[0,1,0] neg_lo:[0,0,1] neg_hi:[0,0,1]
	v_pk_mul_f32 v[140:141], v[28:29], v[30:31] op_sel_hi:[1,0]
	v_pk_mul_f32 v[30:31], v[118:119], v[30:31] op_sel_hi:[1,0]
	v_pk_fma_f32 v[162:163], v[28:29], v[138:139], v[140:141] op_sel:[0,0,1] op_sel_hi:[1,1,0]
	v_pk_fma_f32 v[28:29], v[28:29], v[138:139], v[140:141] op_sel:[0,0,1] op_sel_hi:[1,0,0] neg_lo:[0,0,1] neg_hi:[0,0,1]
	v_pk_fma_f32 v[140:141], v[118:119], v[138:139], v[30:31] op_sel:[0,0,1] op_sel_hi:[1,1,0]
	v_pk_fma_f32 v[30:31], v[118:119], v[138:139], v[30:31] op_sel:[0,0,1] op_sel_hi:[1,0,0] neg_lo:[0,0,1] neg_hi:[0,0,1]
	v_mov_b32_e32 v163, v29
	v_mov_b32_e32 v141, v31
	v_pk_add_f32 v[30:31], v[116:117], v[140:141]
	v_pk_add_f32 v[28:29], v[26:27], v[162:163]
	v_pk_mul_f32 v[118:119], v[124:125], v[30:31] op_sel:[1,0]
	v_mov_b32_e32 v161, v25
	v_pk_fma_f32 v[138:139], v[124:125], v[30:31], v[118:119] op_sel:[0,0,1] op_sel_hi:[1,1,0]
	v_pk_fma_f32 v[30:31], v[124:125], v[30:31], v[118:119] op_sel:[0,0,1] op_sel_hi:[0,1,0] neg_lo:[0,0,1] neg_hi:[0,0,1]
	v_mov_b32_e32 v139, v31
	v_pk_add_f32 v[30:31], v[28:29], v[138:139]
	v_pk_add_f32 v[24:25], v[20:21], v[160:161]
	v_pk_mul_f32 v[118:119], v[128:129], v[30:31] op_sel:[1,0]
	v_pk_add_f32 v[116:117], v[116:117], v[140:141] neg_lo:[0,1] neg_hi:[0,1]
	v_pk_fma_f32 v[164:165], v[128:129], v[30:31], v[118:119] op_sel:[0,0,1] op_sel_hi:[1,1,0]
	v_pk_fma_f32 v[30:31], v[128:129], v[30:31], v[118:119] op_sel:[0,0,1] op_sel_hi:[0,1,0] neg_lo:[0,0,1] neg_hi:[0,0,1]
	v_mov_b32_e32 v165, v31
	v_pk_add_f32 v[30:31], v[24:25], v[164:165]
	v_pk_add_f32 v[26:27], v[26:27], v[162:163] neg_lo:[0,1] neg_hi:[0,1]
	v_pk_mul_f32 v[118:119], v[120:121], v[30:31] op_sel:[1,0]
	v_pk_add_f32 v[28:29], v[28:29], v[138:139] neg_lo:[0,1] neg_hi:[0,1]
	v_pk_fma_f32 v[166:167], v[120:121], v[30:31], v[118:119] op_sel:[0,0,1] op_sel_hi:[1,1,0]
	v_pk_fma_f32 v[30:31], v[120:121], v[30:31], v[118:119] op_sel:[0,0,1] op_sel_hi:[0,1,0] neg_lo:[0,0,1] neg_hi:[0,0,1]
	v_pk_mul_f32 v[118:119], v[124:125], v[6:7] op_sel_hi:[0,1]
	v_pk_fma_f32 v[142:143], v[124:125], v[6:7], v[118:119] op_sel:[1,0,1] op_sel_hi:[1,1,0] neg_lo:[0,0,1] neg_hi:[0,0,1]
	v_pk_fma_f32 v[6:7], v[124:125], v[6:7], v[118:119] op_sel:[1,0,1] op_sel_hi:[1,1,0]
	v_pk_mul_f32 v[118:119], v[124:125], v[14:15] op_sel_hi:[0,1]
	v_pk_fma_f32 v[144:145], v[124:125], v[14:15], v[118:119] op_sel:[1,0,1] op_sel_hi:[1,1,0] neg_lo:[0,0,1] neg_hi:[0,0,1]
	v_pk_fma_f32 v[14:15], v[124:125], v[14:15], v[118:119] op_sel:[1,0,1] op_sel_hi:[1,1,0]
	v_mov_b32_e32 v143, v7
	v_mov_b32_e32 v145, v15
	v_pk_add_f32 v[14:15], v[10:11], v[144:145]
	v_pk_add_f32 v[6:7], v[0:1], v[142:143]
	v_pk_mul_f32 v[118:119], v[126:127], v[14:15] op_sel:[1,0]
	v_pk_add_f32 v[20:21], v[20:21], v[160:161] neg_lo:[0,1] neg_hi:[0,1]
	v_pk_fma_f32 v[148:149], v[126:127], v[14:15], v[118:119] op_sel:[0,0,1] op_sel_hi:[1,1,0]
	v_pk_fma_f32 v[14:15], v[126:127], v[14:15], v[118:119] op_sel:[0,0,1] op_sel_hi:[0,1,0] neg_lo:[0,0,1] neg_hi:[0,0,1]
	v_pk_mul_f32 v[118:119], v[124:125], v[22:23] op_sel_hi:[0,1]
	v_pk_fma_f32 v[150:151], v[124:125], v[22:23], v[118:119] op_sel:[1,0,1] op_sel_hi:[1,1,0] neg_lo:[0,0,1] neg_hi:[0,0,1]
	v_pk_fma_f32 v[22:23], v[124:125], v[22:23], v[118:119] op_sel:[1,0,1] op_sel_hi:[1,1,0]
	v_pk_mul_f32 v[118:119], v[124:125], v[116:117] op_sel_hi:[0,1]
	v_pk_fma_f32 v[140:141], v[124:125], v[116:117], v[118:119] op_sel:[1,0,1] op_sel_hi:[1,1,0] neg_lo:[0,0,1] neg_hi:[0,0,1]
	v_pk_fma_f32 v[116:117], v[124:125], v[116:117], v[118:119] op_sel:[1,0,1] op_sel_hi:[1,1,0]
	v_mov_b32_e32 v151, v23
	v_mov_b32_e32 v141, v117
	v_pk_add_f32 v[116:117], v[26:27], v[140:141]
	v_pk_add_f32 v[22:23], v[18:19], v[150:151]
	v_pk_mul_f32 v[118:119], v[126:127], v[116:117] op_sel:[1,0]
	v_mov_b32_e32 v149, v15
	v_pk_fma_f32 v[124:125], v[126:127], v[116:117], v[118:119] op_sel:[0,0,1] op_sel_hi:[1,1,0]
	v_pk_fma_f32 v[116:117], v[126:127], v[116:117], v[118:119] op_sel:[0,0,1] op_sel_hi:[0,1,0] neg_lo:[0,0,1] neg_hi:[0,0,1]
	v_mov_b32_e32 v125, v117
	v_pk_add_f32 v[116:117], v[22:23], v[124:125]
	v_pk_add_f32 v[14:15], v[6:7], v[148:149]
	s_waitcnt lgkmcnt(1)
; template <int R, class XT, class TWT>
; __device__ __forceinline__ void dit_task(XT X, TWT tw, int s, int task) {
;     const int lgM = 13 - s, lgq = lgM - R, q = 1 << lgq;
;     const int j0 = task & (q - 1), blk = task >> lgq, base = (blk << lgM) + j0;
;     const int pb = PADI(base), qp = (q >= 32) ? q + (q >> 4) : q;
;     f32x2v v[1 << R];
; #pragma unroll
;     for (int k = 0; k < (1 << R); ++k) v[k] = X[pb + k * qp];
; #pragma unroll
;     for (int r = R - 1; r >= 0; --r) {
;         const int pb = R - 1 - r;
; #pragma unroll
;         for (int k = 0; k < (1 << R); ++k) if (!((k >> pb) & 1)) {
;             const int klo = k & ((1 << pb) - 1);
;             const f32x2v w = tw[(j0 + (klo << lgq)) << (s + r)];
;             const f32x2v a = v[k], qv = v[k + (1 << pb)]; const f32x2v b = (f32x2v){qv.x * w.x + qv.y * w.y, qv.y * w.x - qv.x * w.y};
;             v[k] = a + b; v[k + (1 << pb)] = a - b;
;         }
;     }
; #pragma unroll
;     for (int k = 0; k < (1 << R); ++k) X[pb + k * qp] = v[k];
; }
	v_pk_mul_f32 v[118:119], v[132:133], v[116:117] op_sel:[1,0]
	v_pk_add_f32 v[10:11], v[10:11], v[144:145] neg_lo:[0,1] neg_hi:[0,1]
	v_pk_fma_f32 v[126:127], v[132:133], v[116:117], v[118:119] op_sel:[0,0,1] op_sel_hi:[1,1,0]
	v_pk_fma_f32 v[116:117], v[132:133], v[116:117], v[118:119] op_sel:[0,0,1] op_sel_hi:[0,1,0] neg_lo:[0,0,1] neg_hi:[0,0,1]
	v_mov_b32_e32 v127, v117
	v_pk_mul_f32 v[118:119], v[128:129], v[12:13] op_sel_hi:[0,1]
	v_pk_add_f32 v[116:117], v[14:15], v[126:127]
	v_pk_add_f32 v[14:15], v[14:15], v[126:127] neg_lo:[0,1] neg_hi:[0,1]
	v_pk_fma_f32 v[126:127], v[128:129], v[12:13], v[118:119] op_sel:[1,0,1] op_sel_hi:[1,1,0] neg_lo:[0,0,1] neg_hi:[0,0,1]
	v_pk_fma_f32 v[12:13], v[128:129], v[12:13], v[118:119] op_sel:[1,0,1] op_sel_hi:[1,1,0]
	v_pk_mul_f32 v[118:119], v[128:129], v[28:29] op_sel_hi:[0,1]
	v_pk_fma_f32 v[138:139], v[128:129], v[28:29], v[118:119] op_sel:[1,0,1] op_sel_hi:[1,1,0] neg_lo:[0,0,1] neg_hi:[0,0,1]
	v_pk_fma_f32 v[28:29], v[128:129], v[28:29], v[118:119] op_sel:[1,0,1] op_sel_hi:[1,1,0]
	v_mov_b32_e32 v127, v13
	v_mov_b32_e32 v139, v29
	v_pk_add_f32 v[28:29], v[20:21], v[138:139]
	v_pk_add_f32 v[12:13], v[2:3], v[126:127]
	v_pk_mul_f32 v[118:119], v[122:123], v[28:29] op_sel:[1,0]
	v_pk_add_f32 v[26:27], v[26:27], v[140:141] neg_lo:[0,1] neg_hi:[0,1]
	v_pk_fma_f32 v[128:129], v[122:123], v[28:29], v[118:119] op_sel:[0,0,1] op_sel_hi:[1,1,0]
	v_pk_fma_f32 v[28:29], v[122:123], v[28:29], v[118:119] op_sel:[0,0,1] op_sel_hi:[0,1,0] neg_lo:[0,0,1] neg_hi:[0,0,1]
	v_mov_b32_e32 v129, v29
	v_pk_mul_f32 v[118:119], v[130:131], v[10:11] op_sel_hi:[0,1]
	v_pk_add_f32 v[28:29], v[12:13], v[128:129]
	v_pk_add_f32 v[12:13], v[12:13], v[128:129] neg_lo:[0,1] neg_hi:[0,1]
	v_pk_fma_f32 v[128:129], v[130:131], v[10:11], v[118:119] op_sel:[1,0,1] op_sel_hi:[1,1,0] neg_lo:[0,0,1] neg_hi:[0,0,1]
	v_pk_fma_f32 v[10:11], v[130:131], v[10:11], v[118:119] op_sel:[1,0,1] op_sel_hi:[1,1,0]
	v_pk_mul_f32 v[118:119], v[130:131], v[26:27] op_sel_hi:[0,1]
	v_pk_fma_f32 v[140:141], v[130:131], v[26:27], v[118:119] op_sel:[1,0,1] op_sel_hi:[1,1,0] neg_lo:[0,0,1] neg_hi:[0,0,1]
	v_pk_fma_f32 v[26:27], v[130:131], v[26:27], v[118:119] op_sel:[1,0,1] op_sel_hi:[1,1,0]
	v_pk_add_f32 v[18:19], v[18:19], v[150:151] neg_lo:[0,1] neg_hi:[0,1]
	v_mov_b32_e32 v141, v27
	v_pk_add_f32 v[26:27], v[18:19], v[140:141]
	v_pk_add_f32 v[0:1], v[0:1], v[142:143] neg_lo:[0,1] neg_hi:[0,1]
	s_waitcnt lgkmcnt(0)
	v_pk_mul_f32 v[118:119], v[136:137], v[26:27] op_sel:[1,0]
	v_mov_b32_e32 v129, v11
	v_pk_fma_f32 v[130:131], v[136:137], v[26:27], v[118:119] op_sel:[0,0,1] op_sel_hi:[1,1,0]
	v_pk_fma_f32 v[26:27], v[136:137], v[26:27], v[118:119] op_sel:[0,0,1] op_sel_hi:[0,1,0] neg_lo:[0,0,1] neg_hi:[0,0,1]
	v_pk_add_f32 v[24:25], v[24:25], v[164:165] neg_lo:[0,1] neg_hi:[0,1]
	v_pk_add_f32 v[10:11], v[0:1], v[128:129]
	v_mov_b32_e32 v131, v27
	v_pk_mul_f32 v[118:119], v[120:121], v[24:25] op_sel_hi:[0,1]
	v_pk_add_f32 v[22:23], v[22:23], v[124:125] neg_lo:[0,1] neg_hi:[0,1]
	v_pk_add_f32 v[26:27], v[10:11], v[130:131]
	v_pk_add_f32 v[10:11], v[10:11], v[130:131] neg_lo:[0,1] neg_hi:[0,1]
	v_pk_fma_f32 v[130:131], v[120:121], v[24:25], v[118:119] op_sel:[1,0,1] op_sel_hi:[1,1,0] neg_lo:[0,0,1] neg_hi:[0,0,1]
	v_pk_fma_f32 v[24:25], v[120:121], v[24:25], v[118:119] op_sel:[1,0,1] op_sel_hi:[1,1,0]
	v_pk_mul_f32 v[118:119], v[132:133], v[22:23] op_sel_hi:[0,1]
	v_pk_fma_f32 v[120:121], v[132:133], v[22:23], v[118:119] op_sel:[1,0,1] op_sel_hi:[1,1,0] neg_lo:[0,0,1] neg_hi:[0,0,1]
	v_pk_fma_f32 v[22:23], v[132:133], v[22:23], v[118:119] op_sel:[1,0,1] op_sel_hi:[1,1,0]
	v_pk_add_f32 v[20:21], v[20:21], v[138:139] neg_lo:[0,1] neg_hi:[0,1]
	v_pk_add_f32 v[6:7], v[6:7], v[148:149] neg_lo:[0,1] neg_hi:[0,1]
	v_mov_b32_e32 v121, v23
	v_pk_mul_f32 v[118:119], v[122:123], v[20:21] op_sel_hi:[0,1]
	v_pk_add_f32 v[22:23], v[6:7], v[120:121]
	v_pk_add_f32 v[6:7], v[6:7], v[120:121] neg_lo:[0,1] neg_hi:[0,1]
	v_pk_fma_f32 v[120:121], v[122:123], v[20:21], v[118:119] op_sel:[1,0,1] op_sel_hi:[1,1,0] neg_lo:[0,0,1] neg_hi:[0,0,1]
	v_pk_fma_f32 v[20:21], v[122:123], v[20:21], v[118:119] op_sel:[1,0,1] op_sel_hi:[1,1,0]
	v_pk_add_f32 v[18:19], v[18:19], v[140:141] neg_lo:[0,1] neg_hi:[0,1]
	v_mov_b32_e32 v155, v17
	v_pk_add_f32 v[2:3], v[2:3], v[126:127] neg_lo:[0,1] neg_hi:[0,1]
	v_mov_b32_e32 v121, v21
	v_pk_mul_f32 v[118:119], v[136:137], v[18:19] op_sel_hi:[0,1]
	v_pk_add_f32 v[16:17], v[8:9], v[154:155]
	v_mov_b32_e32 v167, v31
	v_pk_add_f32 v[20:21], v[2:3], v[120:121]
	v_pk_add_f32 v[2:3], v[2:3], v[120:121] neg_lo:[0,1] neg_hi:[0,1]
	v_pk_fma_f32 v[120:121], v[136:137], v[18:19], v[118:119] op_sel:[1,0,1] op_sel_hi:[1,1,0] neg_lo:[0,0,1] neg_hi:[0,0,1]
	v_pk_fma_f32 v[18:19], v[136:137], v[18:19], v[118:119] op_sel:[1,0,1] op_sel_hi:[1,1,0]
	v_pk_add_f32 v[30:31], v[16:17], v[166:167]
	v_pk_add_f32 v[8:9], v[8:9], v[154:155] neg_lo:[0,1] neg_hi:[0,1]
	v_mov_b32_e32 v131, v25
	v_pk_add_f32 v[0:1], v[0:1], v[128:129] neg_lo:[0,1] neg_hi:[0,1]
	v_mov_b32_e32 v121, v19
	v_pk_add_f32 v[16:17], v[16:17], v[166:167] neg_lo:[0,1] neg_hi:[0,1]
	v_pk_add_f32 v[24:25], v[8:9], v[130:131]
	v_pk_add_f32 v[8:9], v[8:9], v[130:131] neg_lo:[0,1] neg_hi:[0,1]
	v_pk_add_f32 v[18:19], v[0:1], v[120:121]
	v_pk_add_f32 v[0:1], v[0:1], v[120:121] neg_lo:[0,1] neg_hi:[0,1]
	ds_write2_b64 v84, v[30:31], v[116:117] offset1:2
	ds_write2_b64 v84, v[28:29], v[26:27] offset0:4 offset1:6
	ds_write2_b64 v84, v[24:25], v[22:23] offset0:8 offset1:10
	ds_write2_b64 v84, v[20:21], v[18:19] offset0:12 offset1:14
	ds_write2_b64 v84, v[16:17], v[14:15] offset0:16 offset1:18
	ds_write2_b64 v84, v[12:13], v[10:11] offset0:20 offset1:22
	ds_write2_b64 v84, v[8:9], v[6:7] offset0:24 offset1:26
	ds_write2_b64 v84, v[2:3], v[0:1] offset0:28 offset1:30
	s_waitcnt lgkmcnt(0)
	s_barrier
; template <int R, class XT, class TWT>
; __device__ __forceinline__ void dit_task(XT X, TWT tw, int s, int task) {
;     const int lgM = 13 - s, lgq = lgM - R, q = 1 << lgq;
;     const int j0 = task & (q - 1), blk = task >> lgq, base = (blk << lgM) + j0;
;     const int pb = PADI(base), qp = (q >= 32) ? q + (q >> 4) : q;
;     f32x2v v[1 << R];
; #pragma unroll
;     for (int k = 0; k < (1 << R); ++k) v[k] = X[pb + k * qp];
; #pragma unroll
;     for (int r = R - 1; r >= 0; --r) {
;         const int pb = R - 1 - r;
; #pragma unroll
;         for (int k = 0; k < (1 << R); ++k) if (!((k >> pb) & 1)) {
;             const int klo = k & ((1 << pb) - 1);
;             const f32x2v w = tw[(j0 + (klo << lgq)) << (s + r)];
;             const f32x2v a = v[k], qv = v[k + (1 << pb)]; const f32x2v b = (f32x2v){qv.x * w.x + qv.y * w.y, qv.y * w.x - qv.x * w.y};
;             v[k] = a + b; v[k + (1 << pb)] = a - b;
;         }
;     }
; #pragma unroll
;     for (int k = 0; k < (1 << R); ++k) X[pb + k * qp] = v[k];
; }
; template <bool LAT>
; __device__ __forceinline__ void hyconv_unit(const Frame& F, LAS f32x2v* X, const TwHalf tw, LAS bf16* OUT, const float* skip, bf16* MIX, int u) {
;     ...
;                 unsigned ga[4], gb[4], za[4], zb[4];
; #pragma unroll
;                 for (int r = 0; r < 4; ++r) { const int pr = F.tid + 512 * r; ga[r] = *(const unsigned*)(g0 + 2 * pr); gb[r] = *(const unsigned*)(g1 + 2 * pr); za[r] = *(const unsigned*)(v0 + 2 * pr); zb[r] = *(const unsigned*)(v1 + 2 * pr); }
	v_lshl_add_u64 v[168:169], s[24:25], 0, v[50:51]
	v_lshl_add_u64 v[168:169], s[2:3], 0, v[168:169]
	global_load_dword v182, v[168:169], off
	global_load_dword v183, v[52:53], off
	v_lshl_add_u64 v[170:171], s[26:27], 0, v[50:51]
	v_lshl_add_u64 v[170:171], s[2:3], 0, v[170:171]
	global_load_dword v184, v[170:171], off
	global_load_dword v185, v[54:55], off
	v_lshl_add_u64 v[172:173], s[24:25], 0, v[56:57]
	v_lshl_add_u64 v[172:173], s[2:3], 0, v[172:173]
	global_load_dword v186, v[172:173], off
	v_lshl_add_u64 v[174:175], s[26:27], 0, v[56:57]
	v_lshl_add_u64 v[174:175], s[2:3], 0, v[174:175]
	global_load_dword v187, v[174:175], off
	v_lshl_add_u64 v[176:177], s[24:25], 0, v[62:63]
	v_lshl_add_u64 v[176:177], s[2:3], 0, v[176:177]
	global_load_dword v188, v[176:177], off
	v_lshl_add_u64 v[178:179], s[26:27], 0, v[62:63]
	v_lshl_add_u64 v[178:179], s[2:3], 0, v[178:179]
	global_load_dword v189, v[178:179], off
	global_load_dword v190, v[170:171], off offset:2048
	global_load_dword v191, v[168:169], off offset:2048
	global_load_dword v192, v[58:59], off
	global_load_dword v193, v[60:61], off
	global_load_dword v194, v[64:65], off
	global_load_dword v195, v[66:67], off
	global_load_dword v196, v[54:55], off offset:2048
	global_load_dword v197, v[52:53], off offset:2048
	ds_read2_b64 v[0:3], v81 offset1:34
	ds_read2_b64 v[6:9], v81 offset0:68 offset1:102
	ds_read2_b64 v[10:13], v81 offset0:136 offset1:170
	ds_read2_b64 v[14:17], v81 offset0:204 offset1:238
	ds_read2_b64 v[18:21], v110 offset0:16 offset1:50
	ds_read2_b64 v[22:25], v110 offset0:84 offset1:118
	ds_read2_b64 v[26:29], v110 offset0:152 offset1:186
	ds_read2_b64 v[116:119], v110 offset0:220 offset1:254
	ds_read_b64 v[30:31], v99
	ds_read_b64 v[124:125], v97
	ds_read_b64 v[126:127], v98
	ds_read_b64 v[128:129], v83
	ds_read_b64 v[130:131], v95
	ds_read_b64 v[132:133], v96
	ds_read_b64 v[136:137], v82
	ds_read2st64_b64 v[120:123], v94 offset1:16
	s_waitcnt lgkmcnt(4)
	v_xor_b32_e32 v5, 0x80000000, v128
	v_cndmask_b32_e64 v139, v5, v129, s[40:41]
	v_cndmask_b32_e64 v138, v129, v128, s[40:41]
	v_mov_b32_e32 v128, v139
	v_pk_mul_f32 v[140:141], v[2:3], v[128:129] op_sel_hi:[1,0]
	s_addc_u32 s1, s25, s3
	v_pk_fma_f32 v[142:143], v[2:3], v[138:139], v[140:141] op_sel:[0,0,1] op_sel_hi:[1,1,0]
	v_pk_fma_f32 v[2:3], v[2:3], v[138:139], v[140:141] op_sel:[0,0,1] op_sel_hi:[1,0,0] neg_lo:[0,0,1] neg_hi:[0,0,1]
	v_pk_mul_f32 v[140:141], v[8:9], v[128:129] op_sel_hi:[1,0]
	v_mov_b32_e32 v143, v3
	v_pk_fma_f32 v[144:145], v[8:9], v[138:139], v[140:141] op_sel:[0,0,1] op_sel_hi:[1,1,0]
	v_pk_fma_f32 v[8:9], v[8:9], v[138:139], v[140:141] op_sel:[0,0,1] op_sel_hi:[1,0,0] neg_lo:[0,0,1] neg_hi:[0,0,1]
	v_pk_add_f32 v[2:3], v[0:1], v[142:143]
	v_mov_b32_e32 v145, v9
	v_pk_add_f32 v[8:9], v[6:7], v[144:145]
	v_pk_add_f32 v[6:7], v[6:7], v[144:145] neg_lo:[0,1] neg_hi:[0,1]
	v_pk_mul_f32 v[140:141], v[30:31], v[8:9] op_sel:[1,0]
	v_pk_add_f32 v[0:1], v[0:1], v[142:143] neg_lo:[0,1] neg_hi:[0,1]
	v_pk_fma_f32 v[146:147], v[30:31], v[8:9], v[140:141] op_sel:[0,0,1] op_sel_hi:[1,1,0]
	v_pk_fma_f32 v[8:9], v[30:31], v[8:9], v[140:141] op_sel:[0,0,1] op_sel_hi:[0,1,0] neg_lo:[0,0,1] neg_hi:[0,0,1]
	v_pk_mul_f32 v[140:141], v[12:13], v[128:129] op_sel_hi:[1,0]
	v_mov_b32_e32 v147, v9
	v_pk_fma_f32 v[148:149], v[12:13], v[138:139], v[140:141] op_sel:[0,0,1] op_sel_hi:[1,1,0]
	v_pk_fma_f32 v[12:13], v[12:13], v[138:139], v[140:141] op_sel:[0,0,1] op_sel_hi:[1,0,0] neg_lo:[0,0,1] neg_hi:[0,0,1]
	v_pk_mul_f32 v[140:141], v[16:17], v[128:129] op_sel_hi:[1,0]
	v_mov_b32_e32 v149, v13
	v_pk_fma_f32 v[150:151], v[16:17], v[138:139], v[140:141] op_sel:[0,0,1] op_sel_hi:[1,1,0]
	v_pk_fma_f32 v[16:17], v[16:17], v[138:139], v[140:141] op_sel:[0,0,1] op_sel_hi:[1,0,0] neg_lo:[0,0,1] neg_hi:[0,0,1]
	v_pk_add_f32 v[12:13], v[10:11], v[148:149]
	v_mov_b32_e32 v151, v17
	v_pk_add_f32 v[16:17], v[14:15], v[150:151]
	v_pk_add_f32 v[14:15], v[14:15], v[150:151] neg_lo:[0,1] neg_hi:[0,1]
	v_pk_mul_f32 v[140:141], v[30:31], v[16:17] op_sel:[1,0]
	v_pk_add_f32 v[10:11], v[10:11], v[148:149] neg_lo:[0,1] neg_hi:[0,1]
	v_pk_fma_f32 v[152:153], v[30:31], v[16:17], v[140:141] op_sel:[0,0,1] op_sel_hi:[1,1,0]
	v_pk_fma_f32 v[16:17], v[30:31], v[16:17], v[140:141] op_sel:[0,0,1] op_sel_hi:[0,1,0] neg_lo:[0,0,1] neg_hi:[0,0,1]
	v_mov_b32_e32 v153, v17
	v_pk_add_f32 v[16:17], v[12:13], v[152:153]
	v_pk_add_f32 v[12:13], v[12:13], v[152:153] neg_lo:[0,1] neg_hi:[0,1]
	v_pk_mul_f32 v[140:141], v[124:125], v[16:17] op_sel:[1,0]
	v_pk_add_f32 v[8:9], v[2:3], v[146:147]
	v_pk_fma_f32 v[154:155], v[124:125], v[16:17], v[140:141] op_sel:[0,0,1] op_sel_hi:[1,1,0]
	v_pk_fma_f32 v[16:17], v[124:125], v[16:17], v[140:141] op_sel:[0,0,1] op_sel_hi:[0,1,0] neg_lo:[0,0,1] neg_hi:[0,0,1]
	v_pk_mul_f32 v[140:141], v[20:21], v[128:129] op_sel_hi:[1,0]
	v_pk_add_f32 v[2:3], v[2:3], v[146:147] neg_lo:[0,1] neg_hi:[0,1]
	v_pk_fma_f32 v[156:157], v[20:21], v[138:139], v[140:141] op_sel:[0,0,1] op_sel_hi:[1,1,0]
	v_pk_fma_f32 v[20:21], v[20:21], v[138:139], v[140:141] op_sel:[0,0,1] op_sel_hi:[1,0,0] neg_lo:[0,0,1] neg_hi:[0,0,1]
	v_pk_mul_f32 v[140:141], v[24:25], v[128:129] op_sel_hi:[1,0]
	v_mov_b32_e32 v157, v21
	v_pk_fma_f32 v[158:159], v[24:25], v[138:139], v[140:141] op_sel:[0,0,1] op_sel_hi:[1,1,0]
	v_pk_fma_f32 v[24:25], v[24:25], v[138:139], v[140:141] op_sel:[0,0,1] op_sel_hi:[1,0,0] neg_lo:[0,0,1] neg_hi:[0,0,1]
	v_pk_add_f32 v[20:21], v[18:19], v[156:157]
	v_mov_b32_e32 v159, v25
	v_pk_add_f32 v[24:25], v[22:23], v[158:159]
	v_pk_add_f32 v[22:23], v[22:23], v[158:159] neg_lo:[0,1] neg_hi:[0,1]
	v_pk_mul_f32 v[140:141], v[30:31], v[24:25] op_sel:[1,0]
; template <int R, class XT, class TWT>
; __device__ __forceinline__ void dit_task(XT X, TWT tw, int s, int task) {
;     const int lgM = 13 - s, lgq = lgM - R, q = 1 << lgq;
;     const int j0 = task & (q - 1), blk = task >> lgq, base = (blk << lgM) + j0;
;     const int pb = PADI(base), qp = (q >= 32) ? q + (q >> 4) : q;
;     f32x2v v[1 << R];
; #pragma unroll
;     for (int k = 0; k < (1 << R); ++k) v[k] = X[pb + k * qp];
; #pragma unroll
;     for (int r = R - 1; r >= 0; --r) {
;         const int pb = R - 1 - r;
; #pragma unroll
;         for (int k = 0; k < (1 << R); ++k) if (!((k >> pb) & 1)) {
;             const int klo = k & ((1 << pb) - 1);
;             const f32x2v w = tw[(j0 + (klo << lgq)) << (s + r)];
;             const f32x2v a = v[k], qv = v[k + (1 << pb)]; const f32x2v b = (f32x2v){qv.x * w.x + qv.y * w.y, qv.y * w.x - qv.x * w.y};
;             v[k] = a + b; v[k + (1 << pb)] = a - b;
;         }
;     }
; #pragma unroll
;     for (int k = 0; k < (1 << R); ++k) X[pb + k * qp] = v[k];
; }
	v_pk_add_f32 v[18:19], v[18:19], v[156:157] neg_lo:[0,1] neg_hi:[0,1]
	v_pk_fma_f32 v[160:161], v[30:31], v[24:25], v[140:141] op_sel:[0,0,1] op_sel_hi:[1,1,0]
	v_pk_fma_f32 v[24:25], v[30:31], v[24:25], v[140:141] op_sel:[0,0,1] op_sel_hi:[0,1,0] neg_lo:[0,0,1] neg_hi:[0,0,1]
	v_pk_mul_f32 v[140:141], v[28:29], v[128:129] op_sel_hi:[1,0]
	v_pk_mul_f32 v[128:129], v[118:119], v[128:129] op_sel_hi:[1,0]
	v_pk_fma_f32 v[162:163], v[28:29], v[138:139], v[140:141] op_sel:[0,0,1] op_sel_hi:[1,1,0]
	v_pk_fma_f32 v[28:29], v[28:29], v[138:139], v[140:141] op_sel:[0,0,1] op_sel_hi:[1,0,0] neg_lo:[0,0,1] neg_hi:[0,0,1]
	v_pk_fma_f32 v[140:141], v[118:119], v[138:139], v[128:129] op_sel:[0,0,1] op_sel_hi:[1,1,0]
	v_pk_fma_f32 v[118:119], v[118:119], v[138:139], v[128:129] op_sel:[0,0,1] op_sel_hi:[1,0,0] neg_lo:[0,0,1] neg_hi:[0,0,1]
	v_mov_b32_e32 v163, v29
	v_mov_b32_e32 v141, v119
	v_pk_add_f32 v[118:119], v[116:117], v[140:141]
	v_pk_add_f32 v[28:29], v[26:27], v[162:163]
	v_pk_mul_f32 v[128:129], v[30:31], v[118:119] op_sel:[1,0]
	v_mov_b32_e32 v161, v25
	v_pk_fma_f32 v[138:139], v[30:31], v[118:119], v[128:129] op_sel:[0,0,1] op_sel_hi:[1,1,0]
	v_pk_fma_f32 v[118:119], v[30:31], v[118:119], v[128:129] op_sel:[0,0,1] op_sel_hi:[0,1,0] neg_lo:[0,0,1] neg_hi:[0,0,1]
	v_mov_b32_e32 v139, v119
	v_pk_add_f32 v[118:119], v[28:29], v[138:139]
	v_pk_add_f32 v[24:25], v[20:21], v[160:161]
	v_pk_mul_f32 v[128:129], v[124:125], v[118:119] op_sel:[1,0]
	v_pk_add_f32 v[116:117], v[116:117], v[140:141] neg_lo:[0,1] neg_hi:[0,1]
	v_pk_fma_f32 v[164:165], v[124:125], v[118:119], v[128:129] op_sel:[0,0,1] op_sel_hi:[1,1,0]
	v_pk_fma_f32 v[118:119], v[124:125], v[118:119], v[128:129] op_sel:[0,0,1] op_sel_hi:[0,1,0] neg_lo:[0,0,1] neg_hi:[0,0,1]
	v_mov_b32_e32 v165, v119
	v_pk_add_f32 v[118:119], v[24:25], v[164:165]
	v_pk_add_f32 v[26:27], v[26:27], v[162:163] neg_lo:[0,1] neg_hi:[0,1]
	s_waitcnt lgkmcnt(0)
	v_pk_mul_f32 v[128:129], v[120:121], v[118:119] op_sel:[1,0]
	v_pk_add_f32 v[28:29], v[28:29], v[138:139] neg_lo:[0,1] neg_hi:[0,1]
	v_pk_fma_f32 v[166:167], v[120:121], v[118:119], v[128:129] op_sel:[0,0,1] op_sel_hi:[1,1,0]
	v_pk_fma_f32 v[118:119], v[120:121], v[118:119], v[128:129] op_sel:[0,0,1] op_sel_hi:[0,1,0] neg_lo:[0,0,1] neg_hi:[0,0,1]
	v_pk_mul_f32 v[128:129], v[30:31], v[6:7] op_sel_hi:[0,1]
	v_pk_fma_f32 v[142:143], v[30:31], v[6:7], v[128:129] op_sel:[1,0,1] op_sel_hi:[1,1,0] neg_lo:[0,0,1] neg_hi:[0,0,1]
	v_pk_fma_f32 v[6:7], v[30:31], v[6:7], v[128:129] op_sel:[1,0,1] op_sel_hi:[1,1,0]
	v_pk_mul_f32 v[128:129], v[30:31], v[14:15] op_sel_hi:[0,1]
	v_pk_fma_f32 v[144:145], v[30:31], v[14:15], v[128:129] op_sel:[1,0,1] op_sel_hi:[1,1,0] neg_lo:[0,0,1] neg_hi:[0,0,1]
	v_pk_fma_f32 v[14:15], v[30:31], v[14:15], v[128:129] op_sel:[1,0,1] op_sel_hi:[1,1,0]
	v_mov_b32_e32 v143, v7
	v_mov_b32_e32 v145, v15
	v_pk_add_f32 v[14:15], v[10:11], v[144:145]
	v_pk_add_f32 v[6:7], v[0:1], v[142:143]
	v_pk_mul_f32 v[128:129], v[126:127], v[14:15] op_sel:[1,0]
	v_pk_add_f32 v[20:21], v[20:21], v[160:161] neg_lo:[0,1] neg_hi:[0,1]
	v_pk_fma_f32 v[148:149], v[126:127], v[14:15], v[128:129] op_sel:[0,0,1] op_sel_hi:[1,1,0]
	v_pk_fma_f32 v[14:15], v[126:127], v[14:15], v[128:129] op_sel:[0,0,1] op_sel_hi:[0,1,0] neg_lo:[0,0,1] neg_hi:[0,0,1]
	v_pk_mul_f32 v[128:129], v[30:31], v[22:23] op_sel_hi:[0,1]
	v_pk_fma_f32 v[150:151], v[30:31], v[22:23], v[128:129] op_sel:[1,0,1] op_sel_hi:[1,1,0] neg_lo:[0,0,1] neg_hi:[0,0,1]
	v_pk_fma_f32 v[22:23], v[30:31], v[22:23], v[128:129] op_sel:[1,0,1] op_sel_hi:[1,1,0]
	v_pk_mul_f32 v[128:129], v[30:31], v[116:117] op_sel_hi:[0,1]
	v_pk_fma_f32 v[140:141], v[30:31], v[116:117], v[128:129] op_sel:[1,0,1] op_sel_hi:[1,1,0] neg_lo:[0,0,1] neg_hi:[0,0,1]
	v_pk_fma_f32 v[30:31], v[30:31], v[116:117], v[128:129] op_sel:[1,0,1] op_sel_hi:[1,1,0]
	v_mov_b32_e32 v151, v23
	v_mov_b32_e32 v141, v31
	v_pk_add_f32 v[30:31], v[26:27], v[140:141]
	v_pk_add_f32 v[22:23], v[18:19], v[150:151]
	v_pk_mul_f32 v[116:117], v[126:127], v[30:31] op_sel:[1,0]
	v_mov_b32_e32 v149, v15
	v_pk_fma_f32 v[128:129], v[126:127], v[30:31], v[116:117] op_sel:[0,0,1] op_sel_hi:[1,1,0]
	v_pk_fma_f32 v[30:31], v[126:127], v[30:31], v[116:117] op_sel:[0,0,1] op_sel_hi:[0,1,0] neg_lo:[0,0,1] neg_hi:[0,0,1]
	v_mov_b32_e32 v129, v31
	v_pk_add_f32 v[30:31], v[22:23], v[128:129]
	v_pk_add_f32 v[14:15], v[6:7], v[148:149]
	v_pk_mul_f32 v[116:117], v[130:131], v[30:31] op_sel:[1,0]
	v_pk_add_f32 v[10:11], v[10:11], v[144:145] neg_lo:[0,1] neg_hi:[0,1]
	v_pk_fma_f32 v[126:127], v[130:131], v[30:31], v[116:117] op_sel:[0,0,1] op_sel_hi:[1,1,0]
	v_pk_fma_f32 v[30:31], v[130:131], v[30:31], v[116:117] op_sel:[0,0,1] op_sel_hi:[0,1,0] neg_lo:[0,0,1] neg_hi:[0,0,1]
	v_mov_b32_e32 v127, v31
	v_pk_mul_f32 v[116:117], v[124:125], v[12:13] op_sel_hi:[0,1]
	v_pk_add_f32 v[30:31], v[14:15], v[126:127]
	v_pk_add_f32 v[14:15], v[14:15], v[126:127] neg_lo:[0,1] neg_hi:[0,1]
	v_pk_fma_f32 v[126:127], v[124:125], v[12:13], v[116:117] op_sel:[1,0,1] op_sel_hi:[1,1,0] neg_lo:[0,0,1] neg_hi:[0,0,1]
	v_pk_fma_f32 v[12:13], v[124:125], v[12:13], v[116:117] op_sel:[1,0,1] op_sel_hi:[1,1,0]
	v_pk_mul_f32 v[116:117], v[124:125], v[28:29] op_sel_hi:[0,1]
	v_pk_fma_f32 v[138:139], v[124:125], v[28:29], v[116:117] op_sel:[1,0,1] op_sel_hi:[1,1,0] neg_lo:[0,0,1] neg_hi:[0,0,1]
	v_pk_fma_f32 v[28:29], v[124:125], v[28:29], v[116:117] op_sel:[1,0,1] op_sel_hi:[1,1,0]
	v_mov_b32_e32 v127, v13
	v_mov_b32_e32 v139, v29
	v_pk_add_f32 v[28:29], v[20:21], v[138:139]
	v_pk_add_f32 v[12:13], v[2:3], v[126:127]
	v_pk_mul_f32 v[116:117], v[122:123], v[28:29] op_sel:[1,0]
; template <int R, class XT, class TWT>
; __device__ __forceinline__ void dit_task(XT X, TWT tw, int s, int task) {
;     const int lgM = 13 - s, lgq = lgM - R, q = 1 << lgq;
;     const int j0 = task & (q - 1), blk = task >> lgq, base = (blk << lgM) + j0;
;     const int pb = PADI(base), qp = (q >= 32) ? q + (q >> 4) : q;
;     f32x2v v[1 << R];
; #pragma unroll
;     for (int k = 0; k < (1 << R); ++k) v[k] = X[pb + k * qp];
; #pragma unroll
;     for (int r = R - 1; r >= 0; --r) {
;         const int pb = R - 1 - r;
; #pragma unroll
;         for (int k = 0; k < (1 << R); ++k) if (!((k >> pb) & 1)) {
;             const int klo = k & ((1 << pb) - 1);
;             const f32x2v w = tw[(j0 + (klo << lgq)) << (s + r)];
;             const f32x2v a = v[k], qv = v[k + (1 << pb)]; const f32x2v b = (f32x2v){qv.x * w.x + qv.y * w.y, qv.y * w.x - qv.x * w.y};
;             v[k] = a + b; v[k + (1 << pb)] = a - b;
;         }
;     }
; #pragma unroll
;     for (int k = 0; k < (1 << R); ++k) X[pb + k * qp] = v[k];
; }
	v_pk_add_f32 v[26:27], v[26:27], v[140:141] neg_lo:[0,1] neg_hi:[0,1]
	v_pk_fma_f32 v[124:125], v[122:123], v[28:29], v[116:117] op_sel:[0,0,1] op_sel_hi:[1,1,0]
	v_pk_fma_f32 v[28:29], v[122:123], v[28:29], v[116:117] op_sel:[0,0,1] op_sel_hi:[0,1,0] neg_lo:[0,0,1] neg_hi:[0,0,1]
	v_mov_b32_e32 v125, v29
	v_pk_mul_f32 v[116:117], v[136:137], v[10:11] op_sel_hi:[0,1]
	v_pk_add_f32 v[28:29], v[12:13], v[124:125]
	v_pk_add_f32 v[12:13], v[12:13], v[124:125] neg_lo:[0,1] neg_hi:[0,1]
	v_pk_fma_f32 v[124:125], v[136:137], v[10:11], v[116:117] op_sel:[1,0,1] op_sel_hi:[1,1,0] neg_lo:[0,0,1] neg_hi:[0,0,1]
	v_pk_fma_f32 v[10:11], v[136:137], v[10:11], v[116:117] op_sel:[1,0,1] op_sel_hi:[1,1,0]
	v_pk_mul_f32 v[116:117], v[136:137], v[26:27] op_sel_hi:[0,1]
	v_pk_fma_f32 v[140:141], v[136:137], v[26:27], v[116:117] op_sel:[1,0,1] op_sel_hi:[1,1,0] neg_lo:[0,0,1] neg_hi:[0,0,1]
	v_pk_fma_f32 v[26:27], v[136:137], v[26:27], v[116:117] op_sel:[1,0,1] op_sel_hi:[1,1,0]
	v_pk_add_f32 v[18:19], v[18:19], v[150:151] neg_lo:[0,1] neg_hi:[0,1]
	v_mov_b32_e32 v141, v27
	v_pk_add_f32 v[26:27], v[18:19], v[140:141]
	v_pk_add_f32 v[0:1], v[0:1], v[142:143] neg_lo:[0,1] neg_hi:[0,1]
	v_pk_mul_f32 v[116:117], v[132:133], v[26:27] op_sel:[1,0]
	v_mov_b32_e32 v125, v11
	v_pk_fma_f32 v[136:137], v[132:133], v[26:27], v[116:117] op_sel:[0,0,1] op_sel_hi:[1,1,0]
	v_pk_fma_f32 v[26:27], v[132:133], v[26:27], v[116:117] op_sel:[0,0,1] op_sel_hi:[0,1,0] neg_lo:[0,0,1] neg_hi:[0,0,1]
	v_pk_add_f32 v[24:25], v[24:25], v[164:165] neg_lo:[0,1] neg_hi:[0,1]
	v_pk_add_f32 v[10:11], v[0:1], v[124:125]
	v_mov_b32_e32 v137, v27
	v_pk_mul_f32 v[116:117], v[120:121], v[24:25] op_sel_hi:[0,1]
	v_pk_add_f32 v[22:23], v[22:23], v[128:129] neg_lo:[0,1] neg_hi:[0,1]
	v_pk_add_f32 v[26:27], v[10:11], v[136:137]
	v_pk_add_f32 v[10:11], v[10:11], v[136:137] neg_lo:[0,1] neg_hi:[0,1]
	v_pk_fma_f32 v[136:137], v[120:121], v[24:25], v[116:117] op_sel:[1,0,1] op_sel_hi:[1,1,0] neg_lo:[0,0,1] neg_hi:[0,0,1]
	v_pk_fma_f32 v[24:25], v[120:121], v[24:25], v[116:117] op_sel:[1,0,1] op_sel_hi:[1,1,0]
	v_pk_mul_f32 v[116:117], v[130:131], v[22:23] op_sel_hi:[0,1]
	v_pk_fma_f32 v[120:121], v[130:131], v[22:23], v[116:117] op_sel:[1,0,1] op_sel_hi:[1,1,0] neg_lo:[0,0,1] neg_hi:[0,0,1]
	v_pk_fma_f32 v[22:23], v[130:131], v[22:23], v[116:117] op_sel:[1,0,1] op_sel_hi:[1,1,0]
	v_pk_add_f32 v[20:21], v[20:21], v[138:139] neg_lo:[0,1] neg_hi:[0,1]
	v_pk_add_f32 v[6:7], v[6:7], v[148:149] neg_lo:[0,1] neg_hi:[0,1]
	v_mov_b32_e32 v121, v23
	v_pk_mul_f32 v[116:117], v[122:123], v[20:21] op_sel_hi:[0,1]
	v_pk_add_f32 v[22:23], v[6:7], v[120:121]
	v_pk_add_f32 v[6:7], v[6:7], v[120:121] neg_lo:[0,1] neg_hi:[0,1]
	v_pk_fma_f32 v[120:121], v[122:123], v[20:21], v[116:117] op_sel:[1,0,1] op_sel_hi:[1,1,0] neg_lo:[0,0,1] neg_hi:[0,0,1]
	v_pk_fma_f32 v[20:21], v[122:123], v[20:21], v[116:117] op_sel:[1,0,1] op_sel_hi:[1,1,0]
	v_pk_add_f32 v[18:19], v[18:19], v[140:141] neg_lo:[0,1] neg_hi:[0,1]
	v_mov_b32_e32 v155, v17
	v_pk_add_f32 v[2:3], v[2:3], v[126:127] neg_lo:[0,1] neg_hi:[0,1]
	v_mov_b32_e32 v121, v21
	v_pk_mul_f32 v[116:117], v[132:133], v[18:19] op_sel_hi:[0,1]
	v_pk_add_f32 v[16:17], v[8:9], v[154:155]
	v_mov_b32_e32 v167, v119
	v_pk_add_f32 v[20:21], v[2:3], v[120:121]
	v_pk_add_f32 v[2:3], v[2:3], v[120:121] neg_lo:[0,1] neg_hi:[0,1]
	v_pk_fma_f32 v[120:121], v[132:133], v[18:19], v[116:117] op_sel:[1,0,1] op_sel_hi:[1,1,0] neg_lo:[0,0,1] neg_hi:[0,0,1]
	v_pk_fma_f32 v[18:19], v[132:133], v[18:19], v[116:117] op_sel:[1,0,1] op_sel_hi:[1,1,0]
	v_pk_add_f32 v[118:119], v[16:17], v[166:167]
	v_pk_add_f32 v[8:9], v[8:9], v[154:155] neg_lo:[0,1] neg_hi:[0,1]
	v_mov_b32_e32 v137, v25
	v_pk_add_f32 v[0:1], v[0:1], v[124:125] neg_lo:[0,1] neg_hi:[0,1]
	v_mov_b32_e32 v121, v19
	v_pk_add_f32 v[16:17], v[16:17], v[166:167] neg_lo:[0,1] neg_hi:[0,1]
	v_pk_add_f32 v[24:25], v[8:9], v[136:137]
	v_pk_add_f32 v[8:9], v[8:9], v[136:137] neg_lo:[0,1] neg_hi:[0,1]
	v_pk_add_f32 v[18:19], v[0:1], v[120:121]
	v_pk_add_f32 v[0:1], v[0:1], v[120:121] neg_lo:[0,1] neg_hi:[0,1]
	ds_write2_b64 v81, v[118:119], v[30:31] offset1:34
	ds_write2_b64 v81, v[28:29], v[26:27] offset0:68 offset1:102
	ds_write2_b64 v81, v[24:25], v[22:23] offset0:136 offset1:170
	ds_write2_b64 v81, v[20:21], v[18:19] offset0:204 offset1:238
	ds_write2_b64 v110, v[16:17], v[14:15] offset0:16 offset1:50
	ds_write2_b64 v110, v[12:13], v[10:11] offset0:84 offset1:118
	ds_write2_b64 v110, v[8:9], v[6:7] offset0:152 offset1:186
	ds_write2_b64 v110, v[2:3], v[0:1] offset0:220 offset1:254
	s_waitcnt lgkmcnt(0)
	s_barrier
; template <int R, class XT, class TWT>
; __device__ __forceinline__ void dit_task(XT X, TWT tw, int s, int task) {
;     const int lgM = 13 - s, lgq = lgM - R, q = 1 << lgq;
;     const int j0 = task & (q - 1), blk = task >> lgq, base = (blk << lgM) + j0;
;     const int pb = PADI(base), qp = (q >= 32) ? q + (q >> 4) : q;
;     f32x2v v[1 << R];
; #pragma unroll
;     for (int k = 0; k < (1 << R); ++k) v[k] = X[pb + k * qp];
; #pragma unroll
;     for (int r = R - 1; r >= 0; --r) {
;         const int pb = R - 1 - r;
; #pragma unroll
;         for (int k = 0; k < (1 << R); ++k) if (!((k >> pb) & 1)) {
;             const int klo = k & ((1 << pb) - 1);
;             const f32x2v w = tw[(j0 + (klo << lgq)) << (s + r)];
;             const f32x2v a = v[k], qv = v[k + (1 << pb)]; const f32x2v b = (f32x2v){qv.x * w.x + qv.y * w.y, qv.y * w.x - qv.x * w.y};
;             v[k] = a + b; v[k + (1 << pb)] = a - b;
;         }
;     }
; #pragma unroll
;     for (int k = 0; k < (1 << R); ++k) X[pb + k * qp] = v[k];
; }
	ds_read_b64 v[6:7], v75
	ds_read_b64 v[8:9], v75 offset:4352
	ds_read_b64 v[10:11], v75 offset:8704
	ds_read_b64 v[12:13], v75 offset:13056
	ds_read_b64 v[14:15], v75 offset:17408
	ds_read_b64 v[16:17], v75 offset:21760
	ds_read_b64 v[18:19], v75 offset:26112
	ds_read_b64 v[20:21], v75 offset:30464
	ds_read_b64 v[22:23], v75 offset:34816
	ds_read_b64 v[24:25], v75 offset:39168
	ds_read_b64 v[26:27], v75 offset:43520
	ds_read_b64 v[28:29], v75 offset:47872
	ds_read_b64 v[30:31], v75 offset:52224
	ds_read_b64 v[110:111], v75 offset:56576
	ds_read_b64 v[116:117], v75 offset:60928
	ds_read_b64 v[118:119], v75 offset:65280
	ds_read_b64 v[120:121], v80
	ds_read_b64 v[122:123], v93
	ds_read_b64 v[124:125], v91
	ds_read_b64 v[126:127], v92
	ds_read2st64_b64 v[0:3], v76 offset1:16
	ds_read_b64 v[128:129], v79
	ds_read_b64 v[130:131], v77
	ds_read_b64 v[132:133], v78
	s_waitcnt lgkmcnt(7)
	v_xor_b32_e32 v5, 0x80000000, v120
	v_cndmask_b32_e64 v137, v5, v121, s[38:39]
	v_cndmask_b32_e64 v136, v121, v120, s[38:39]
	v_mov_b32_e32 v120, v137
	v_pk_mul_f32 v[138:139], v[8:9], v[120:121] op_sel_hi:[1,0]
	s_add_u32 s2, s26, s2
	v_pk_fma_f32 v[140:141], v[8:9], v[136:137], v[138:139] op_sel:[0,0,1] op_sel_hi:[1,1,0]
	v_pk_fma_f32 v[8:9], v[8:9], v[136:137], v[138:139] op_sel:[0,0,1] op_sel_hi:[1,0,0] neg_lo:[0,0,1] neg_hi:[0,0,1]
	v_pk_mul_f32 v[138:139], v[12:13], v[120:121] op_sel_hi:[1,0]
	v_mov_b32_e32 v141, v9
	v_pk_fma_f32 v[142:143], v[12:13], v[136:137], v[138:139] op_sel:[0,0,1] op_sel_hi:[1,1,0]
	v_pk_fma_f32 v[12:13], v[12:13], v[136:137], v[138:139] op_sel:[0,0,1] op_sel_hi:[1,0,0] neg_lo:[0,0,1] neg_hi:[0,0,1]
	v_pk_add_f32 v[8:9], v[6:7], v[140:141]
	v_mov_b32_e32 v143, v13
	v_pk_add_f32 v[12:13], v[10:11], v[142:143]
	v_pk_add_f32 v[10:11], v[10:11], v[142:143] neg_lo:[0,1] neg_hi:[0,1]
	s_waitcnt lgkmcnt(6)
	v_pk_mul_f32 v[138:139], v[122:123], v[12:13] op_sel:[1,0]
	v_pk_add_f32 v[6:7], v[6:7], v[140:141] neg_lo:[0,1] neg_hi:[0,1]
	v_pk_fma_f32 v[144:145], v[122:123], v[12:13], v[138:139] op_sel:[0,0,1] op_sel_hi:[1,1,0]
	v_pk_fma_f32 v[12:13], v[122:123], v[12:13], v[138:139] op_sel:[0,0,1] op_sel_hi:[0,1,0] neg_lo:[0,0,1] neg_hi:[0,0,1]
	v_pk_mul_f32 v[138:139], v[16:17], v[120:121] op_sel_hi:[1,0]
	v_mov_b32_e32 v145, v13
	v_pk_fma_f32 v[146:147], v[16:17], v[136:137], v[138:139] op_sel:[0,0,1] op_sel_hi:[1,1,0]
	v_pk_fma_f32 v[16:17], v[16:17], v[136:137], v[138:139] op_sel:[0,0,1] op_sel_hi:[1,0,0] neg_lo:[0,0,1] neg_hi:[0,0,1]
	v_pk_mul_f32 v[138:139], v[20:21], v[120:121] op_sel_hi:[1,0]
	v_mov_b32_e32 v147, v17
	v_pk_fma_f32 v[148:149], v[20:21], v[136:137], v[138:139] op_sel:[0,0,1] op_sel_hi:[1,1,0]
	v_pk_fma_f32 v[20:21], v[20:21], v[136:137], v[138:139] op_sel:[0,0,1] op_sel_hi:[1,0,0] neg_lo:[0,0,1] neg_hi:[0,0,1]
	v_pk_add_f32 v[16:17], v[14:15], v[146:147]
	v_mov_b32_e32 v149, v21
	v_pk_add_f32 v[20:21], v[18:19], v[148:149]
	v_pk_add_f32 v[18:19], v[18:19], v[148:149] neg_lo:[0,1] neg_hi:[0,1]
	v_pk_mul_f32 v[138:139], v[122:123], v[20:21] op_sel:[1,0]
	v_pk_add_f32 v[14:15], v[14:15], v[146:147] neg_lo:[0,1] neg_hi:[0,1]
	v_pk_fma_f32 v[150:151], v[122:123], v[20:21], v[138:139] op_sel:[0,0,1] op_sel_hi:[1,1,0]
	v_pk_fma_f32 v[20:21], v[122:123], v[20:21], v[138:139] op_sel:[0,0,1] op_sel_hi:[0,1,0] neg_lo:[0,0,1] neg_hi:[0,0,1]
	v_mov_b32_e32 v151, v21
	v_pk_add_f32 v[20:21], v[16:17], v[150:151]
	v_pk_add_f32 v[16:17], v[16:17], v[150:151] neg_lo:[0,1] neg_hi:[0,1]
	s_waitcnt lgkmcnt(5)
	v_pk_mul_f32 v[138:139], v[124:125], v[20:21] op_sel:[1,0]
	v_pk_add_f32 v[12:13], v[8:9], v[144:145]
	v_pk_fma_f32 v[152:153], v[124:125], v[20:21], v[138:139] op_sel:[0,0,1] op_sel_hi:[1,1,0]
	v_pk_fma_f32 v[20:21], v[124:125], v[20:21], v[138:139] op_sel:[0,0,1] op_sel_hi:[0,1,0] neg_lo:[0,0,1] neg_hi:[0,0,1]
	v_pk_mul_f32 v[138:139], v[24:25], v[120:121] op_sel_hi:[1,0]
	v_pk_add_f32 v[8:9], v[8:9], v[144:145] neg_lo:[0,1] neg_hi:[0,1]
	v_pk_fma_f32 v[154:155], v[24:25], v[136:137], v[138:139] op_sel:[0,0,1] op_sel_hi:[1,1,0]
	v_pk_fma_f32 v[24:25], v[24:25], v[136:137], v[138:139] op_sel:[0,0,1] op_sel_hi:[1,0,0] neg_lo:[0,0,1] neg_hi:[0,0,1]
	v_pk_mul_f32 v[138:139], v[28:29], v[120:121] op_sel_hi:[1,0]
	v_mov_b32_e32 v155, v25
	v_pk_fma_f32 v[156:157], v[28:29], v[136:137], v[138:139] op_sel:[0,0,1] op_sel_hi:[1,1,0]
	v_pk_fma_f32 v[28:29], v[28:29], v[136:137], v[138:139] op_sel:[0,0,1] op_sel_hi:[1,0,0] neg_lo:[0,0,1] neg_hi:[0,0,1]
	v_pk_add_f32 v[24:25], v[22:23], v[154:155]
	v_mov_b32_e32 v157, v29
	v_pk_add_f32 v[28:29], v[26:27], v[156:157]
	v_pk_add_f32 v[26:27], v[26:27], v[156:157] neg_lo:[0,1] neg_hi:[0,1]
	v_pk_mul_f32 v[138:139], v[122:123], v[28:29] op_sel:[1,0]
	v_pk_add_f32 v[22:23], v[22:23], v[154:155] neg_lo:[0,1] neg_hi:[0,1]
	v_pk_fma_f32 v[158:159], v[122:123], v[28:29], v[138:139] op_sel:[0,0,1] op_sel_hi:[1,1,0]
	v_pk_fma_f32 v[28:29], v[122:123], v[28:29], v[138:139] op_sel:[0,0,1] op_sel_hi:[0,1,0] neg_lo:[0,0,1] neg_hi:[0,0,1]
	v_pk_mul_f32 v[138:139], v[110:111], v[120:121] op_sel_hi:[1,0]
	v_pk_mul_f32 v[120:121], v[118:119], v[120:121] op_sel_hi:[1,0]
	v_pk_fma_f32 v[160:161], v[110:111], v[136:137], v[138:139] op_sel:[0,0,1] op_sel_hi:[1,1,0]
	v_pk_fma_f32 v[110:111], v[110:111], v[136:137], v[138:139] op_sel:[0,0,1] op_sel_hi:[1,0,0] neg_lo:[0,0,1] neg_hi:[0,0,1]
	v_pk_fma_f32 v[138:139], v[118:119], v[136:137], v[120:121] op_sel:[0,0,1] op_sel_hi:[1,1,0]
	v_pk_fma_f32 v[118:119], v[118:119], v[136:137], v[120:121] op_sel:[0,0,1] op_sel_hi:[1,0,0] neg_lo:[0,0,1] neg_hi:[0,0,1]
	v_mov_b32_e32 v161, v111
	v_mov_b32_e32 v139, v119
	v_pk_add_f32 v[118:119], v[116:117], v[138:139]
	v_pk_add_f32 v[110:111], v[30:31], v[160:161]
	v_pk_mul_f32 v[120:121], v[122:123], v[118:119] op_sel:[1,0]
	v_mov_b32_e32 v159, v29
	v_pk_fma_f32 v[136:137], v[122:123], v[118:119], v[120:121] op_sel:[0,0,1] op_sel_hi:[1,1,0]
	v_pk_fma_f32 v[118:119], v[122:123], v[118:119], v[120:121] op_sel:[0,0,1] op_sel_hi:[0,1,0] neg_lo:[0,0,1] neg_hi:[0,0,1]
	v_mov_b32_e32 v137, v119
	v_pk_add_f32 v[118:119], v[110:111], v[136:137]
	v_pk_add_f32 v[28:29], v[24:25], v[158:159]
	v_pk_mul_f32 v[120:121], v[124:125], v[118:119] op_sel:[1,0]
	v_pk_add_f32 v[116:117], v[116:117], v[138:139] neg_lo:[0,1] neg_hi:[0,1]
	v_pk_fma_f32 v[162:163], v[124:125], v[118:119], v[120:121] op_sel:[0,0,1] op_sel_hi:[1,1,0]
	v_pk_fma_f32 v[118:119], v[124:125], v[118:119], v[120:121] op_sel:[0,0,1] op_sel_hi:[0,1,0] neg_lo:[0,0,1] neg_hi:[0,0,1]
	v_mov_b32_e32 v163, v119
	v_pk_add_f32 v[118:119], v[28:29], v[162:163]
	v_pk_add_f32 v[30:31], v[30:31], v[160:161] neg_lo:[0,1] neg_hi:[0,1]
	s_waitcnt lgkmcnt(3)
; template <int R, class XT, class TWT>
; __device__ __forceinline__ void dit_task(XT X, TWT tw, int s, int task) {
;     const int lgM = 13 - s, lgq = lgM - R, q = 1 << lgq;
;     const int j0 = task & (q - 1), blk = task >> lgq, base = (blk << lgM) + j0;
;     const int pb = PADI(base), qp = (q >= 32) ? q + (q >> 4) : q;
;     f32x2v v[1 << R];
; #pragma unroll
;     for (int k = 0; k < (1 << R); ++k) v[k] = X[pb + k * qp];
; #pragma unroll
;     for (int r = R - 1; r >= 0; --r) {
;         const int pb = R - 1 - r;
; #pragma unroll
;         for (int k = 0; k < (1 << R); ++k) if (!((k >> pb) & 1)) {
;             const int klo = k & ((1 << pb) - 1);
;             const f32x2v w = tw[(j0 + (klo << lgq)) << (s + r)];
;             const f32x2v a = v[k], qv = v[k + (1 << pb)]; const f32x2v b = (f32x2v){qv.x * w.x + qv.y * w.y, qv.y * w.x - qv.x * w.y};
;             v[k] = a + b; v[k + (1 << pb)] = a - b;
;         }
;     }
; #pragma unroll
;     for (int k = 0; k < (1 << R); ++k) X[pb + k * qp] = v[k];
; }
	v_pk_mul_f32 v[120:121], v[0:1], v[118:119] op_sel:[1,0]
	v_pk_add_f32 v[110:111], v[110:111], v[136:137] neg_lo:[0,1] neg_hi:[0,1]
	v_pk_fma_f32 v[164:165], v[0:1], v[118:119], v[120:121] op_sel:[0,0,1] op_sel_hi:[1,1,0]
	v_pk_fma_f32 v[118:119], v[0:1], v[118:119], v[120:121] op_sel:[0,0,1] op_sel_hi:[0,1,0] neg_lo:[0,0,1] neg_hi:[0,0,1]
	v_pk_mul_f32 v[120:121], v[122:123], v[10:11] op_sel_hi:[0,1]
	v_pk_fma_f32 v[140:141], v[122:123], v[10:11], v[120:121] op_sel:[1,0,1] op_sel_hi:[1,1,0] neg_lo:[0,0,1] neg_hi:[0,0,1]
	v_pk_fma_f32 v[10:11], v[122:123], v[10:11], v[120:121] op_sel:[1,0,1] op_sel_hi:[1,1,0]
	v_pk_mul_f32 v[120:121], v[122:123], v[18:19] op_sel_hi:[0,1]
	v_pk_fma_f32 v[142:143], v[122:123], v[18:19], v[120:121] op_sel:[1,0,1] op_sel_hi:[1,1,0] neg_lo:[0,0,1] neg_hi:[0,0,1]
	v_pk_fma_f32 v[18:19], v[122:123], v[18:19], v[120:121] op_sel:[1,0,1] op_sel_hi:[1,1,0]
	v_mov_b32_e32 v141, v11
	v_mov_b32_e32 v143, v19
	v_pk_add_f32 v[18:19], v[14:15], v[142:143]
	v_pk_add_f32 v[10:11], v[6:7], v[140:141]
	v_pk_mul_f32 v[120:121], v[126:127], v[18:19] op_sel:[1,0]
	v_pk_add_f32 v[24:25], v[24:25], v[158:159] neg_lo:[0,1] neg_hi:[0,1]
	v_pk_fma_f32 v[146:147], v[126:127], v[18:19], v[120:121] op_sel:[0,0,1] op_sel_hi:[1,1,0]
	v_pk_fma_f32 v[18:19], v[126:127], v[18:19], v[120:121] op_sel:[0,0,1] op_sel_hi:[0,1,0] neg_lo:[0,0,1] neg_hi:[0,0,1]
	v_pk_mul_f32 v[120:121], v[122:123], v[26:27] op_sel_hi:[0,1]
	v_pk_fma_f32 v[148:149], v[122:123], v[26:27], v[120:121] op_sel:[1,0,1] op_sel_hi:[1,1,0] neg_lo:[0,0,1] neg_hi:[0,0,1]
	v_pk_fma_f32 v[26:27], v[122:123], v[26:27], v[120:121] op_sel:[1,0,1] op_sel_hi:[1,1,0]
	v_pk_mul_f32 v[120:121], v[122:123], v[116:117] op_sel_hi:[0,1]
	v_pk_fma_f32 v[138:139], v[122:123], v[116:117], v[120:121] op_sel:[1,0,1] op_sel_hi:[1,1,0] neg_lo:[0,0,1] neg_hi:[0,0,1]
	v_pk_fma_f32 v[116:117], v[122:123], v[116:117], v[120:121] op_sel:[1,0,1] op_sel_hi:[1,1,0]
	v_mov_b32_e32 v149, v27
	v_mov_b32_e32 v139, v117
	v_pk_add_f32 v[116:117], v[30:31], v[138:139]
	v_pk_add_f32 v[26:27], v[22:23], v[148:149]
	v_pk_mul_f32 v[120:121], v[126:127], v[116:117] op_sel:[1,0]
	v_mov_b32_e32 v147, v19
	v_pk_fma_f32 v[122:123], v[126:127], v[116:117], v[120:121] op_sel:[0,0,1] op_sel_hi:[1,1,0]
	v_pk_fma_f32 v[116:117], v[126:127], v[116:117], v[120:121] op_sel:[0,0,1] op_sel_hi:[0,1,0] neg_lo:[0,0,1] neg_hi:[0,0,1]
	v_mov_b32_e32 v123, v117
	v_pk_add_f32 v[116:117], v[26:27], v[122:123]
	v_pk_add_f32 v[18:19], v[10:11], v[146:147]
	s_waitcnt lgkmcnt(1)
	v_pk_mul_f32 v[120:121], v[130:131], v[116:117] op_sel:[1,0]
	v_pk_add_f32 v[14:15], v[14:15], v[142:143] neg_lo:[0,1] neg_hi:[0,1]
	v_pk_fma_f32 v[126:127], v[130:131], v[116:117], v[120:121] op_sel:[0,0,1] op_sel_hi:[1,1,0]
	v_pk_fma_f32 v[116:117], v[130:131], v[116:117], v[120:121] op_sel:[0,0,1] op_sel_hi:[0,1,0] neg_lo:[0,0,1] neg_hi:[0,0,1]
	v_mov_b32_e32 v127, v117
	v_pk_mul_f32 v[120:121], v[124:125], v[16:17] op_sel_hi:[0,1]
	v_pk_add_f32 v[116:117], v[18:19], v[126:127]
	v_pk_add_f32 v[18:19], v[18:19], v[126:127] neg_lo:[0,1] neg_hi:[0,1]
	v_pk_fma_f32 v[126:127], v[124:125], v[16:17], v[120:121] op_sel:[1,0,1] op_sel_hi:[1,1,0] neg_lo:[0,0,1] neg_hi:[0,0,1]
	v_pk_fma_f32 v[16:17], v[124:125], v[16:17], v[120:121] op_sel:[1,0,1] op_sel_hi:[1,1,0]
	v_pk_mul_f32 v[120:121], v[124:125], v[110:111] op_sel_hi:[0,1]
	v_pk_fma_f32 v[136:137], v[124:125], v[110:111], v[120:121] op_sel:[1,0,1] op_sel_hi:[1,1,0] neg_lo:[0,0,1] neg_hi:[0,0,1]
	v_pk_fma_f32 v[110:111], v[124:125], v[110:111], v[120:121] op_sel:[1,0,1] op_sel_hi:[1,1,0]
	v_mov_b32_e32 v127, v17
	v_mov_b32_e32 v137, v111
	v_pk_add_f32 v[110:111], v[24:25], v[136:137]
	v_pk_add_f32 v[16:17], v[8:9], v[126:127]
	v_pk_mul_f32 v[120:121], v[2:3], v[110:111] op_sel:[1,0]
	v_pk_add_f32 v[30:31], v[30:31], v[138:139] neg_lo:[0,1] neg_hi:[0,1]
	v_pk_fma_f32 v[124:125], v[2:3], v[110:111], v[120:121] op_sel:[0,0,1] op_sel_hi:[1,1,0]
	v_pk_fma_f32 v[110:111], v[2:3], v[110:111], v[120:121] op_sel:[0,0,1] op_sel_hi:[0,1,0] neg_lo:[0,0,1] neg_hi:[0,0,1]
	v_mov_b32_e32 v125, v111
	v_pk_mul_f32 v[120:121], v[128:129], v[14:15] op_sel_hi:[0,1]
	v_pk_add_f32 v[110:111], v[16:17], v[124:125]
	v_pk_add_f32 v[16:17], v[16:17], v[124:125] neg_lo:[0,1] neg_hi:[0,1]
	v_pk_fma_f32 v[124:125], v[128:129], v[14:15], v[120:121] op_sel:[1,0,1] op_sel_hi:[1,1,0] neg_lo:[0,0,1] neg_hi:[0,0,1]
	v_pk_fma_f32 v[14:15], v[128:129], v[14:15], v[120:121] op_sel:[1,0,1] op_sel_hi:[1,1,0]
	v_pk_mul_f32 v[120:121], v[128:129], v[30:31] op_sel_hi:[0,1]
	v_pk_fma_f32 v[138:139], v[128:129], v[30:31], v[120:121] op_sel:[1,0,1] op_sel_hi:[1,1,0] neg_lo:[0,0,1] neg_hi:[0,0,1]
	v_pk_fma_f32 v[30:31], v[128:129], v[30:31], v[120:121] op_sel:[1,0,1] op_sel_hi:[1,1,0]
	v_pk_add_f32 v[22:23], v[22:23], v[148:149] neg_lo:[0,1] neg_hi:[0,1]
	v_mov_b32_e32 v139, v31
	v_pk_add_f32 v[30:31], v[22:23], v[138:139]
	v_pk_add_f32 v[6:7], v[6:7], v[140:141] neg_lo:[0,1] neg_hi:[0,1]
	s_waitcnt lgkmcnt(0)
; #define LAS __attribute__((address_space(3)))
; template <int R, class XT, class TWT>
; __device__ __forceinline__ void dit_task(XT X, TWT tw, int s, int task) {
;     ...
;     for (int k = 0; k < (1 << R); ++k) X[pb + k * qp] = v[k];
; template <bool LAT>
; __device__ __forceinline__ void hyconv_unit(const Frame& F, LAS f32x2v* X, const TwHalf tw, LAS bf16* OUT, const float* skip, bf16* MIX, int u) {
;     ...
;                 unsigned ga[4], gb[4], za[4], zb[4];
; #pragma unroll
;                 for (int r = 0; r < 4; ++r) { const int pr = F.tid + 512 * r; ga[r] = *(const unsigned*)(g0 + 2 * pr); gb[r] = *(const unsigned*)(g1 + 2 * pr); za[r] = *(const unsigned*)(v0 + 2 * pr); zb[r] = *(const unsigned*)(v1 + 2 * pr); }
; #pragma unroll
;                 for (int r = 0; r < 8; ++r) { const int e = 2 * (F.tid + 512 * r); f32x4 zz = (f32x4){0.f, 0.f, 0.f, 0.f};
;                     if (r < 4) { const f32x4 xx = *(const LAS f32x4*)(X + PADI(e));
;                         zz.x = bflo(ga[r]) * (xx.x + bflo(za[r]) * sk); zz.y = bflo(gb[r]) * (xx.y + bflo(zb[r]) * sk); zz.z = bfhi(ga[r]) * (xx.z + bfhi(za[r]) * sk); zz.w = bfhi(gb[r]) * (xx.w + bfhi(zb[r]) * sk);
	v_pk_mul_f32 v[120:121], v[132:133], v[30:31] op_sel:[1,0]
	v_mov_b32_e32 v125, v15
	v_pk_fma_f32 v[128:129], v[132:133], v[30:31], v[120:121] op_sel:[0,0,1] op_sel_hi:[1,1,0]
	v_pk_fma_f32 v[30:31], v[132:133], v[30:31], v[120:121] op_sel:[0,0,1] op_sel_hi:[0,1,0] neg_lo:[0,0,1] neg_hi:[0,0,1]
	v_pk_add_f32 v[28:29], v[28:29], v[162:163] neg_lo:[0,1] neg_hi:[0,1]
	v_pk_add_f32 v[14:15], v[6:7], v[124:125]
	v_mov_b32_e32 v129, v31
	v_pk_mul_f32 v[120:121], v[0:1], v[28:29] op_sel_hi:[0,1]
	v_pk_add_f32 v[26:27], v[26:27], v[122:123] neg_lo:[0,1] neg_hi:[0,1]
	v_pk_add_f32 v[30:31], v[14:15], v[128:129]
	v_pk_add_f32 v[14:15], v[14:15], v[128:129] neg_lo:[0,1] neg_hi:[0,1]
	v_pk_fma_f32 v[128:129], v[0:1], v[28:29], v[120:121] op_sel:[1,0,1] op_sel_hi:[1,1,0] neg_lo:[0,0,1] neg_hi:[0,0,1]
	v_pk_fma_f32 v[0:1], v[0:1], v[28:29], v[120:121] op_sel:[1,0,1] op_sel_hi:[1,1,0]
	v_pk_mul_f32 v[28:29], v[130:131], v[26:27] op_sel_hi:[0,1]
	v_pk_fma_f32 v[120:121], v[130:131], v[26:27], v[28:29] op_sel:[1,0,1] op_sel_hi:[1,1,0] neg_lo:[0,0,1] neg_hi:[0,0,1]
	v_pk_fma_f32 v[26:27], v[130:131], v[26:27], v[28:29] op_sel:[1,0,1] op_sel_hi:[1,1,0]
	v_pk_add_f32 v[24:25], v[24:25], v[136:137] neg_lo:[0,1] neg_hi:[0,1]
	v_pk_add_f32 v[10:11], v[10:11], v[146:147] neg_lo:[0,1] neg_hi:[0,1]
	v_mov_b32_e32 v121, v27
	v_pk_mul_f32 v[28:29], v[2:3], v[24:25] op_sel_hi:[0,1]
	v_pk_add_f32 v[22:23], v[22:23], v[138:139] neg_lo:[0,1] neg_hi:[0,1]
	v_mov_b32_e32 v153, v21
	v_pk_add_f32 v[26:27], v[10:11], v[120:121]
	v_pk_add_f32 v[10:11], v[10:11], v[120:121] neg_lo:[0,1] neg_hi:[0,1]
	v_pk_fma_f32 v[120:121], v[2:3], v[24:25], v[28:29] op_sel:[1,0,1] op_sel_hi:[1,1,0] neg_lo:[0,0,1] neg_hi:[0,0,1]
	v_pk_fma_f32 v[2:3], v[2:3], v[24:25], v[28:29] op_sel:[1,0,1] op_sel_hi:[1,1,0]
	v_pk_mul_f32 v[24:25], v[132:133], v[22:23] op_sel_hi:[0,1]
	v_pk_add_f32 v[20:21], v[12:13], v[152:153]
	v_mov_b32_e32 v165, v119
	v_pk_fma_f32 v[28:29], v[132:133], v[22:23], v[24:25] op_sel:[1,0,1] op_sel_hi:[1,1,0] neg_lo:[0,0,1] neg_hi:[0,0,1]
	v_pk_fma_f32 v[22:23], v[132:133], v[22:23], v[24:25] op_sel:[1,0,1] op_sel_hi:[1,1,0]
	v_pk_add_f32 v[118:119], v[20:21], v[164:165]
	v_pk_add_f32 v[12:13], v[12:13], v[152:153] neg_lo:[0,1] neg_hi:[0,1]
	v_mov_b32_e32 v129, v1
	v_pk_add_f32 v[8:9], v[8:9], v[126:127] neg_lo:[0,1] neg_hi:[0,1]
	v_mov_b32_e32 v121, v3
	v_pk_add_f32 v[6:7], v[6:7], v[124:125] neg_lo:[0,1] neg_hi:[0,1]
	v_mov_b32_e32 v29, v23
	s_addc_u32 s3, s27, s3
	v_pk_add_f32 v[20:21], v[20:21], v[164:165] neg_lo:[0,1] neg_hi:[0,1]
	v_pk_add_f32 v[0:1], v[12:13], v[128:129]
	v_pk_add_f32 v[12:13], v[12:13], v[128:129] neg_lo:[0,1] neg_hi:[0,1]
	v_pk_add_f32 v[2:3], v[8:9], v[120:121]
	v_pk_add_f32 v[8:9], v[8:9], v[120:121] neg_lo:[0,1] neg_hi:[0,1]
	v_pk_add_f32 v[22:23], v[6:7], v[28:29]
	v_pk_add_f32 v[6:7], v[6:7], v[28:29] neg_lo:[0,1] neg_hi:[0,1]
	ds_write_b64 v75, v[118:119]
	ds_write_b64 v75, v[116:117] offset:4352
	ds_write_b64 v75, v[110:111] offset:8704
	ds_write_b64 v75, v[30:31] offset:13056
	ds_write_b64 v75, v[0:1] offset:17408
	ds_write_b64 v75, v[26:27] offset:21760
	ds_write_b64 v75, v[2:3] offset:26112
	ds_write_b64 v75, v[22:23] offset:30464
	ds_write_b64 v75, v[20:21] offset:34816
	ds_write_b64 v75, v[18:19] offset:39168
	ds_write_b64 v75, v[16:17] offset:43520
	ds_write_b64 v75, v[14:15] offset:47872
	ds_write_b64 v75, v[12:13] offset:52224
	ds_write_b64 v75, v[10:11] offset:56576
	ds_write_b64 v75, v[8:9] offset:60928
	ds_write_b64 v75, v[6:7] offset:65280
	s_waitcnt lgkmcnt(0)
	s_barrier
	s_waitcnt vmcnt(0)
	v_mov_b32_e32 v5, v182
	v_mov_b32_e32 v21, v183
	v_mov_b32_e32 v23, v184
	v_mov_b32_e32 v25, v185
	v_mov_b32_e32 v13, v186
	v_mov_b32_e32 v12, v187
	v_mov_b32_e32 v9, v188
	v_mov_b32_e32 v8, v189
	v_mov_b32_e32 v16, v190
	v_mov_b32_e32 v18, v191
	v_mov_b32_e32 v15, v192
	v_mov_b32_e32 v14, v193
	v_mov_b32_e32 v11, v194
	v_mov_b32_e32 v10, v195
	v_mov_b32_e32 v17, v196
	v_mov_b32_e32 v19, v197
	ds_read_b128 v[0:3], v33
	s_and_b64 vcc, exec, s[20:21]
	s_mov_b64 s[0:1], -1
	s_waitcnt lgkmcnt(0)
	v_mov_b32_e32 v26, v0
	v_mov_b32_e32 v27, v2
	v_mov_b32_e32 v2, v1
	s_waitcnt vmcnt(15)
	v_lshlrev_b32_e32 v6, 16, v5
	s_waitcnt vmcnt(14)
	v_lshlrev_b32_e32 v20, 16, v21
	v_and_b32_e32 v21, 0xffff0000, v21
	s_waitcnt vmcnt(12)
	v_lshlrev_b32_e32 v24, 16, v25
	v_and_b32_e32 v25, 0xffff0000, v25
	v_lshlrev_b32_e32 v22, 16, v23
	v_and_b32_e32 v7, 0xffff0000, v5
	v_pk_fma_f32 v[20:21], v[4:5], v[20:21], v[26:27] op_sel_hi:[0,1,1]
	v_and_b32_e32 v23, 0xffff0000, v23
	v_pk_fma_f32 v[0:1], v[4:5], v[24:25], v[2:3] op_sel_hi:[0,1,1]
	v_pk_mul_f32 v[6:7], v[20:21], v[6:7]
	v_pk_mul_f32 v[2:3], v[0:1], v[22:23]
	s_cbranch_vccnz .LBB0_795
	s_andn2_b64 vcc, exec, s[0:1]
	s_cbranch_vccz .LBB0_796
